# GEMM tile epilogue de-serialisation (out-proj + three in-proj 128x256 instances): the 12 scale loads per tile are issued before the K loop into free registers, no memory waits inside the epilogue
# speedup vs baseline: 1.0096x; 1.0096x over previous
; __device__ __forceinline__ int opaque_tid() { int t = threadIdx.x; asm volatile("" : "+v"(t)); return t; }
; template <bool I8>
; __device__ __forceinline__ void gemm_mainloop_n256(const bf16_t* __restrict__ A, int lda, const bf16_t* __restrict__ Bt, int ldb,
;                                                    int K, int m0, int n0, f32x4 (&acc)[4][8], char* smem) {
;   const int tid = opaque_tid(), lane = tid & 63, w = tid >> 6;
;   const int wm = w >> 1, wn = w & 1;
; #pragma unroll
;   for (int i = 0; i < 4; ++i)
; #pragma unroll
;     for (int j = 0; j < 8; ++j) acc[i][j] = f32x4{0.f, 0.f, 0.f, 0.f};
;   const int nk = K / 64;
;   const int rowoff = lane >> 3, lch = (lane & 7) ^ rowoff;
;   const bf16_t* gA = A + (size_t)(m0 + w * 8 + rowoff) * lda + lch * 8;
;   const bf16_t* gB = Bt + (size_t)(n0 + w * 8 + rowoff) * ldb + lch * 8;
;   const int fr = lane & 15, fq = lane >> 4;
; template <bool I8, class Epi> ...
;   const int lane = threadIdx.x & 63, w = threadIdx.x >> 6;
;   const int wm = w >> 1, wn = w & 1;
;   f32x4 acc[4][8];
;   gemm_mainloop_n256<I8>(A, lda, Bt, ldb, K, m0, n0, acc, smem);
; #pragma unroll
;   for (int i = 0; i < 4; ++i) {
;     const int row = m0 + wm * 64 + i * 16 + (lane >> 4) * 4;
;     float4 rs = float4{1.f, 1.f, 1.f, 1.f};
;     if (I8) rs = *reinterpret_cast<const float4*>(rscale + row);
.LBB0_556:
	s_andn2_b64 vcc, exec, s[6:7]
	s_cbranch_vccnz .LBB0_233
	s_lshl_b32 s6, s47, 7
	s_lshl_b32 s10, s46, 10
	s_and_b32 s11, s6, 0x380
	s_ashr_i32 s8, s47, 3
	s_or_b32 s9, s11, s10
	s_cmp_gt_i32 s8, 7
	s_mov_b64 s[6:7], -1
	s_cbranch_scc0 .LBB0_567
	s_lshl_b32 s12, s8, 8
	s_cmp_gt_u32 s8, 11
	s_cbranch_scc0 .LBB0_562
	v_mov_b32_e32 v2, v0
	s_add_i32 s6, s11, s10
	v_bfe_u32 v4, v2, 3, 3
	v_bfe_u32 v9, v2, 4, 2
	v_ashrrev_i32_e32 v3, 6, v2
	v_and_b32_e32 v5, 7, v2
	v_bitop3_b32 v6, v4, v2, 7 bitop3:0x78
	v_and_b32_e32 v8, 15, v2
	v_lshrrev_b32_e32 v10, 1, v2
	v_bitop3_b32 v2, v9, v2, 7 bitop3:0x78
	v_lshlrev_b32_e32 v7, 3, v3
	v_lshlrev_b32_e32 v136, 10, v3
	v_lshlrev_b32_e32 v3, 7, v3
	v_lshlrev_b32_e32 v138, 4, v2
	v_bitop3_b32 v2, v9, v5, 4 bitop3:0x36
	v_and_or_b32 v3, v3, s82, v8
	v_lshlrev_b32_e32 v141, 4, v2
	v_add3_u32 v2, v4, s12, v7
	v_lshlrev_b32_e32 v140, 7, v3
	v_ashrrev_i32_e32 v3, 31, v2
	v_lshlrev_b64 v[2:3], 11, v[2:3]
	v_lshlrev_b32_e32 v5, 4, v6
	v_or_b32_e32 v2, v2, v5
	v_lshl_add_u64 v[130:131], s[22:23], 0, v[2:3]
	v_add3_u32 v2, s6, v4, v7
	v_ashrrev_i32_e32 v3, 31, v2
	v_lshlrev_b64 v[2:3], 11, v[2:3]
	v_and_or_b32 v10, v10, s84, v8
	v_or_b32_e32 v2, v2, v5
	v_mov_b32_e32 v14, 0
	v_lshlrev_b32_e32 v139, 7, v10
	v_lshl_add_u64 v[132:133], s[20:21], 0, v[2:3]
	s_mov_b64 s[6:7], 0
	v_mov_b32_e32 v15, v14
	v_mov_b32_e32 v16, v14
	v_mov_b32_e32 v17, v14
	v_mov_b32_e32 v2, v14
	v_mov_b32_e32 v3, v14
	v_mov_b32_e32 v4, v14
	v_mov_b32_e32 v5, v14
	v_mov_b32_e32 v6, v14
	v_mov_b32_e32 v7, v14
	v_mov_b32_e32 v8, v14
	v_mov_b32_e32 v9, v14
	v_mov_b32_e32 v10, v14
	v_mov_b32_e32 v11, v14
	v_mov_b32_e32 v12, v14
	v_mov_b32_e32 v13, v14
	v_mov_b32_e32 v18, v14
	v_mov_b32_e32 v19, v14
	v_mov_b32_e32 v20, v14
	v_mov_b32_e32 v21, v14
	v_mov_b32_e32 v22, v14
	v_mov_b32_e32 v23, v14
	v_mov_b32_e32 v24, v14
	v_mov_b32_e32 v25, v14
	v_mov_b32_e32 v26, v14
	v_mov_b32_e32 v27, v14
	v_mov_b32_e32 v28, v14
	v_mov_b32_e32 v29, v14
	v_mov_b32_e32 v30, v14
	v_mov_b32_e32 v31, v14
	v_mov_b32_e32 v32, v14
	v_mov_b32_e32 v33, v14
	v_mov_b32_e32 v34, v14
	v_mov_b32_e32 v35, v14
	v_mov_b32_e32 v36, v14
	v_mov_b32_e32 v37, v14
	v_mov_b32_e32 v38, v14
	v_mov_b32_e32 v39, v14
	v_mov_b32_e32 v40, v14
	v_mov_b32_e32 v41, v14
	v_mov_b32_e32 v42, v14
	v_mov_b32_e32 v43, v14
	v_mov_b32_e32 v44, v14
	v_mov_b32_e32 v45, v14
	v_mov_b32_e32 v46, v14
	v_mov_b32_e32 v47, v14
	v_mov_b32_e32 v48, v14
	v_mov_b32_e32 v49, v14
	v_mov_b32_e32 v50, v14
	v_mov_b32_e32 v51, v14
	v_mov_b32_e32 v52, v14
	v_mov_b32_e32 v53, v14
	v_mov_b32_e32 v54, v14
	v_mov_b32_e32 v55, v14
	v_mov_b32_e32 v56, v14
	v_mov_b32_e32 v57, v14
	v_mov_b32_e32 v58, v14
	v_mov_b32_e32 v59, v14
	v_mov_b32_e32 v60, v14
	v_mov_b32_e32 v61, v14
	v_mov_b32_e32 v62, v14
	v_mov_b32_e32 v63, v14
	v_mov_b32_e32 v64, v14
	v_mov_b32_e32 v65, v14
	v_mov_b32_e32 v66, v14
	v_mov_b32_e32 v67, v14
	v_mov_b32_e32 v68, v14
	v_mov_b32_e32 v69, v14
	v_mov_b32_e32 v70, v14
	v_mov_b32_e32 v71, v14
	v_mov_b32_e32 v72, v14
	v_mov_b32_e32 v73, v14
	v_mov_b32_e32 v74, v14
	v_mov_b32_e32 v75, v14
	v_mov_b32_e32 v76, v14
	v_mov_b32_e32 v77, v14
	v_mov_b32_e32 v78, v14
	v_mov_b32_e32 v79, v14
	v_mov_b32_e32 v80, v14
	v_mov_b32_e32 v81, v14
	v_mov_b32_e32 v82, v14
	v_mov_b32_e32 v83, v14
	v_mov_b32_e32 v84, v14
	v_mov_b32_e32 v85, v14
	v_mov_b32_e32 v86, v14
	v_mov_b32_e32 v87, v14
	v_mov_b32_e32 v88, v14
	v_mov_b32_e32 v89, v14
	v_mov_b32_e32 v90, v14
	v_mov_b32_e32 v91, v14
	v_mov_b32_e32 v92, v14
	v_mov_b32_e32 v93, v14
	v_mov_b32_e32 v94, v14
	v_mov_b32_e32 v95, v14
	v_mov_b32_e32 v96, v14
	v_mov_b32_e32 v97, v14
	v_mov_b32_e32 v98, v14
	v_mov_b32_e32 v99, v14
	v_mov_b32_e32 v100, v14
	v_mov_b32_e32 v101, v14
	v_mov_b32_e32 v102, v14
	v_mov_b32_e32 v103, v14
	v_mov_b32_e32 v104, v14
	v_mov_b32_e32 v105, v14
	v_mov_b32_e32 v106, v14
	v_mov_b32_e32 v107, v14
	v_mov_b32_e32 v108, v14
	v_mov_b32_e32 v109, v14
	v_mov_b32_e32 v110, v14
	v_mov_b32_e32 v111, v14
	v_mov_b32_e32 v112, v14
	v_mov_b32_e32 v113, v14
	v_mov_b32_e32 v114, v14
	v_mov_b32_e32 v115, v14
	v_mov_b32_e32 v116, v14
	v_mov_b32_e32 v117, v14
	v_mov_b32_e32 v118, v14
	v_mov_b32_e32 v119, v14
	v_mov_b32_e32 v120, v14
	v_mov_b32_e32 v121, v14
	v_mov_b32_e32 v122, v14
	v_mov_b32_e32 v123, v14
	v_mov_b32_e32 v124, v14
	v_mov_b32_e32 v125, v14
	v_mov_b32_e32 v126, v14
	v_mov_b32_e32 v127, v14
	v_mov_b32_e32 v128, v14
	v_mov_b32_e32 v129, v14
	v_add_u32_e32 v240, s9, v145
	v_ashrrev_i32_e32 v241, 31, v240
	v_or_b32_e32 v242, s12, v165
	v_lshl_add_u64 v[244:245], v[240:241], 2, s[24:25]
	v_ashrrev_i32_e32 v243, 31, v242
	v_lshl_add_u64 v[246:247], v[242:243], 2, s[26:27]
	global_load_dwordx4 v[208:211], v[244:245], off
	global_load_dwordx4 v[212:215], v[244:245], off offset:64
	global_load_dwordx4 v[216:219], v[244:245], off offset:128
	global_load_dwordx4 v[220:223], v[244:245], off offset:192
	global_load_dword v224, v[246:247], off
	global_load_dword v226, v[246:247], off offset:64
	global_load_dword v228, v[246:247], off offset:128
	global_load_dword v230, v[246:247], off offset:192
	global_load_dword v232, v[246:247], off offset:256
	global_load_dword v234, v[246:247], off offset:320
	global_load_dword v236, v[246:247], off offset:384
	global_load_dword v238, v[246:247], off offset:448
; template <bool I8>
; __device__ __forceinline__ void gemm_mainloop_n256(const bf16_t* __restrict__ A, int lda, const bf16_t* __restrict__ Bt, int ldb,
;                                                    int K, int m0, int n0, f32x4 (&acc)[4][8], char* smem) {
;     ...
;   for (int kt = 0; kt < nk; ++kt) {
; #pragma unroll
;     for (int i_ = 0; i_ < 4; ++i_)
;       __builtin_amdgcn_global_load_lds((const unsigned*)(gA + (size_t)(i_ * 32) * lda + kt * 64),
;                                        (unsigned*)(smem + (i_ * 4 + w) * 1024), 16, 0, 0);
; #pragma unroll
;     for (int i_ = 0; i_ < 8; ++i_)
;       __builtin_amdgcn_global_load_lds((const unsigned*)(gB + (size_t)(i_ * 32) * ldb + kt * 64),
;                                        (unsigned*)(smem + 16384 + (i_ * 4 + w) * 1024), 16, 0, 0);
;     asm volatile("s_waitcnt vmcnt(0)" ::: "memory");
;     __syncthreads();
;     const char* sA = smem;
;     const char* sB = smem + 16384;
; #pragma unroll
;     for (int kk = 0; kk < 2; ++kk) {
;       bf16x8 af[4], bfr[8];
;       const int ch = kk * 4 + fq;
; #pragma unroll
;       for (int i = 0; i < 4; ++i) {
;         const int row = wm * 64 + i * 16 + fr;
;         af[i] = *reinterpret_cast<const bf16x8*>(sA + row * 128 + ((ch ^ (row & 7)) << 4));
;       }
; #pragma unroll
;       for (int j = 0; j < 8; ++j) {
;         const int col = wn * 128 + j * 16 + fr;
;         bfr[j] = *reinterpret_cast<const bf16x8*>(sB + col * 128 + ((ch ^ (col & 7)) << 4));
;       }
; #pragma unroll
;       for (int i = 0; i < 4; ++i)
; #pragma unroll
;         for (int j = 0; j < 8; ++j) {
;           if (I8) {
;             typedef __attribute__((ext_vector_type(4))) int i32x4;
;             acc[i][j] = __builtin_bit_cast(f32x4, __builtin_amdgcn_mfma_i32_16x16x64_i8(__builtin_bit_cast(i32x4, af[i]), __builtin_bit_cast(i32x4, bfr[j]),
;                                                                                          __builtin_bit_cast(i32x4, acc[i][j]), 0, 0, 0));
;           } else {
;             acc[i][j] = __builtin_amdgcn_mfma_f32_16x16x32_bf16(af[i], bfr[j], acc[i][j], 0, 0, 0);
;           }
;         }
.LBB0_560:
	v_readfirstlane_b32 s13, v136
	v_add_u32_e32 v142, 0x1000, v136
	v_lshl_add_u64 v[146:147], v[132:133], 0, s[6:7]
	v_add_u32_e32 v144, 0x2000, v136
	v_readfirstlane_b32 s14, v142
	s_mov_b32 m0, s13
	v_add_u32_e32 v156, 0x3000, v136
	v_lshl_add_u64 v[150:151], v[146:147], 0, s[54:55]
	v_readfirstlane_b32 s15, v144
	global_load_lds_dwordx4 v[146:147], off
	s_mov_b32 m0, s14
	v_add_u32_e32 v157, 0x4000, v136
	v_lshl_add_u64 v[152:153], v[146:147], 0, s[56:57]
	v_readfirstlane_b32 s16, v156
	global_load_lds_dwordx4 v[150:151], off
	s_mov_b32 m0, s15
	v_add_u32_e32 v158, 0x5000, v136
	v_lshl_add_u64 v[154:155], v[146:147], 0, s[58:59]
	v_readfirstlane_b32 s17, v157
	global_load_lds_dwordx4 v[152:153], off
	s_mov_b32 m0, s16
	v_lshl_add_u64 v[148:149], v[130:131], 0, s[6:7]
	v_add_u32_e32 v160, 0x6000, v136
	v_readfirstlane_b32 s46, v158
	global_load_lds_dwordx4 v[154:155], off
	s_mov_b32 m0, s17
	v_add_u32_e32 v162, 0x7000, v136
	v_lshl_add_u64 v[156:157], v[148:149], 0, s[54:55]
	v_readfirstlane_b32 s47, v160
	global_load_lds_dwordx4 v[148:149], off
	s_mov_b32 m0, s46
	v_add_u32_e32 v170, 0x8000, v136
	v_lshl_add_u64 v[158:159], v[148:149], 0, s[56:57]
	v_readfirstlane_b32 s76, v162
	global_load_lds_dwordx4 v[156:157], off
	s_mov_b32 m0, s47
	v_add_u32_e32 v172, 0x9000, v136
	v_lshl_add_u64 v[160:161], v[148:149], 0, s[58:59]
	v_readfirstlane_b32 s77, v170
	global_load_lds_dwordx4 v[158:159], off
	s_mov_b32 m0, s76
	v_add_u32_e32 v174, 0xa000, v136
	v_lshl_add_u64 v[162:163], v[148:149], 0, s[68:69]
	v_readfirstlane_b32 s78, v172
	global_load_lds_dwordx4 v[160:161], off
	s_mov_b32 m0, s77
	v_add_u32_e32 v176, 0xb000, v136
	v_lshl_add_u64 v[170:171], v[148:149], 0, s[70:71]
	v_readfirstlane_b32 s79, v174
	global_load_lds_dwordx4 v[162:163], off
	s_mov_b32 m0, s78
	v_lshl_add_u64 v[172:173], v[148:149], 0, s[72:73]
	v_readfirstlane_b32 s91, v176
	global_load_lds_dwordx4 v[170:171], off
	s_mov_b32 m0, s79
	v_lshl_add_u64 v[174:175], v[148:149], 0, s[74:75]
	global_load_lds_dwordx4 v[172:173], off
	s_mov_b32 m0, s91
	v_add_u32_e32 v189, v138, v139
	global_load_lds_dwordx4 v[174:175], off
	v_add_u32_e32 v193, v138, v140
	s_waitcnt vmcnt(0)
	s_waitcnt vmcnt(0) lgkmcnt(0)
	s_barrier
	ds_read_b128 v[146:149], v189
	ds_read_b128 v[150:153], v193 offset:16384
	ds_read_b128 v[154:157], v189 offset:2048
	ds_read_b128 v[158:161], v193 offset:18432
	ds_read_b128 v[170:173], v193 offset:20480
	ds_read_b128 v[174:177], v193 offset:22528
	ds_read_b128 v[178:181], v193 offset:24576
	ds_read_b128 v[196:199], v193 offset:26624
	ds_read_b128 v[200:203], v193 offset:28672
	ds_read_b128 v[204:207], v193 offset:30720
	s_waitcnt lgkmcnt(8)
	v_mfma_i32_16x16x64_i8 v[126:129], v[146:149], v[150:153], v[126:129]
	v_add_u32_e32 v142, v141, v139
	v_add_u32_e32 v144, v141, v140
	s_add_u32 s6, s6, 0x80
	s_waitcnt lgkmcnt(6)
	v_mfma_i32_16x16x64_i8 v[122:125], v[146:149], v[158:161], v[122:125]
	s_addc_u32 s7, s7, 0
	s_cmpk_lg_i32 s6, 0x800
	s_waitcnt lgkmcnt(5)
	v_mfma_i32_16x16x64_i8 v[118:121], v[146:149], v[170:173], v[118:121]
	s_waitcnt lgkmcnt(4)
	v_mfma_i32_16x16x64_i8 v[114:117], v[146:149], v[174:177], v[114:117]
	s_waitcnt lgkmcnt(3)
	v_mfma_i32_16x16x64_i8 v[110:113], v[146:149], v[178:181], v[110:113]
	s_waitcnt lgkmcnt(2)
	v_mfma_i32_16x16x64_i8 v[106:109], v[146:149], v[196:199], v[106:109]
	s_waitcnt lgkmcnt(1)
	v_mfma_i32_16x16x64_i8 v[102:105], v[146:149], v[200:203], v[102:105]
	s_waitcnt lgkmcnt(0)
	v_mfma_i32_16x16x64_i8 v[98:101], v[146:149], v[204:207], v[98:101]
	v_mfma_i32_16x16x64_i8 v[94:97], v[154:157], v[150:153], v[94:97]
	v_mfma_i32_16x16x64_i8 v[90:93], v[154:157], v[158:161], v[90:93]
	v_mfma_i32_16x16x64_i8 v[86:89], v[154:157], v[170:173], v[86:89]
	v_mfma_i32_16x16x64_i8 v[82:85], v[154:157], v[174:177], v[82:85]
	v_mfma_i32_16x16x64_i8 v[78:81], v[154:157], v[178:181], v[78:81]
	v_mfma_i32_16x16x64_i8 v[74:77], v[154:157], v[196:199], v[74:77]
	v_mfma_i32_16x16x64_i8 v[70:73], v[154:157], v[200:203], v[70:73]
	v_mfma_i32_16x16x64_i8 v[66:69], v[154:157], v[204:207], v[66:69]
	ds_read_b128 v[146:149], v189 offset:4096
	ds_read_b128 v[154:157], v189 offset:6144
	s_waitcnt lgkmcnt(1)
	v_mfma_i32_16x16x64_i8 v[62:65], v[146:149], v[150:153], v[62:65]
	v_mfma_i32_16x16x64_i8 v[58:61], v[146:149], v[158:161], v[58:61]
	v_mfma_i32_16x16x64_i8 v[54:57], v[146:149], v[170:173], v[54:57]
	v_mfma_i32_16x16x64_i8 v[50:53], v[146:149], v[174:177], v[50:53]
	v_mfma_i32_16x16x64_i8 v[46:49], v[146:149], v[178:181], v[46:49]
	v_mfma_i32_16x16x64_i8 v[42:45], v[146:149], v[196:199], v[42:45]
	v_mfma_i32_16x16x64_i8 v[38:41], v[146:149], v[200:203], v[38:41]
	v_mfma_i32_16x16x64_i8 v[34:37], v[146:149], v[204:207], v[34:37]
	ds_read_b128 v[146:149], v142
	s_waitcnt lgkmcnt(1)
	v_mfma_i32_16x16x64_i8 v[30:33], v[154:157], v[150:153], v[30:33]
	v_mfma_i32_16x16x64_i8 v[26:29], v[154:157], v[158:161], v[26:29]
	v_mfma_i32_16x16x64_i8 v[22:25], v[154:157], v[170:173], v[22:25]
	v_mfma_i32_16x16x64_i8 v[18:21], v[154:157], v[174:177], v[18:21]
	v_mfma_i32_16x16x64_i8 v[10:13], v[154:157], v[178:181], v[10:13]
	v_mfma_i32_16x16x64_i8 v[6:9], v[154:157], v[196:199], v[6:9]
	v_mfma_i32_16x16x64_i8 v[2:5], v[154:157], v[200:203], v[2:5]
	v_mfma_i32_16x16x64_i8 v[14:17], v[154:157], v[204:207], v[14:17]
	ds_read_b128 v[150:153], v144 offset:16384
	ds_read_b128 v[154:157], v142 offset:2048
	ds_read_b128 v[158:161], v144 offset:18432
	ds_read_b128 v[170:173], v144 offset:20480
	ds_read_b128 v[174:177], v144 offset:22528
	ds_read_b128 v[178:181], v144 offset:24576
	ds_read_b128 v[196:199], v144 offset:26624
	ds_read_b128 v[200:203], v144 offset:28672
	ds_read_b128 v[204:207], v144 offset:30720
	s_waitcnt lgkmcnt(8)
; template <bool I8, class Epi> ...
;     ...
; #pragma unroll
;   for (int i = 0; i < 4; ++i) {
;     const int row = m0 + wm * 64 + i * 16 + (lane >> 4) * 4;
;     float4 rs = float4{1.f, 1.f, 1.f, 1.f};
;     if (I8) rs = *reinterpret_cast<const float4*>(rscale + row);
; #pragma unroll
;     for (int j = 0; j < 8; ++j) {
;       const int col = n0 + wn * 128 + j * 16 + (lane & 15);
;       if (I8) {
;         typedef __attribute__((ext_vector_type(4))) int i32x4;
;         const i32x4 ia = __builtin_bit_cast(i32x4, acc[i][j]);
;         const float cs = cscale[col];
;         epi(row, col, f32x4{(float)ia[0] * rs.x * cs, (float)ia[1] * rs.y * cs, (float)ia[2] * rs.z * cs, (float)ia[3] * rs.w * cs});
;       } else {
;         epi(row, col, acc[i][j]);
;       }
;     }
;   __device__ __forceinline__ void operator()(int row, int col, f32x4 v) const {
; #pragma unroll
;     for (int r = 0; r < 4; ++r) xbcraw[(size_t)(row + r) * DXBC + (col - 3072)] = f2bf(v[r]);
;   }
	v_mfma_i32_16x16x64_i8 v[126:129], v[146:149], v[150:153], v[126:129]
	s_waitcnt lgkmcnt(6)
	v_mfma_i32_16x16x64_i8 v[122:125], v[146:149], v[158:161], v[122:125]
	s_waitcnt lgkmcnt(5)
	v_mfma_i32_16x16x64_i8 v[118:121], v[146:149], v[170:173], v[118:121]
	s_waitcnt lgkmcnt(4)
	v_mfma_i32_16x16x64_i8 v[114:117], v[146:149], v[174:177], v[114:117]
	s_waitcnt lgkmcnt(3)
	v_mfma_i32_16x16x64_i8 v[110:113], v[146:149], v[178:181], v[110:113]
	s_waitcnt lgkmcnt(2)
	v_mfma_i32_16x16x64_i8 v[106:109], v[146:149], v[196:199], v[106:109]
	s_waitcnt lgkmcnt(1)
	v_mfma_i32_16x16x64_i8 v[102:105], v[146:149], v[200:203], v[102:105]
	s_waitcnt lgkmcnt(0)
	v_mfma_i32_16x16x64_i8 v[98:101], v[146:149], v[204:207], v[98:101]
	v_mfma_i32_16x16x64_i8 v[94:97], v[154:157], v[150:153], v[94:97]
	v_mfma_i32_16x16x64_i8 v[90:93], v[154:157], v[158:161], v[90:93]
	v_mfma_i32_16x16x64_i8 v[86:89], v[154:157], v[170:173], v[86:89]
	v_mfma_i32_16x16x64_i8 v[82:85], v[154:157], v[174:177], v[82:85]
	v_mfma_i32_16x16x64_i8 v[78:81], v[154:157], v[178:181], v[78:81]
	v_mfma_i32_16x16x64_i8 v[74:77], v[154:157], v[196:199], v[74:77]
	v_mfma_i32_16x16x64_i8 v[70:73], v[154:157], v[200:203], v[70:73]
	v_mfma_i32_16x16x64_i8 v[66:69], v[154:157], v[204:207], v[66:69]
	ds_read_b128 v[146:149], v142 offset:4096
	ds_read_b128 v[154:157], v142 offset:6144
	s_waitcnt lgkmcnt(0)
	s_barrier
	v_mfma_i32_16x16x64_i8 v[62:65], v[146:149], v[150:153], v[62:65]
	v_mfma_i32_16x16x64_i8 v[58:61], v[146:149], v[158:161], v[58:61]
	v_mfma_i32_16x16x64_i8 v[54:57], v[146:149], v[170:173], v[54:57]
	v_mfma_i32_16x16x64_i8 v[50:53], v[146:149], v[174:177], v[50:53]
	v_mfma_i32_16x16x64_i8 v[46:49], v[146:149], v[178:181], v[46:49]
	v_mfma_i32_16x16x64_i8 v[42:45], v[146:149], v[196:199], v[42:45]
	v_mfma_i32_16x16x64_i8 v[38:41], v[146:149], v[200:203], v[38:41]
	v_mfma_i32_16x16x64_i8 v[34:37], v[146:149], v[204:207], v[34:37]
	v_mfma_i32_16x16x64_i8 v[30:33], v[154:157], v[150:153], v[30:33]
	v_mfma_i32_16x16x64_i8 v[26:29], v[154:157], v[158:161], v[26:29]
	v_mfma_i32_16x16x64_i8 v[22:25], v[154:157], v[170:173], v[22:25]
	v_mfma_i32_16x16x64_i8 v[18:21], v[154:157], v[174:177], v[18:21]
	v_mfma_i32_16x16x64_i8 v[10:13], v[154:157], v[178:181], v[10:13]
	v_mfma_i32_16x16x64_i8 v[6:9], v[154:157], v[196:199], v[6:9]
	v_mfma_i32_16x16x64_i8 v[2:5], v[154:157], v[200:203], v[2:5]
	v_mfma_i32_16x16x64_i8 v[14:17], v[154:157], v[204:207], v[14:17]
	s_cbranch_scc1 .LBB0_560
	v_add_u32_e32 v138, s9, v145
	v_ashrrev_i32_e32 v139, 31, v138
	v_lshl_add_u64 v[140:141], v[138:139], 2, s[24:25]
	v_or_b32_e32 v136, s12, v165
	v_cvt_f32_i32_e32 v162, v118
	v_cvt_f32_i32_e32 v163, v119
	v_lshl_add_u64 v[118:119], v[136:137], 1, s[40:41]
	v_lshl_add_u64 v[146:147], v[136:137], 2, s[26:27]
	v_cvt_f32_i32_e32 v154, v126
	v_cvt_f32_i32_e32 v155, v127
	v_cvt_f32_i32_e32 v158, v122
	v_cvt_f32_i32_e32 v159, v123
	v_or_b32_e32 v126, 2, v138
	v_or_b32_e32 v127, 3, v138
	v_mad_i64_i32 v[122:123], s[6:7], v138, s83, v[118:119]
	v_cvt_f32_i32_e32 v156, v128
	v_cvt_f32_i32_e32 v157, v129
	v_cvt_f32_i32_e32 v160, v124
	v_or_b32_e32 v124, 1, v138
	v_mad_i64_i32 v[148:149], s[6:7], v126, s83, v[118:119]
	v_mad_i64_i32 v[150:151], s[6:7], v127, s83, v[118:119]
	v_add_co_u32_e32 v146, vcc, s86, v122
	v_cvt_f32_i32_e32 v161, v125
	v_mad_i64_i32 v[124:125], s[6:7], v124, s83, v[118:119]
	v_addc_co_u32_e32 v147, vcc, -1, v123, vcc
	v_add_co_u32_e32 v152, vcc, s86, v124
	v_cvt_f32_i32_e32 v102, v102
	s_nop 0
	v_addc_co_u32_e32 v153, vcc, -1, v125, vcc
	v_cvt_f32_i32_e32 v103, v103
	v_cvt_f32_i32_e32 v98, v98
	v_cvt_f32_i32_e32 v104, v104
	v_cvt_f32_i32_e32 v99, v99
	v_cvt_f32_i32_e32 v105, v105
	v_cvt_f32_i32_e32 v100, v100
	v_add_co_u32_e32 v148, vcc, s86, v148
	v_cvt_f32_i32_e32 v101, v101
	s_nop 0
	v_addc_co_u32_e32 v149, vcc, -1, v149, vcc
	v_cvt_f32_i32_e32 v95, v95
	v_add_co_u32_e32 v150, vcc, s86, v150
	v_cvt_f32_i32_e32 v94, v94
	v_cvt_f32_i32_e32 v96, v96
	v_addc_co_u32_e32 v151, vcc, -1, v151, vcc
	v_cvt_f32_i32_e32 v97, v97
	v_cvt_f32_i32_e32 v82, v82
	v_cvt_f32_i32_e32 v83, v83
	v_cvt_f32_i32_e32 v84, v84
	v_cvt_f32_i32_e32 v85, v85
	v_cvt_f32_i32_e32 v78, v78
	v_cvt_f32_i32_e32 v79, v79
	v_cvt_f32_i32_e32 v66, v66
	v_cvt_f32_i32_e32 v67, v67
	v_cvt_f32_i32_e32 v68, v68
	v_cvt_f32_i32_e32 v69, v69
	v_cvt_f32_i32_e32 v74, v74
	v_cvt_f32_i32_e32 v75, v75
	v_cvt_f32_i32_e32 v70, v70
	v_cvt_f32_i32_e32 v76, v76
	v_cvt_f32_i32_e32 v71, v71
	v_cvt_f32_i32_e32 v77, v77
	v_cvt_f32_i32_e32 v72, v72
	v_cvt_f32_i32_e32 v73, v73
	v_cvt_f32_i32_e32 v63, v63
	v_cvt_f32_i32_e32 v62, v62
	v_cvt_f32_i32_e32 v64, v64
	v_cvt_f32_i32_e32 v65, v65
	v_cvt_f32_i32_e32 v38, v38
	v_cvt_f32_i32_e32 v39, v39
	v_mul_f32_e32 v154, v208, v154
	v_mul_f32_e32 v102, v208, v102
	v_mul_f32_e32 v155, v209, v155
	v_mul_f32_e32 v156, v210, v156
	v_mul_f32_e32 v157, v211, v157
	v_mul_f32_e32 v158, v208, v158
	v_mul_f32_e32 v159, v209, v159
	v_mul_f32_e32 v160, v210, v160
	v_mul_f32_e32 v161, v211, v161
	v_mul_f32_e32 v103, v209, v103
	v_mul_f32_e32 v98, v208, v98
	v_mul_f32_e32 v154, v154, v224
	v_mul_f32_e32 v155, v155, v224
	v_mul_f32_e32 v156, v156, v224
	v_mul_f32_e32 v157, v224, v157
	v_mul_f32_e32 v158, v158, v226
	v_mul_f32_e32 v159, v159, v226
	v_mul_f32_e32 v160, v160, v226
	v_mul_f32_e32 v161, v161, v226
	v_cvt_pk_bf16_f32 v154, v154, s0
	v_mul_f32_e32 v104, v210, v104
	v_mul_f32_e32 v99, v209, v99
	v_mul_f32_e32 v102, v102, v236
	v_mul_f32_e32 v103, v103, v236
	v_cvt_pk_bf16_f32 v102, v102, s0
	v_mul_f32_e32 v98, v98, v238
	v_cvt_pk_bf16_f32 v155, v155, s0
	v_cvt_pk_bf16_f32 v156, v156, s0
	v_cvt_pk_bf16_f32 v157, v157, s0
; template <bool I8, class Epi> ...
;     ...
; #pragma unroll
;   for (int i = 0; i < 4; ++i) {
;     const int row = m0 + wm * 64 + i * 16 + (lane >> 4) * 4;
;     float4 rs = float4{1.f, 1.f, 1.f, 1.f};
;     if (I8) rs = *reinterpret_cast<const float4*>(rscale + row);
; #pragma unroll
;     for (int j = 0; j < 8; ++j) {
;       const int col = n0 + wn * 128 + j * 16 + (lane & 15);
;       if (I8) {
;         typedef __attribute__((ext_vector_type(4))) int i32x4;
;         const i32x4 ia = __builtin_bit_cast(i32x4, acc[i][j]);
;         const float cs = cscale[col];
;         epi(row, col, f32x4{(float)ia[0] * rs.x * cs, (float)ia[1] * rs.y * cs, (float)ia[2] * rs.z * cs, (float)ia[3] * rs.w * cs});
;       } else {
;         epi(row, col, acc[i][j]);
;       }
;     }
;   __device__ __forceinline__ void operator()(int row, int col, f32x4 v) const {
; #pragma unroll
;     for (int r = 0; r < 4; ++r) xbcraw[(size_t)(row + r) * DXBC + (col - 3072)] = f2bf(v[r]);
;   }
	v_cvt_pk_bf16_f32 v158, v158, s0
	v_cvt_pk_bf16_f32 v159, v159, s0
	v_cvt_pk_bf16_f32 v160, v160, s0
	v_cvt_pk_bf16_f32 v161, v161, s0
	global_store_short v[146:147], v154, off offset:-2048
	global_store_short v[152:153], v155, off offset:-2048
	global_store_short v[148:149], v156, off offset:-2048
	global_store_short v[150:151], v157, off offset:-2048
	global_store_short v[146:147], v158, off offset:-2016
	global_store_short v[152:153], v159, off offset:-2016
	global_store_short v[148:149], v160, off offset:-2016
	global_store_short v[150:151], v161, off offset:-2016
	v_mul_f32_e32 v104, v104, v236
	v_mul_f32_e32 v105, v211, v105
	global_store_short v[146:147], v102, off offset:-1856
	v_cvt_pk_bf16_f32 v102, v103, s0
	v_mul_f32_e32 v99, v99, v238
	v_mul_f32_e32 v100, v210, v100
	v_cvt_pk_bf16_f32 v98, v98, s0
	v_mul_f32_e32 v105, v105, v236
	global_store_short v[152:153], v102, off offset:-1856
	v_cvt_pk_bf16_f32 v102, v104, s0
	v_mul_f32_e32 v100, v100, v238
	v_mul_f32_e32 v101, v211, v101
	global_store_short v[146:147], v98, off offset:-1824
	v_cvt_pk_bf16_f32 v98, v99, s0
	global_store_short v[148:149], v102, off offset:-1856
	v_cvt_pk_bf16_f32 v102, v105, s0
	v_mul_f32_e32 v101, v101, v238
	global_store_short v[152:153], v98, off offset:-1824
	v_cvt_pk_bf16_f32 v98, v100, s0
	v_mul_f32_e32 v95, v213, v95
	global_store_short v[150:151], v102, off offset:-1856
	global_store_short v[148:149], v98, off offset:-1824
	v_cvt_pk_bf16_f32 v98, v101, s0
	v_mul_f32_e32 v94, v212, v94
	v_mul_f32_e32 v102, v224, v95
	v_mul_f32_e32 v95, v214, v96
	global_store_short v[150:151], v98, off offset:-1824
	v_or_b32_e32 v98, 16, v138
	v_mul_f32_e32 v94, v224, v94
	v_mul_f32_e32 v103, v224, v95
	v_mul_f32_e32 v95, v215, v97
	v_mul_f32_e32 v104, v224, v95
	v_cvt_pk_bf16_f32 v96, v94, s0
	v_mad_i64_i32 v[94:95], s[6:7], v98, s83, v[118:119]
	v_add_co_u32_e32 v94, vcc, s86, v94
	v_or_b32_e32 v99, 17, v138
	s_nop 0
	v_addc_co_u32_e32 v95, vcc, -1, v95, vcc
	global_store_short v[94:95], v96, off offset:-2048
	v_mad_i64_i32 v[96:97], s[6:7], v99, s83, v[118:119]
	v_add_co_u32_e32 v96, vcc, s86, v96
	v_or_b32_e32 v100, 18, v138
	v_cvt_pk_bf16_f32 v98, v102, s0
	v_addc_co_u32_e32 v97, vcc, -1, v97, vcc
	v_mul_f32_e32 v82, v212, v82
	global_store_short v[96:97], v98, off offset:-2048
	v_mad_i64_i32 v[98:99], s[6:7], v100, s83, v[118:119]
	v_mul_f32_e32 v82, v230, v82
	v_mul_f32_e32 v83, v213, v83
	v_or_b32_e32 v101, 19, v138
	v_add_co_u32_e32 v98, vcc, s86, v98
	v_mul_f32_e32 v83, v230, v83
	v_mul_f32_e32 v84, v214, v84
	v_cvt_pk_bf16_f32 v82, v82, s0
	v_addc_co_u32_e32 v99, vcc, -1, v99, vcc
	v_mad_i64_i32 v[100:101], s[6:7], v101, s83, v[118:119]
	v_mul_f32_e32 v84, v230, v84
	v_mul_f32_e32 v85, v215, v85
	global_store_short v[94:95], v82, off offset:-1952
	v_cvt_pk_bf16_f32 v82, v83, s0
	v_add_co_u32_e32 v100, vcc, s86, v100
	v_mul_f32_e32 v85, v230, v85
	global_store_short v[96:97], v82, off offset:-1952
	v_cvt_pk_bf16_f32 v82, v84, s0
	v_addc_co_u32_e32 v101, vcc, -1, v101, vcc
	global_store_short v[98:99], v82, off offset:-1952
	v_cvt_pk_bf16_f32 v82, v85, s0
	v_mul_f32_e32 v78, v212, v78
	global_store_short v[100:101], v82, off offset:-1952
	v_mul_f32_e32 v82, v232, v78
	v_mul_f32_e32 v78, v213, v79
	v_cvt_f32_i32_e32 v83, v80
	v_mul_f32_e32 v84, v232, v78
	v_cvt_f32_i32_e32 v85, v81
	v_mul_f32_e32 v66, v212, v66
	v_mul_f32_e32 v66, v238, v66
	v_mul_f32_e32 v67, v213, v67
	v_mul_f32_e32 v67, v238, v67
	v_mul_f32_e32 v68, v214, v68
	v_cvt_pk_bf16_f32 v66, v66, s0
	v_mul_f32_e32 v68, v238, v68
	v_mul_f32_e32 v69, v215, v69
	global_store_short v[94:95], v66, off offset:-1824
	v_cvt_pk_bf16_f32 v66, v67, s0
	v_mul_f32_e32 v69, v238, v69
	global_store_short v[96:97], v66, off offset:-1824
	v_cvt_pk_bf16_f32 v66, v68, s0
	global_store_short v[98:99], v66, off offset:-1824
	v_cvt_pk_bf16_f32 v66, v69, s0
	global_store_short v[100:101], v66, off offset:-1824
	v_mul_f32_e32 v74, v212, v74
	v_mul_f32_e32 v74, v234, v74
	v_mul_f32_e32 v75, v213, v75
	v_mul_f32_e32 v70, v212, v70
	v_mul_f32_e32 v75, v234, v75
	v_mul_f32_e32 v76, v214, v76
	v_cvt_pk_bf16_f32 v74, v74, s0
	v_mul_f32_e32 v70, v236, v70
	v_mul_f32_e32 v71, v213, v71
	v_mul_f32_e32 v76, v234, v76
	v_mul_f32_e32 v77, v215, v77
	global_store_short v[94:95], v74, off offset:-1888
	v_cvt_pk_bf16_f32 v74, v75, s0
	v_mul_f32_e32 v71, v236, v71
	v_mul_f32_e32 v72, v214, v72
	v_cvt_pk_bf16_f32 v70, v70, s0
	v_mul_f32_e32 v77, v234, v77
	global_store_short v[96:97], v74, off offset:-1888
	v_cvt_pk_bf16_f32 v74, v76, s0
	v_mul_f32_e32 v72, v236, v72
	v_mul_f32_e32 v73, v215, v73
	global_store_short v[94:95], v70, off offset:-1856
	v_cvt_pk_bf16_f32 v70, v71, s0
	global_store_short v[98:99], v74, off offset:-1888
	v_cvt_pk_bf16_f32 v74, v77, s0
	v_mul_f32_e32 v73, v236, v73
	global_store_short v[96:97], v70, off offset:-1856
	v_cvt_pk_bf16_f32 v70, v72, s0
	global_store_short v[100:101], v74, off offset:-1888
	global_store_short v[98:99], v70, off offset:-1856
	v_cvt_pk_bf16_f32 v70, v73, s0
	global_store_short v[100:101], v70, off offset:-1856
	v_or_b32_e32 v70, 32, v138
	v_or_b32_e32 v71, 33, v138
	v_cvt_f32_i32_e32 v34, v34
	v_cvt_f32_i32_e32 v40, v40
	v_cvt_f32_i32_e32 v35, v35
	v_cvt_f32_i32_e32 v41, v41
	v_cvt_f32_i32_e32 v36, v36
	v_or_b32_e32 v72, 34, v138
	v_cvt_f32_i32_e32 v37, v37
	v_cvt_f32_i32_e32 v31, v31
	v_or_b32_e32 v73, 35, v138
	v_cvt_f32_i32_e32 v30, v30
	v_cvt_f32_i32_e32 v32, v32
	v_cvt_f32_i32_e32 v33, v33
	v_cvt_f32_i32_e32 v2, v2
	v_cvt_f32_i32_e32 v3, v3
	v_cvt_f32_i32_e32 v4, v4
	v_cvt_f32_i32_e32 v5, v5
	v_cvt_f32_i32_e32 v114, v114
	v_cvt_f32_i32_e32 v110, v110
	v_cvt_f32_i32_e32 v106, v106
; template <bool I8, class Epi> ...
;     ...
;   for (int i = 0; i < 4; ++i) {
;     const int row = m0 + wm * 64 + i * 16 + (lane >> 4) * 4;
;     float4 rs = float4{1.f, 1.f, 1.f, 1.f};
;     if (I8) rs = *reinterpret_cast<const float4*>(rscale + row);
; #pragma unroll
;     for (int j = 0; j < 8; ++j) {
;       const int col = n0 + wn * 128 + j * 16 + (lane & 15);
;       if (I8) {
;         typedef __attribute__((ext_vector_type(4))) int i32x4;
;         const i32x4 ia = __builtin_bit_cast(i32x4, acc[i][j]);
;         const float cs = cscale[col];
;         epi(row, col, f32x4{(float)ia[0] * rs.x * cs, (float)ia[1] * rs.y * cs, (float)ia[2] * rs.z * cs, (float)ia[3] * rs.w * cs});
;       } else {
;         epi(row, col, acc[i][j]);
;       }
;     }
;   }
;   __device__ __forceinline__ void operator()(int row, int col, f32x4 v) const {
; #pragma unroll
;     for (int r = 0; r < 4; ++r) xbcraw[(size_t)(row + r) * DXBC + (col - 3072)] = f2bf(v[r]);
;   }
	v_cvt_f32_i32_e32 v90, v90
	v_cvt_f32_i32_e32 v86, v86
	v_cvt_f32_i32_e32 v58, v58
	v_cvt_f32_i32_e32 v54, v54
	v_cvt_f32_i32_e32 v50, v50
	v_cvt_f32_i32_e32 v46, v46
	v_cvt_f32_i32_e32 v42, v42
	v_cvt_f32_i32_e32 v26, v26
	v_cvt_f32_i32_e32 v22, v22
	v_mul_f32_e32 v63, v217, v63
	v_mul_f32_e32 v62, v216, v62
	v_mul_f32_e32 v74, v224, v63
	v_mul_f32_e32 v63, v218, v64
	v_mul_f32_e32 v62, v224, v62
	v_mul_f32_e32 v75, v224, v63
	v_mul_f32_e32 v63, v219, v65
	v_mul_f32_e32 v76, v224, v63
	v_cvt_pk_bf16_f32 v64, v62, s0
	v_mad_i64_i32 v[62:63], s[6:7], v70, s83, v[118:119]
	v_add_co_u32_e32 v62, vcc, s86, v62
	v_cvt_pk_bf16_f32 v70, v74, s0
	s_nop 0
	v_addc_co_u32_e32 v63, vcc, -1, v63, vcc
	global_store_short v[62:63], v64, off offset:-2048
	v_mad_i64_i32 v[64:65], s[6:7], v71, s83, v[118:119]
	v_add_co_u32_e32 v64, vcc, s86, v64
	v_mul_f32_e32 v38, v216, v38
	s_nop 0
	v_addc_co_u32_e32 v65, vcc, -1, v65, vcc
	global_store_short v[64:65], v70, off offset:-2048
	v_mad_i64_i32 v[70:71], s[6:7], v72, s83, v[118:119]
	v_mul_f32_e32 v38, v236, v38
	v_mul_f32_e32 v39, v217, v39
	v_mul_f32_e32 v34, v216, v34
	v_add_co_u32_e32 v70, vcc, s86, v70
	v_mul_f32_e32 v39, v236, v39
	v_mul_f32_e32 v40, v218, v40
	v_cvt_pk_bf16_f32 v38, v38, s0
	v_mul_f32_e32 v34, v238, v34
	v_mul_f32_e32 v35, v217, v35
	v_addc_co_u32_e32 v71, vcc, -1, v71, vcc
	v_mad_i64_i32 v[72:73], s[6:7], v73, s83, v[118:119]
	v_mul_f32_e32 v40, v236, v40
	v_mul_f32_e32 v41, v219, v41
	global_store_short v[62:63], v38, off offset:-1856
	v_cvt_pk_bf16_f32 v38, v39, s0
	v_mul_f32_e32 v35, v238, v35
	v_mul_f32_e32 v36, v218, v36
	v_cvt_pk_bf16_f32 v34, v34, s0
	v_add_co_u32_e32 v72, vcc, s86, v72
	v_mul_f32_e32 v41, v236, v41
	global_store_short v[64:65], v38, off offset:-1856
	v_cvt_pk_bf16_f32 v38, v40, s0
	v_mul_f32_e32 v36, v238, v36
	v_mul_f32_e32 v37, v219, v37
	global_store_short v[62:63], v34, off offset:-1824
	v_cvt_pk_bf16_f32 v34, v35, s0
	v_addc_co_u32_e32 v73, vcc, -1, v73, vcc
	global_store_short v[70:71], v38, off offset:-1856
	v_cvt_pk_bf16_f32 v38, v41, s0
	v_mul_f32_e32 v37, v238, v37
	global_store_short v[64:65], v34, off offset:-1824
	v_cvt_pk_bf16_f32 v34, v36, s0
	v_mul_f32_e32 v31, v221, v31
	global_store_short v[72:73], v38, off offset:-1856
	global_store_short v[70:71], v34, off offset:-1824
	v_cvt_pk_bf16_f32 v34, v37, s0
	v_mul_f32_e32 v30, v220, v30
	v_mul_f32_e32 v38, v224, v31
	v_mul_f32_e32 v31, v222, v32
	global_store_short v[72:73], v34, off offset:-1824
	v_or_b32_e32 v34, 48, v138
	v_mul_f32_e32 v30, v224, v30
	v_mul_f32_e32 v39, v224, v31
	v_mul_f32_e32 v31, v223, v33
	v_mul_f32_e32 v40, v224, v31
	v_cvt_pk_bf16_f32 v32, v30, s0
	v_mad_i64_i32 v[30:31], s[6:7], v34, s83, v[118:119]
	v_add_co_u32_e32 v30, vcc, s86, v30
	v_or_b32_e32 v35, 49, v138
	s_nop 0
	v_addc_co_u32_e32 v31, vcc, -1, v31, vcc
	global_store_short v[30:31], v32, off offset:-2048
	v_mad_i64_i32 v[32:33], s[6:7], v35, s83, v[118:119]
	v_add_co_u32_e32 v32, vcc, s86, v32
	v_or_b32_e32 v36, 50, v138
	v_cvt_pk_bf16_f32 v34, v38, s0
	v_addc_co_u32_e32 v33, vcc, -1, v33, vcc
	v_mul_f32_e32 v2, v220, v2
	global_store_short v[32:33], v34, off offset:-2048
	v_mad_i64_i32 v[34:35], s[6:7], v36, s83, v[118:119]
	v_mul_f32_e32 v2, v236, v2
	v_mul_f32_e32 v3, v221, v3
	v_or_b32_e32 v37, 51, v138
	v_add_co_u32_e32 v34, vcc, s86, v34
	v_mul_f32_e32 v3, v236, v3
	v_mul_f32_e32 v4, v222, v4
	v_cvt_pk_bf16_f32 v2, v2, s0
	v_addc_co_u32_e32 v35, vcc, -1, v35, vcc
	v_mad_i64_i32 v[36:37], s[6:7], v37, s83, v[118:119]
	v_mul_f32_e32 v4, v236, v4
	v_mul_f32_e32 v5, v223, v5
	global_store_short v[30:31], v2, off offset:-1856
	v_cvt_pk_bf16_f32 v2, v3, s0
	v_add_co_u32_e32 v36, vcc, s86, v36
	v_mul_f32_e32 v5, v236, v5
	global_store_short v[32:33], v2, off offset:-1856
	v_cvt_pk_bf16_f32 v2, v4, s0
	v_addc_co_u32_e32 v37, vcc, -1, v37, vcc
	v_cvt_f32_i32_e32 v18, v18
	v_cvt_f32_i32_e32 v10, v10
	v_cvt_f32_i32_e32 v6, v6
	global_store_short v[34:35], v2, off offset:-1856
	v_cvt_f32_i32_e32 v2, v14
	v_cvt_pk_bf16_f32 v3, v5, s0
	v_cvt_f32_i32_e32 v115, v115
	v_cvt_f32_i32_e32 v111, v111
	v_cvt_f32_i32_e32 v107, v107
	v_cvt_f32_i32_e32 v91, v91
	v_cvt_f32_i32_e32 v87, v87
	v_cvt_f32_i32_e32 v59, v59
	v_cvt_f32_i32_e32 v55, v55
	v_cvt_f32_i32_e32 v51, v51
	v_cvt_f32_i32_e32 v47, v47
	v_cvt_f32_i32_e32 v43, v43
	v_cvt_f32_i32_e32 v27, v27
	v_cvt_f32_i32_e32 v23, v23
	v_cvt_f32_i32_e32 v19, v19
	v_cvt_f32_i32_e32 v11, v11
	v_cvt_f32_i32_e32 v7, v7
	global_store_short v[36:37], v3, off offset:-1856
	v_cvt_f32_i32_e32 v3, v15
	v_cvt_f32_i32_e32 v120, v120
	v_cvt_f32_i32_e32 v116, v116
	v_cvt_f32_i32_e32 v112, v112
	v_cvt_f32_i32_e32 v108, v108
	v_cvt_f32_i32_e32 v92, v92
	v_cvt_f32_i32_e32 v88, v88
	v_cvt_f32_i32_e32 v60, v60
	v_cvt_f32_i32_e32 v56, v56
	v_cvt_f32_i32_e32 v52, v52
	v_cvt_f32_i32_e32 v48, v48
	v_cvt_f32_i32_e32 v44, v44
	v_cvt_f32_i32_e32 v28, v28
	v_cvt_f32_i32_e32 v24, v24
	v_cvt_f32_i32_e32 v20, v20
	v_cvt_f32_i32_e32 v12, v12
	v_cvt_f32_i32_e32 v8, v8
	v_cvt_f32_i32_e32 v4, v16
	v_cvt_f32_i32_e32 v121, v121
	v_cvt_f32_i32_e32 v117, v117
	v_cvt_f32_i32_e32 v113, v113
	v_cvt_f32_i32_e32 v109, v109
	v_cvt_f32_i32_e32 v93, v93
	v_cvt_f32_i32_e32 v89, v89
	v_cvt_f32_i32_e32 v61, v61
	v_cvt_f32_i32_e32 v57, v57
	v_cvt_f32_i32_e32 v53, v53
	v_cvt_f32_i32_e32 v49, v49
	v_cvt_f32_i32_e32 v45, v45
	v_cvt_f32_i32_e32 v29, v29
	v_cvt_f32_i32_e32 v25, v25
	v_cvt_f32_i32_e32 v21, v21
	v_cvt_f32_i32_e32 v13, v13
	v_cvt_f32_i32_e32 v9, v9
	v_cvt_f32_i32_e32 v5, v17
	v_mul_f32_e32 v114, v208, v114
	v_mul_f32_e32 v110, v208, v110
	v_mul_f32_e32 v106, v208, v106
	v_mul_f32_e32 v90, v212, v90
	v_mul_f32_e32 v86, v212, v86
; template <bool I8, class Epi> ...
;     ...
;   for (int i = 0; i < 4; ++i) {
;     const int row = m0 + wm * 64 + i * 16 + (lane >> 4) * 4;
;     float4 rs = float4{1.f, 1.f, 1.f, 1.f};
;     if (I8) rs = *reinterpret_cast<const float4*>(rscale + row);
; #pragma unroll
;     for (int j = 0; j < 8; ++j) {
;       const int col = n0 + wn * 128 + j * 16 + (lane & 15);
;       if (I8) {
;         typedef __attribute__((ext_vector_type(4))) int i32x4;
;         const i32x4 ia = __builtin_bit_cast(i32x4, acc[i][j]);
;         const float cs = cscale[col];
;         epi(row, col, f32x4{(float)ia[0] * rs.x * cs, (float)ia[1] * rs.y * cs, (float)ia[2] * rs.z * cs, (float)ia[3] * rs.w * cs});
;       } else {
;         epi(row, col, acc[i][j]);
;       }
;     }
;   }
;   __device__ __forceinline__ void operator()(int row, int col, f32x4 v) const {
; #pragma unroll
;     for (int r = 0; r < 4; ++r) xbcraw[(size_t)(row + r) * DXBC + (col - 3072)] = f2bf(v[r]);
;   }
	v_mul_f32_e32 v58, v216, v58
	v_mul_f32_e32 v54, v216, v54
	v_mul_f32_e32 v50, v216, v50
	v_mul_f32_e32 v46, v216, v46
	v_mul_f32_e32 v42, v216, v42
	v_mul_f32_e32 v26, v220, v26
	v_mul_f32_e32 v22, v220, v22
	v_mul_f32_e32 v18, v220, v18
	v_mul_f32_e32 v10, v220, v10
	v_mul_f32_e32 v6, v220, v6
	v_mul_f32_e32 v2, v220, v2
	v_mul_f32_e32 v114, v114, v230
	v_mul_f32_e32 v115, v209, v115
	v_mul_f32_e32 v110, v110, v232
	v_mul_f32_e32 v111, v209, v111
	v_mul_f32_e32 v106, v106, v234
	v_mul_f32_e32 v107, v209, v107
	v_mul_f32_e32 v90, v226, v90
	v_mul_f32_e32 v91, v213, v91
	v_mul_f32_e32 v86, v228, v86
	v_mul_f32_e32 v87, v213, v87
	v_mul_f32_e32 v58, v226, v58
	v_mul_f32_e32 v59, v217, v59
	v_mul_f32_e32 v54, v228, v54
	v_mul_f32_e32 v55, v217, v55
	v_mul_f32_e32 v50, v230, v50
	v_mul_f32_e32 v51, v217, v51
	v_mul_f32_e32 v46, v232, v46
	v_mul_f32_e32 v47, v217, v47
	v_mul_f32_e32 v42, v234, v42
	v_mul_f32_e32 v43, v217, v43
	v_mul_f32_e32 v26, v226, v26
	v_mul_f32_e32 v27, v221, v27
	v_mul_f32_e32 v22, v228, v22
	v_mul_f32_e32 v23, v221, v23
	v_mul_f32_e32 v18, v230, v18
	v_mul_f32_e32 v19, v221, v19
	v_mul_f32_e32 v10, v232, v10
	v_mul_f32_e32 v11, v221, v11
	v_mul_f32_e32 v6, v234, v6
	v_mul_f32_e32 v7, v221, v7
	v_mul_f32_e32 v2, v238, v2
	v_mul_f32_e32 v3, v221, v3
	v_mul_f32_e32 v120, v210, v120
	v_mul_f32_e32 v115, v115, v230
	v_mul_f32_e32 v116, v210, v116
	v_cvt_pk_bf16_f32 v114, v114, s0
	v_mul_f32_e32 v111, v111, v232
	v_mul_f32_e32 v112, v210, v112
	v_cvt_pk_bf16_f32 v110, v110, s0
	v_mul_f32_e32 v107, v107, v234
	v_mul_f32_e32 v108, v210, v108
	v_cvt_pk_bf16_f32 v106, v106, s0
	v_mul_f32_e32 v91, v226, v91
	v_mul_f32_e32 v92, v214, v92
	v_cvt_pk_bf16_f32 v90, v90, s0
	v_mul_f32_e32 v87, v228, v87
	v_mul_f32_e32 v88, v214, v88
	v_cvt_pk_bf16_f32 v86, v86, s0
	v_mul_f32_e32 v83, v214, v83
	v_cvt_pk_bf16_f32 v82, v82, s0
	v_mul_f32_e32 v59, v226, v59
	v_mul_f32_e32 v60, v218, v60
	v_cvt_pk_bf16_f32 v58, v58, s0
	v_mul_f32_e32 v55, v228, v55
	v_mul_f32_e32 v56, v218, v56
	v_cvt_pk_bf16_f32 v54, v54, s0
	v_mul_f32_e32 v51, v230, v51
	v_mul_f32_e32 v52, v218, v52
	v_cvt_pk_bf16_f32 v50, v50, s0
	v_mul_f32_e32 v47, v232, v47
	v_mul_f32_e32 v48, v218, v48
	v_cvt_pk_bf16_f32 v46, v46, s0
	v_mul_f32_e32 v43, v234, v43
	v_mul_f32_e32 v44, v218, v44
	v_cvt_pk_bf16_f32 v42, v42, s0
	v_mul_f32_e32 v27, v226, v27
	v_mul_f32_e32 v28, v222, v28
	v_cvt_pk_bf16_f32 v26, v26, s0
	v_mul_f32_e32 v23, v228, v23
	v_mul_f32_e32 v24, v222, v24
	v_cvt_pk_bf16_f32 v22, v22, s0
	v_mul_f32_e32 v19, v230, v19
	v_mul_f32_e32 v20, v222, v20
	v_cvt_pk_bf16_f32 v18, v18, s0
	v_mul_f32_e32 v11, v232, v11
	v_mul_f32_e32 v12, v222, v12
	v_cvt_pk_bf16_f32 v10, v10, s0
	v_mul_f32_e32 v7, v234, v7
	v_mul_f32_e32 v8, v222, v8
	v_cvt_pk_bf16_f32 v6, v6, s0
	v_mul_f32_e32 v3, v238, v3
	v_mul_f32_e32 v4, v222, v4
	v_cvt_pk_bf16_f32 v2, v2, s0
	v_mul_f32_e32 v162, v208, v162
	v_mul_f32_e32 v154, v209, v163
	v_mul_f32_e32 v120, v120, v228
	v_mul_f32_e32 v121, v211, v121
	v_mul_f32_e32 v116, v116, v230
	v_mul_f32_e32 v117, v211, v117
	global_store_short v[146:147], v114, off offset:-1952
	v_cvt_pk_bf16_f32 v114, v115, s0
	v_mul_f32_e32 v112, v112, v232
	v_mul_f32_e32 v113, v211, v113
	global_store_short v[146:147], v110, off offset:-1920
	v_cvt_pk_bf16_f32 v110, v111, s0
	v_mul_f32_e32 v108, v108, v234
	v_mul_f32_e32 v109, v211, v109
	global_store_short v[146:147], v106, off offset:-1888
	v_cvt_pk_bf16_f32 v106, v107, s0
	v_mul_f32_e32 v92, v226, v92
	v_mul_f32_e32 v93, v215, v93
	global_store_short v[94:95], v90, off offset:-2016
	v_cvt_pk_bf16_f32 v90, v91, s0
	v_mul_f32_e32 v88, v228, v88
	v_mul_f32_e32 v89, v215, v89
	global_store_short v[94:95], v86, off offset:-1984
	v_cvt_pk_bf16_f32 v86, v87, s0
	v_mul_f32_e32 v83, v232, v83
	v_mul_f32_e32 v85, v215, v85
	global_store_short v[94:95], v82, off offset:-1920
	v_cvt_pk_bf16_f32 v82, v84, s0
	v_mul_f32_e32 v60, v226, v60
	v_mul_f32_e32 v61, v219, v61
	global_store_short v[62:63], v58, off offset:-2016
	v_cvt_pk_bf16_f32 v58, v59, s0
	v_mul_f32_e32 v56, v228, v56
	v_mul_f32_e32 v57, v219, v57
	global_store_short v[62:63], v54, off offset:-1984
	v_cvt_pk_bf16_f32 v54, v55, s0
	v_mul_f32_e32 v52, v230, v52
	v_mul_f32_e32 v53, v219, v53
	global_store_short v[62:63], v50, off offset:-1952
	v_cvt_pk_bf16_f32 v50, v51, s0
	v_mul_f32_e32 v48, v232, v48
	v_mul_f32_e32 v49, v219, v49
	global_store_short v[62:63], v46, off offset:-1920
	v_cvt_pk_bf16_f32 v46, v47, s0
	v_mul_f32_e32 v44, v234, v44
	v_mul_f32_e32 v45, v219, v45
	global_store_short v[62:63], v42, off offset:-1888
	v_cvt_pk_bf16_f32 v42, v43, s0
	v_mul_f32_e32 v28, v226, v28
	v_mul_f32_e32 v29, v223, v29
	global_store_short v[30:31], v26, off offset:-2016
	v_cvt_pk_bf16_f32 v26, v27, s0
	v_mul_f32_e32 v24, v228, v24
	v_mul_f32_e32 v25, v223, v25
	global_store_short v[30:31], v22, off offset:-1984
	v_cvt_pk_bf16_f32 v22, v23, s0
	v_mul_f32_e32 v20, v230, v20
	v_mul_f32_e32 v21, v223, v21
	global_store_short v[30:31], v18, off offset:-1952
	v_cvt_pk_bf16_f32 v18, v19, s0
	v_mul_f32_e32 v12, v232, v12
	v_mul_f32_e32 v13, v223, v13
	global_store_short v[30:31], v10, off offset:-1920
	v_cvt_pk_bf16_f32 v10, v11, s0
	v_mul_f32_e32 v8, v234, v8
	v_mul_f32_e32 v9, v223, v9
	global_store_short v[30:31], v6, off offset:-1888
	v_cvt_pk_bf16_f32 v6, v7, s0
	v_mul_f32_e32 v4, v238, v4
	v_mul_f32_e32 v5, v223, v5
	global_store_short v[30:31], v2, off offset:-1824
	v_cvt_pk_bf16_f32 v2, v3, s0
	v_mul_f32_e32 v162, v162, v228
	v_mul_f32_e32 v154, v154, v228
	v_mul_f32_e32 v121, v121, v228
	v_cvt_pk_bf16_f32 v120, v120, s0
	v_mul_f32_e32 v117, v117, v230
; template <bool I8, class Epi> ...
;     ...
;   for (int i = 0; i < 4; ++i) {
;     const int row = m0 + wm * 64 + i * 16 + (lane >> 4) * 4;
;     float4 rs = float4{1.f, 1.f, 1.f, 1.f};
;     if (I8) rs = *reinterpret_cast<const float4*>(rscale + row);
; #pragma unroll
;     for (int j = 0; j < 8; ++j) {
;       const int col = n0 + wn * 128 + j * 16 + (lane & 15);
;       if (I8) {
;         typedef __attribute__((ext_vector_type(4))) int i32x4;
;         const i32x4 ia = __builtin_bit_cast(i32x4, acc[i][j]);
;         const float cs = cscale[col];
;         epi(row, col, f32x4{(float)ia[0] * rs.x * cs, (float)ia[1] * rs.y * cs, (float)ia[2] * rs.z * cs, (float)ia[3] * rs.w * cs});
;       } else {
;         epi(row, col, acc[i][j]);
;       }
;     }
;   }
;   __device__ __forceinline__ void operator()(int row, int col, f32x4 v) const {
; #pragma unroll
;     for (int r = 0; r < 4; ++r) xbcraw[(size_t)(row + r) * DXBC + (col - 3072)] = f2bf(v[r]);
;   }
	global_store_short v[152:153], v114, off offset:-1952
	v_cvt_pk_bf16_f32 v114, v116, s0
	v_mul_f32_e32 v113, v113, v232
	global_store_short v[152:153], v110, off offset:-1920
	v_cvt_pk_bf16_f32 v110, v112, s0
	v_mul_f32_e32 v109, v109, v234
	global_store_short v[152:153], v106, off offset:-1888
	v_cvt_pk_bf16_f32 v106, v108, s0
	v_cvt_pk_bf16_f32 v102, v103, s0
	v_mul_f32_e32 v93, v226, v93
	global_store_short v[96:97], v90, off offset:-2016
	v_cvt_pk_bf16_f32 v90, v92, s0
	v_mul_f32_e32 v89, v228, v89
	global_store_short v[96:97], v86, off offset:-1984
	v_cvt_pk_bf16_f32 v86, v88, s0
	v_mul_f32_e32 v85, v232, v85
	global_store_short v[96:97], v82, off offset:-1920
	v_cvt_pk_bf16_f32 v82, v83, s0
	v_cvt_pk_bf16_f32 v74, v75, s0
	v_mul_f32_e32 v61, v226, v61
	global_store_short v[64:65], v58, off offset:-2016
	v_cvt_pk_bf16_f32 v58, v60, s0
	v_mul_f32_e32 v57, v228, v57
	global_store_short v[64:65], v54, off offset:-1984
	v_cvt_pk_bf16_f32 v54, v56, s0
	v_mul_f32_e32 v53, v230, v53
	global_store_short v[64:65], v50, off offset:-1952
	v_cvt_pk_bf16_f32 v50, v52, s0
	v_mul_f32_e32 v49, v232, v49
	global_store_short v[64:65], v46, off offset:-1920
	v_cvt_pk_bf16_f32 v46, v48, s0
	v_mul_f32_e32 v45, v234, v45
	global_store_short v[64:65], v42, off offset:-1888
	v_cvt_pk_bf16_f32 v42, v44, s0
	v_cvt_pk_bf16_f32 v38, v39, s0
	v_mul_f32_e32 v29, v226, v29
	global_store_short v[32:33], v26, off offset:-2016
	v_cvt_pk_bf16_f32 v26, v28, s0
	v_mul_f32_e32 v25, v228, v25
	global_store_short v[32:33], v22, off offset:-1984
	v_cvt_pk_bf16_f32 v22, v24, s0
	v_mul_f32_e32 v21, v230, v21
	global_store_short v[32:33], v18, off offset:-1952
	v_cvt_pk_bf16_f32 v18, v20, s0
	v_mul_f32_e32 v13, v232, v13
	global_store_short v[32:33], v10, off offset:-1920
	v_cvt_pk_bf16_f32 v10, v12, s0
	v_mul_f32_e32 v9, v234, v9
	global_store_short v[32:33], v6, off offset:-1888
	v_cvt_pk_bf16_f32 v6, v8, s0
	v_mul_f32_e32 v5, v238, v5
	global_store_short v[32:33], v2, off offset:-1824
	v_cvt_pk_bf16_f32 v2, v4, s0
	v_cvt_pk_bf16_f32 v155, v162, s0
	v_cvt_pk_bf16_f32 v154, v154, s0
	global_store_short v[148:149], v120, off offset:-1984
	v_cvt_pk_bf16_f32 v120, v121, s0
	global_store_short v[148:149], v114, off offset:-1952
	v_cvt_pk_bf16_f32 v114, v117, s0
	global_store_short v[148:149], v110, off offset:-1920
	v_cvt_pk_bf16_f32 v110, v113, s0
	global_store_short v[148:149], v106, off offset:-1888
	v_cvt_pk_bf16_f32 v106, v109, s0
	global_store_short v[98:99], v102, off offset:-2048
	v_cvt_pk_bf16_f32 v102, v104, s0
	global_store_short v[98:99], v90, off offset:-2016
	v_cvt_pk_bf16_f32 v90, v93, s0
	global_store_short v[98:99], v86, off offset:-1984
	v_cvt_pk_bf16_f32 v86, v89, s0
	global_store_short v[98:99], v82, off offset:-1920
	v_cvt_pk_bf16_f32 v82, v85, s0
	global_store_short v[70:71], v74, off offset:-2048
	v_cvt_pk_bf16_f32 v74, v76, s0
	global_store_short v[70:71], v58, off offset:-2016
	v_cvt_pk_bf16_f32 v58, v61, s0
	global_store_short v[70:71], v54, off offset:-1984
	v_cvt_pk_bf16_f32 v54, v57, s0
	global_store_short v[70:71], v50, off offset:-1952
	v_cvt_pk_bf16_f32 v50, v53, s0
	global_store_short v[70:71], v46, off offset:-1920
	v_cvt_pk_bf16_f32 v46, v49, s0
	global_store_short v[70:71], v42, off offset:-1888
	v_cvt_pk_bf16_f32 v42, v45, s0
	global_store_short v[34:35], v38, off offset:-2048
	v_cvt_pk_bf16_f32 v38, v40, s0
	global_store_short v[34:35], v26, off offset:-2016
	v_cvt_pk_bf16_f32 v26, v29, s0
	global_store_short v[34:35], v22, off offset:-1984
	v_cvt_pk_bf16_f32 v22, v25, s0
	global_store_short v[34:35], v18, off offset:-1952
	v_cvt_pk_bf16_f32 v18, v21, s0
	global_store_short v[34:35], v10, off offset:-1920
	v_cvt_pk_bf16_f32 v10, v13, s0
	global_store_short v[34:35], v6, off offset:-1888
	v_cvt_pk_bf16_f32 v6, v9, s0
	global_store_short v[34:35], v2, off offset:-1824
	v_cvt_pk_bf16_f32 v2, v5, s0
	global_store_short v[146:147], v155, off offset:-1984
	global_store_short v[152:153], v154, off offset:-1984
	global_store_short v[150:151], v120, off offset:-1984
	global_store_short v[150:151], v114, off offset:-1952
	global_store_short v[150:151], v110, off offset:-1920
	global_store_short v[150:151], v106, off offset:-1888
	global_store_short v[100:101], v102, off offset:-2048
	global_store_short v[100:101], v90, off offset:-2016
	global_store_short v[100:101], v86, off offset:-1984
	global_store_short v[100:101], v82, off offset:-1920
	global_store_short v[72:73], v74, off offset:-2048
	global_store_short v[72:73], v58, off offset:-2016
	global_store_short v[72:73], v54, off offset:-1984
	global_store_short v[72:73], v50, off offset:-1952
	global_store_short v[72:73], v46, off offset:-1920
	global_store_short v[72:73], v42, off offset:-1888
	global_store_short v[36:37], v38, off offset:-2048
	global_store_short v[36:37], v26, off offset:-2016
	global_store_short v[36:37], v22, off offset:-1984
	global_store_short v[36:37], v18, off offset:-1952
	global_store_short v[36:37], v10, off offset:-1920
	global_store_short v[36:37], v6, off offset:-1888
	global_store_short v[36:37], v2, off offset:-1824
	s_mov_b64 s[6:7], 0
; __device__ __forceinline__ int opaque_tid() { int t = threadIdx.x; asm volatile("" : "+v"(t)); return t; }
; template <bool I8>
; __device__ __forceinline__ void gemm_mainloop_n256(const bf16_t* __restrict__ A, int lda, const bf16_t* __restrict__ Bt, int ldb,
;                                                    int K, int m0, int n0, f32x4 (&acc)[4][8], char* smem) {
;   const int tid = opaque_tid(), lane = tid & 63, w = tid >> 6;
;   const int wm = w >> 1, wn = w & 1;
; #pragma unroll
;   for (int i = 0; i < 4; ++i)
; #pragma unroll
;     for (int j = 0; j < 8; ++j) acc[i][j] = f32x4{0.f, 0.f, 0.f, 0.f};
;   const int nk = K / 64;
;   const int rowoff = lane >> 3, lch = (lane & 7) ^ rowoff;
;   const bf16_t* gA = A + (size_t)(m0 + w * 8 + rowoff) * lda + lch * 8;
;   const bf16_t* gB = Bt + (size_t)(n0 + w * 8 + rowoff) * ldb + lch * 8;
;   const int fr = lane & 15, fq = lane >> 4;
; template <bool I8, class Epi> ...
;     ...
; #pragma unroll
;   for (int i = 0; i < 4; ++i) {
;     const int row = m0 + wm * 64 + i * 16 + (lane >> 4) * 4;
;     float4 rs = float4{1.f, 1.f, 1.f, 1.f};
;     if (I8) rs = *reinterpret_cast<const float4*>(rscale + row);
; #pragma unroll
;     for (int j = 0; j < 8; ++j) {
;       const int col = n0 + wn * 128 + j * 16 + (lane & 15);
;       if (I8) {
;         typedef __attribute__((ext_vector_type(4))) int i32x4;
;         const i32x4 ia = __builtin_bit_cast(i32x4, acc[i][j]);
;         const float cs = cscale[col];
.LBB0_562:
	s_and_b64 vcc, exec, s[6:7]
	s_cbranch_vccz .LBB0_566
	v_mov_b32_e32 v2, v0
	s_add_i32 s6, s11, s10
	v_bfe_u32 v4, v2, 3, 3
	v_bfe_u32 v9, v2, 4, 2
	v_ashrrev_i32_e32 v3, 6, v2
	v_and_b32_e32 v5, 7, v2
	v_bitop3_b32 v6, v4, v2, 7 bitop3:0x78
	v_and_b32_e32 v8, 15, v2
	v_lshrrev_b32_e32 v10, 1, v2
	v_bitop3_b32 v2, v9, v2, 7 bitop3:0x78
	v_lshlrev_b32_e32 v7, 3, v3
	v_lshlrev_b32_e32 v136, 10, v3
	v_lshlrev_b32_e32 v3, 7, v3
	v_lshlrev_b32_e32 v138, 4, v2
	v_bitop3_b32 v2, v9, v5, 4 bitop3:0x36
	v_and_or_b32 v3, v3, s82, v8
	v_lshlrev_b32_e32 v141, 4, v2
	v_add3_u32 v2, v4, s12, v7
	v_lshlrev_b32_e32 v140, 7, v3
	v_ashrrev_i32_e32 v3, 31, v2
	v_lshlrev_b64 v[2:3], 11, v[2:3]
	v_lshlrev_b32_e32 v5, 4, v6
	v_or_b32_e32 v2, v2, v5
	v_lshl_add_u64 v[130:131], s[22:23], 0, v[2:3]
	v_add3_u32 v2, s6, v4, v7
	v_ashrrev_i32_e32 v3, 31, v2
	v_lshlrev_b64 v[2:3], 11, v[2:3]
	v_and_or_b32 v10, v10, s84, v8
	v_or_b32_e32 v2, v2, v5
	v_mov_b32_e32 v14, 0
	v_lshlrev_b32_e32 v139, 7, v10
	v_lshl_add_u64 v[132:133], s[20:21], 0, v[2:3]
	s_mov_b64 s[6:7], 0
	v_mov_b32_e32 v15, v14
	v_mov_b32_e32 v16, v14
	v_mov_b32_e32 v17, v14
	v_mov_b32_e32 v2, v14
	v_mov_b32_e32 v3, v14
	v_mov_b32_e32 v4, v14
	v_mov_b32_e32 v5, v14
	v_mov_b32_e32 v6, v14
	v_mov_b32_e32 v7, v14
	v_mov_b32_e32 v8, v14
	v_mov_b32_e32 v9, v14
	v_mov_b32_e32 v10, v14
	v_mov_b32_e32 v11, v14
	v_mov_b32_e32 v12, v14
	v_mov_b32_e32 v13, v14
	v_mov_b32_e32 v18, v14
	v_mov_b32_e32 v19, v14
	v_mov_b32_e32 v20, v14
	v_mov_b32_e32 v21, v14
	v_mov_b32_e32 v22, v14
	v_mov_b32_e32 v23, v14
	v_mov_b32_e32 v24, v14
	v_mov_b32_e32 v25, v14
	v_mov_b32_e32 v26, v14
	v_mov_b32_e32 v27, v14
	v_mov_b32_e32 v28, v14
	v_mov_b32_e32 v29, v14
	v_mov_b32_e32 v30, v14
	v_mov_b32_e32 v31, v14
	v_mov_b32_e32 v32, v14
	v_mov_b32_e32 v33, v14
	v_mov_b32_e32 v34, v14
	v_mov_b32_e32 v35, v14
	v_mov_b32_e32 v36, v14
	v_mov_b32_e32 v37, v14
	v_mov_b32_e32 v38, v14
	v_mov_b32_e32 v39, v14
	v_mov_b32_e32 v40, v14
	v_mov_b32_e32 v41, v14
	v_mov_b32_e32 v42, v14
	v_mov_b32_e32 v43, v14
	v_mov_b32_e32 v44, v14
	v_mov_b32_e32 v45, v14
	v_mov_b32_e32 v46, v14
	v_mov_b32_e32 v47, v14
	v_mov_b32_e32 v48, v14
	v_mov_b32_e32 v49, v14
	v_mov_b32_e32 v50, v14
	v_mov_b32_e32 v51, v14
	v_mov_b32_e32 v52, v14
	v_mov_b32_e32 v53, v14
	v_mov_b32_e32 v54, v14
	v_mov_b32_e32 v55, v14
	v_mov_b32_e32 v56, v14
	v_mov_b32_e32 v57, v14
	v_mov_b32_e32 v58, v14
	v_mov_b32_e32 v59, v14
	v_mov_b32_e32 v60, v14
	v_mov_b32_e32 v61, v14
	v_mov_b32_e32 v62, v14
	v_mov_b32_e32 v63, v14
	v_mov_b32_e32 v64, v14
	v_mov_b32_e32 v65, v14
	v_mov_b32_e32 v66, v14
	v_mov_b32_e32 v67, v14
	v_mov_b32_e32 v68, v14
	v_mov_b32_e32 v69, v14
	v_mov_b32_e32 v70, v14
	v_mov_b32_e32 v71, v14
	v_mov_b32_e32 v72, v14
	v_mov_b32_e32 v73, v14
	v_mov_b32_e32 v74, v14
	v_mov_b32_e32 v75, v14
	v_mov_b32_e32 v76, v14
	v_mov_b32_e32 v77, v14
	v_mov_b32_e32 v78, v14
	v_mov_b32_e32 v79, v14
	v_mov_b32_e32 v80, v14
	v_mov_b32_e32 v81, v14
	v_mov_b32_e32 v82, v14
	v_mov_b32_e32 v83, v14
	v_mov_b32_e32 v84, v14
	v_mov_b32_e32 v85, v14
	v_mov_b32_e32 v86, v14
	v_mov_b32_e32 v87, v14
	v_mov_b32_e32 v88, v14
	v_mov_b32_e32 v89, v14
	v_mov_b32_e32 v90, v14
	v_mov_b32_e32 v91, v14
	v_mov_b32_e32 v92, v14
	v_mov_b32_e32 v93, v14
	v_mov_b32_e32 v94, v14
	v_mov_b32_e32 v95, v14
	v_mov_b32_e32 v96, v14
	v_mov_b32_e32 v97, v14
	v_mov_b32_e32 v98, v14
	v_mov_b32_e32 v99, v14
	v_mov_b32_e32 v100, v14
	v_mov_b32_e32 v101, v14
	v_mov_b32_e32 v102, v14
	v_mov_b32_e32 v103, v14
	v_mov_b32_e32 v104, v14
	v_mov_b32_e32 v105, v14
	v_mov_b32_e32 v106, v14
	v_mov_b32_e32 v107, v14
	v_mov_b32_e32 v108, v14
	v_mov_b32_e32 v109, v14
	v_mov_b32_e32 v110, v14
	v_mov_b32_e32 v111, v14
	v_mov_b32_e32 v112, v14
	v_mov_b32_e32 v113, v14
	v_mov_b32_e32 v114, v14
	v_mov_b32_e32 v115, v14
	v_mov_b32_e32 v116, v14
	v_mov_b32_e32 v117, v14
	v_mov_b32_e32 v118, v14
	v_mov_b32_e32 v119, v14
	v_mov_b32_e32 v120, v14
	v_mov_b32_e32 v121, v14
	v_mov_b32_e32 v122, v14
	v_mov_b32_e32 v123, v14
	v_mov_b32_e32 v124, v14
	v_mov_b32_e32 v125, v14
	v_mov_b32_e32 v126, v14
	v_mov_b32_e32 v127, v14
	v_mov_b32_e32 v128, v14
	v_mov_b32_e32 v129, v14
	v_add_u32_e32 v240, s9, v145
	v_ashrrev_i32_e32 v241, 31, v240
	v_or_b32_e32 v242, s12, v165
	v_lshl_add_u64 v[244:245], v[240:241], 2, s[24:25]
	v_ashrrev_i32_e32 v243, 31, v242
	v_lshl_add_u64 v[246:247], v[242:243], 2, s[26:27]
	global_load_dwordx4 v[208:211], v[244:245], off
	global_load_dwordx4 v[212:215], v[244:245], off offset:64
	global_load_dwordx4 v[216:219], v[244:245], off offset:128
	global_load_dwordx4 v[220:223], v[244:245], off offset:192
	global_load_dword v224, v[246:247], off
	global_load_dword v226, v[246:247], off offset:64
	global_load_dword v228, v[246:247], off offset:128
	global_load_dword v230, v[246:247], off offset:192
	global_load_dword v232, v[246:247], off offset:256
	global_load_dword v234, v[246:247], off offset:320
	global_load_dword v236, v[246:247], off offset:384
	global_load_dword v238, v[246:247], off offset:448
; template <bool I8>
; __device__ __forceinline__ void gemm_mainloop_n256(const bf16_t* __restrict__ A, int lda, const bf16_t* __restrict__ Bt, int ldb,
;                                                    int K, int m0, int n0, f32x4 (&acc)[4][8], char* smem) {
;     ...
;   for (int kt = 0; kt < nk; ++kt) {
; #pragma unroll
;     for (int i_ = 0; i_ < 4; ++i_)
;       __builtin_amdgcn_global_load_lds((const unsigned*)(gA + (size_t)(i_ * 32) * lda + kt * 64),
;                                        (unsigned*)(smem + (i_ * 4 + w) * 1024), 16, 0, 0);
; #pragma unroll
;     for (int i_ = 0; i_ < 8; ++i_)
;       __builtin_amdgcn_global_load_lds((const unsigned*)(gB + (size_t)(i_ * 32) * ldb + kt * 64),
;                                        (unsigned*)(smem + 16384 + (i_ * 4 + w) * 1024), 16, 0, 0);
;     asm volatile("s_waitcnt vmcnt(0)" ::: "memory");
;     __syncthreads();
;     const char* sA = smem;
;     const char* sB = smem + 16384;
; #pragma unroll
;     for (int kk = 0; kk < 2; ++kk) {
;       bf16x8 af[4], bfr[8];
;       const int ch = kk * 4 + fq;
; #pragma unroll
;       for (int i = 0; i < 4; ++i) {
;         const int row = wm * 64 + i * 16 + fr;
;         af[i] = *reinterpret_cast<const bf16x8*>(sA + row * 128 + ((ch ^ (row & 7)) << 4));
;       }
; #pragma unroll
;       for (int j = 0; j < 8; ++j) {
;         const int col = wn * 128 + j * 16 + fr;
;         bfr[j] = *reinterpret_cast<const bf16x8*>(sB + col * 128 + ((ch ^ (col & 7)) << 4));
;       }
; #pragma unroll
;       for (int i = 0; i < 4; ++i)
; #pragma unroll
;         for (int j = 0; j < 8; ++j) {
;           if (I8) {
;             typedef __attribute__((ext_vector_type(4))) int i32x4;
;             acc[i][j] = __builtin_bit_cast(f32x4, __builtin_amdgcn_mfma_i32_16x16x64_i8(__builtin_bit_cast(i32x4, af[i]), __builtin_bit_cast(i32x4, bfr[j]),
;                                                                                          __builtin_bit_cast(i32x4, acc[i][j]), 0, 0, 0));
;           } else {
;             acc[i][j] = __builtin_amdgcn_mfma_f32_16x16x32_bf16(af[i], bfr[j], acc[i][j], 0, 0, 0);
;           }
;         }
;     }
.LBB0_564:
	v_readfirstlane_b32 s13, v136
	v_add_u32_e32 v142, 0x1000, v136
	v_lshl_add_u64 v[146:147], v[132:133], 0, s[6:7]
	v_add_u32_e32 v144, 0x2000, v136
	v_readfirstlane_b32 s14, v142
	s_mov_b32 m0, s13
	v_add_u32_e32 v156, 0x3000, v136
	v_lshl_add_u64 v[150:151], v[146:147], 0, s[54:55]
	v_readfirstlane_b32 s15, v144
	global_load_lds_dwordx4 v[146:147], off
	s_mov_b32 m0, s14
	v_add_u32_e32 v157, 0x4000, v136
	v_lshl_add_u64 v[152:153], v[146:147], 0, s[56:57]
	v_readfirstlane_b32 s16, v156
	global_load_lds_dwordx4 v[150:151], off
	s_mov_b32 m0, s15
	v_add_u32_e32 v158, 0x5000, v136
	v_lshl_add_u64 v[154:155], v[146:147], 0, s[58:59]
	v_readfirstlane_b32 s17, v157
	global_load_lds_dwordx4 v[152:153], off
	s_mov_b32 m0, s16
	v_lshl_add_u64 v[148:149], v[130:131], 0, s[6:7]
	v_add_u32_e32 v160, 0x6000, v136
	v_readfirstlane_b32 s46, v158
	global_load_lds_dwordx4 v[154:155], off
	s_mov_b32 m0, s17
	v_add_u32_e32 v162, 0x7000, v136
	v_lshl_add_u64 v[156:157], v[148:149], 0, s[54:55]
	v_readfirstlane_b32 s47, v160
	global_load_lds_dwordx4 v[148:149], off
	s_mov_b32 m0, s46
	v_add_u32_e32 v170, 0x8000, v136
	v_lshl_add_u64 v[158:159], v[148:149], 0, s[56:57]
	v_readfirstlane_b32 s76, v162
	global_load_lds_dwordx4 v[156:157], off
	s_mov_b32 m0, s47
	v_add_u32_e32 v172, 0x9000, v136
	v_lshl_add_u64 v[160:161], v[148:149], 0, s[58:59]
	v_readfirstlane_b32 s77, v170
	global_load_lds_dwordx4 v[158:159], off
	s_mov_b32 m0, s76
	v_add_u32_e32 v174, 0xa000, v136
	v_lshl_add_u64 v[162:163], v[148:149], 0, s[68:69]
	v_readfirstlane_b32 s78, v172
	global_load_lds_dwordx4 v[160:161], off
	s_mov_b32 m0, s77
	v_add_u32_e32 v176, 0xb000, v136
	v_lshl_add_u64 v[170:171], v[148:149], 0, s[70:71]
	v_readfirstlane_b32 s79, v174
	global_load_lds_dwordx4 v[162:163], off
	s_mov_b32 m0, s78
	v_lshl_add_u64 v[172:173], v[148:149], 0, s[72:73]
	v_readfirstlane_b32 s91, v176
	global_load_lds_dwordx4 v[170:171], off
	s_mov_b32 m0, s79
	v_lshl_add_u64 v[174:175], v[148:149], 0, s[74:75]
	global_load_lds_dwordx4 v[172:173], off
	s_mov_b32 m0, s91
	v_add_u32_e32 v189, v138, v139
	global_load_lds_dwordx4 v[174:175], off
	v_add_u32_e32 v193, v138, v140
	s_waitcnt vmcnt(0)
	s_waitcnt vmcnt(0) lgkmcnt(0)
	s_barrier
	ds_read_b128 v[146:149], v189
	ds_read_b128 v[150:153], v193 offset:16384
	ds_read_b128 v[154:157], v189 offset:2048
	ds_read_b128 v[158:161], v193 offset:18432
	ds_read_b128 v[170:173], v193 offset:20480
	ds_read_b128 v[174:177], v193 offset:22528
	ds_read_b128 v[178:181], v193 offset:24576
	ds_read_b128 v[196:199], v193 offset:26624
	ds_read_b128 v[200:203], v193 offset:28672
	ds_read_b128 v[204:207], v193 offset:30720
	s_waitcnt lgkmcnt(8)
	v_mfma_i32_16x16x64_i8 v[126:129], v[146:149], v[150:153], v[126:129]
	v_add_u32_e32 v142, v141, v139
	v_add_u32_e32 v144, v141, v140
	s_add_u32 s6, s6, 0x80
	s_waitcnt lgkmcnt(6)
	v_mfma_i32_16x16x64_i8 v[122:125], v[146:149], v[158:161], v[122:125]
	s_addc_u32 s7, s7, 0
	s_cmpk_lg_i32 s6, 0x800
	s_waitcnt lgkmcnt(5)
	v_mfma_i32_16x16x64_i8 v[118:121], v[146:149], v[170:173], v[118:121]
	s_waitcnt lgkmcnt(4)
	v_mfma_i32_16x16x64_i8 v[114:117], v[146:149], v[174:177], v[114:117]
	s_waitcnt lgkmcnt(3)
	v_mfma_i32_16x16x64_i8 v[110:113], v[146:149], v[178:181], v[110:113]
	s_waitcnt lgkmcnt(2)
	v_mfma_i32_16x16x64_i8 v[106:109], v[146:149], v[196:199], v[106:109]
	s_waitcnt lgkmcnt(1)
	v_mfma_i32_16x16x64_i8 v[102:105], v[146:149], v[200:203], v[102:105]
	s_waitcnt lgkmcnt(0)
	v_mfma_i32_16x16x64_i8 v[98:101], v[146:149], v[204:207], v[98:101]
	v_mfma_i32_16x16x64_i8 v[94:97], v[154:157], v[150:153], v[94:97]
	v_mfma_i32_16x16x64_i8 v[90:93], v[154:157], v[158:161], v[90:93]
	v_mfma_i32_16x16x64_i8 v[86:89], v[154:157], v[170:173], v[86:89]
	v_mfma_i32_16x16x64_i8 v[82:85], v[154:157], v[174:177], v[82:85]
	v_mfma_i32_16x16x64_i8 v[78:81], v[154:157], v[178:181], v[78:81]
	v_mfma_i32_16x16x64_i8 v[74:77], v[154:157], v[196:199], v[74:77]
	v_mfma_i32_16x16x64_i8 v[70:73], v[154:157], v[200:203], v[70:73]
	v_mfma_i32_16x16x64_i8 v[66:69], v[154:157], v[204:207], v[66:69]
	ds_read_b128 v[146:149], v189 offset:4096
	ds_read_b128 v[154:157], v189 offset:6144
	s_waitcnt lgkmcnt(1)
	v_mfma_i32_16x16x64_i8 v[62:65], v[146:149], v[150:153], v[62:65]
	v_mfma_i32_16x16x64_i8 v[58:61], v[146:149], v[158:161], v[58:61]
	v_mfma_i32_16x16x64_i8 v[54:57], v[146:149], v[170:173], v[54:57]
	v_mfma_i32_16x16x64_i8 v[50:53], v[146:149], v[174:177], v[50:53]
	v_mfma_i32_16x16x64_i8 v[46:49], v[146:149], v[178:181], v[46:49]
	v_mfma_i32_16x16x64_i8 v[42:45], v[146:149], v[196:199], v[42:45]
	v_mfma_i32_16x16x64_i8 v[38:41], v[146:149], v[200:203], v[38:41]
	v_mfma_i32_16x16x64_i8 v[34:37], v[146:149], v[204:207], v[34:37]
	ds_read_b128 v[146:149], v142
	s_waitcnt lgkmcnt(1)
	v_mfma_i32_16x16x64_i8 v[30:33], v[154:157], v[150:153], v[30:33]
	v_mfma_i32_16x16x64_i8 v[26:29], v[154:157], v[158:161], v[26:29]
	v_mfma_i32_16x16x64_i8 v[22:25], v[154:157], v[170:173], v[22:25]
	v_mfma_i32_16x16x64_i8 v[18:21], v[154:157], v[174:177], v[18:21]
	v_mfma_i32_16x16x64_i8 v[10:13], v[154:157], v[178:181], v[10:13]
	v_mfma_i32_16x16x64_i8 v[6:9], v[154:157], v[196:199], v[6:9]
	v_mfma_i32_16x16x64_i8 v[2:5], v[154:157], v[200:203], v[2:5]
	v_mfma_i32_16x16x64_i8 v[14:17], v[154:157], v[204:207], v[14:17]
	ds_read_b128 v[150:153], v144 offset:16384
	ds_read_b128 v[154:157], v142 offset:2048
	ds_read_b128 v[158:161], v144 offset:18432
	ds_read_b128 v[170:173], v144 offset:20480
	ds_read_b128 v[174:177], v144 offset:22528
	ds_read_b128 v[178:181], v144 offset:24576
	ds_read_b128 v[196:199], v144 offset:26624
	ds_read_b128 v[200:203], v144 offset:28672
	ds_read_b128 v[204:207], v144 offset:30720
	s_waitcnt lgkmcnt(8)
; template <bool I8>
; __device__ __forceinline__ void gemm_mainloop_n256(const bf16_t* __restrict__ A, int lda, const bf16_t* __restrict__ Bt, int ldb,
;                                                    int K, int m0, int n0, f32x4 (&acc)[4][8], char* smem) {
;     ...
; #pragma unroll
;       for (int i = 0; i < 4; ++i)
; #pragma unroll
;         for (int j = 0; j < 8; ++j) {
;           if (I8) {
;             typedef __attribute__((ext_vector_type(4))) int i32x4;
;             acc[i][j] = __builtin_bit_cast(f32x4, __builtin_amdgcn_mfma_i32_16x16x64_i8(__builtin_bit_cast(i32x4, af[i]), __builtin_bit_cast(i32x4, bfr[j]),
;                                                                                          __builtin_bit_cast(i32x4, acc[i][j]), 0, 0, 0));
;           } else {
;             acc[i][j] = __builtin_amdgcn_mfma_f32_16x16x32_bf16(af[i], bfr[j], acc[i][j], 0, 0, 0);
;           }
;         }
;     }
;     __syncthreads();
; template <bool I8, class Epi> ...
;     ...
;   for (int i = 0; i < 4; ++i) {
;     const int row = m0 + wm * 64 + i * 16 + (lane >> 4) * 4;
;     float4 rs = float4{1.f, 1.f, 1.f, 1.f};
;     if (I8) rs = *reinterpret_cast<const float4*>(rscale + row);
; #pragma unroll
;     for (int j = 0; j < 8; ++j) {
;       const int col = n0 + wn * 128 + j * 16 + (lane & 15);
;       if (I8) {
;         typedef __attribute__((ext_vector_type(4))) int i32x4;
;         const i32x4 ia = __builtin_bit_cast(i32x4, acc[i][j]);
;         const float cs = cscale[col];
;         epi(row, col, f32x4{(float)ia[0] * rs.x * cs, (float)ia[1] * rs.y * cs, (float)ia[2] * rs.z * cs, (float)ia[3] * rs.w * cs});
;       } else {
;         epi(row, col, acc[i][j]);
;       }
;     }
;   }
	v_mfma_i32_16x16x64_i8 v[126:129], v[146:149], v[150:153], v[126:129]
	s_waitcnt lgkmcnt(6)
	v_mfma_i32_16x16x64_i8 v[122:125], v[146:149], v[158:161], v[122:125]
	s_waitcnt lgkmcnt(5)
	v_mfma_i32_16x16x64_i8 v[118:121], v[146:149], v[170:173], v[118:121]
	s_waitcnt lgkmcnt(4)
	v_mfma_i32_16x16x64_i8 v[114:117], v[146:149], v[174:177], v[114:117]
	s_waitcnt lgkmcnt(3)
	v_mfma_i32_16x16x64_i8 v[110:113], v[146:149], v[178:181], v[110:113]
	s_waitcnt lgkmcnt(2)
	v_mfma_i32_16x16x64_i8 v[106:109], v[146:149], v[196:199], v[106:109]
	s_waitcnt lgkmcnt(1)
	v_mfma_i32_16x16x64_i8 v[102:105], v[146:149], v[200:203], v[102:105]
	s_waitcnt lgkmcnt(0)
	v_mfma_i32_16x16x64_i8 v[98:101], v[146:149], v[204:207], v[98:101]
	v_mfma_i32_16x16x64_i8 v[94:97], v[154:157], v[150:153], v[94:97]
	v_mfma_i32_16x16x64_i8 v[90:93], v[154:157], v[158:161], v[90:93]
	v_mfma_i32_16x16x64_i8 v[86:89], v[154:157], v[170:173], v[86:89]
	v_mfma_i32_16x16x64_i8 v[82:85], v[154:157], v[174:177], v[82:85]
	v_mfma_i32_16x16x64_i8 v[78:81], v[154:157], v[178:181], v[78:81]
	v_mfma_i32_16x16x64_i8 v[74:77], v[154:157], v[196:199], v[74:77]
	v_mfma_i32_16x16x64_i8 v[70:73], v[154:157], v[200:203], v[70:73]
	v_mfma_i32_16x16x64_i8 v[66:69], v[154:157], v[204:207], v[66:69]
	ds_read_b128 v[146:149], v142 offset:4096
	ds_read_b128 v[154:157], v142 offset:6144
	s_waitcnt lgkmcnt(0)
	s_barrier
	v_mfma_i32_16x16x64_i8 v[62:65], v[146:149], v[150:153], v[62:65]
	v_mfma_i32_16x16x64_i8 v[58:61], v[146:149], v[158:161], v[58:61]
	v_mfma_i32_16x16x64_i8 v[54:57], v[146:149], v[170:173], v[54:57]
	v_mfma_i32_16x16x64_i8 v[50:53], v[146:149], v[174:177], v[50:53]
	v_mfma_i32_16x16x64_i8 v[46:49], v[146:149], v[178:181], v[46:49]
	v_mfma_i32_16x16x64_i8 v[42:45], v[146:149], v[196:199], v[42:45]
	v_mfma_i32_16x16x64_i8 v[38:41], v[146:149], v[200:203], v[38:41]
	v_mfma_i32_16x16x64_i8 v[34:37], v[146:149], v[204:207], v[34:37]
	v_mfma_i32_16x16x64_i8 v[30:33], v[154:157], v[150:153], v[30:33]
	v_mfma_i32_16x16x64_i8 v[26:29], v[154:157], v[158:161], v[26:29]
	v_mfma_i32_16x16x64_i8 v[22:25], v[154:157], v[170:173], v[22:25]
	v_mfma_i32_16x16x64_i8 v[18:21], v[154:157], v[174:177], v[18:21]
	v_mfma_i32_16x16x64_i8 v[10:13], v[154:157], v[178:181], v[10:13]
	v_mfma_i32_16x16x64_i8 v[6:9], v[154:157], v[196:199], v[6:9]
	v_mfma_i32_16x16x64_i8 v[2:5], v[154:157], v[200:203], v[2:5]
	v_mfma_i32_16x16x64_i8 v[14:17], v[154:157], v[204:207], v[14:17]
	s_cbranch_scc1 .LBB0_564
	v_add_u32_e32 v138, s9, v145
	v_ashrrev_i32_e32 v139, 31, v138
	v_lshl_add_u64 v[140:141], v[138:139], 2, s[24:25]
	v_or_b32_e32 v136, s12, v165
	v_lshl_add_u64 v[148:149], v[136:137], 2, s[26:27]
	v_cvt_f32_i32_e32 v147, v126
	v_cvt_f32_i32_e32 v156, v127
	v_cvt_f32_i32_e32 v157, v128
	v_cvt_f32_i32_e32 v160, v124
	v_cvt_f32_i32_e32 v161, v125
	v_cvt_f32_i32_e32 v162, v118
	v_cvt_f32_i32_e32 v170, v120
	v_or_b32_e32 v118, 1, v138
	v_or_b32_e32 v120, 2, v138
	v_cvt_f32_i32_e32 v163, v119
	v_cvt_f32_i32_e32 v171, v121
	v_ashrrev_i32_e32 v119, 31, v118
	v_ashrrev_i32_e32 v121, 31, v120
	v_lshlrev_b64 v[148:149], 11, v[118:119]
	v_lshlrev_b64 v[154:155], 11, v[120:121]
	v_cvt_f32_i32_e32 v98, v98
	v_cvt_f32_i32_e32 v129, v129
	v_cvt_f32_i32_e32 v158, v122
	v_cvt_f32_i32_e32 v159, v123
	v_cvt_f32_i32_e32 v106, v106
	v_cvt_f32_i32_e32 v99, v99
	v_cvt_f32_i32_e32 v107, v107
	v_cvt_f32_i32_e32 v102, v102
	v_cvt_f32_i32_e32 v100, v100
	v_cvt_f32_i32_e32 v108, v108
	v_cvt_f32_i32_e32 v103, v103
	v_cvt_f32_i32_e32 v101, v101
	v_or_b32_e32 v150, 3, v138
	v_lshl_add_u64 v[122:123], v[136:137], 1, s[38:39]
	v_cvt_f32_i32_e32 v109, v109
	v_cvt_f32_i32_e32 v104, v104
	v_lshlrev_b64 v[152:153], 11, v[138:139]
	v_ashrrev_i32_e32 v151, 31, v150
	v_cvt_f32_i32_e32 v105, v105
	v_lshlrev_b64 v[150:151], 11, v[150:151]
	v_lshl_add_u64 v[152:153], v[122:123], 0, v[152:153]
	v_cvt_f32_i32_e32 v95, v95
	v_lshl_add_u64 v[148:149], v[122:123], 0, v[148:149]
	v_lshl_add_u64 v[154:155], v[122:123], 0, v[154:155]
	v_lshl_add_u64 v[150:151], v[122:123], 0, v[150:151]
	v_cvt_f32_i32_e32 v94, v94
	v_cvt_f32_i32_e32 v96, v96
	v_cvt_f32_i32_e32 v82, v82
	v_cvt_f32_i32_e32 v66, v66
	v_cvt_f32_i32_e32 v97, v97
	v_cvt_f32_i32_e32 v83, v83
	v_cvt_f32_i32_e32 v67, v67
	v_cvt_f32_i32_e32 v84, v84
	v_cvt_f32_i32_e32 v70, v70
	v_cvt_f32_i32_e32 v68, v68
	v_cvt_f32_i32_e32 v85, v85
	v_cvt_f32_i32_e32 v78, v78
	v_cvt_f32_i32_e32 v71, v71
	v_cvt_f32_i32_e32 v69, v69
	v_cvt_f32_i32_e32 v79, v79
	v_cvt_f32_i32_e32 v72, v72
	v_cvt_f32_i32_e32 v80, v80
	v_cvt_f32_i32_e32 v73, v73
	v_cvt_f32_i32_e32 v81, v81
	v_cvt_f32_i32_e32 v74, v74
	v_cvt_f32_i32_e32 v75, v75
	v_cvt_f32_i32_e32 v76, v76
	v_cvt_f32_i32_e32 v77, v77
	v_cvt_f32_i32_e32 v63, v63
	v_cvt_f32_i32_e32 v62, v62
	v_cvt_f32_i32_e32 v64, v64
	v_cvt_f32_i32_e32 v34, v34
	v_cvt_f32_i32_e32 v65, v65
	v_cvt_f32_i32_e32 v42, v42
	v_cvt_f32_i32_e32 v35, v35
	v_cvt_f32_i32_e32 v43, v43
	v_cvt_f32_i32_e32 v38, v38
	v_cvt_f32_i32_e32 v36, v36
	v_cvt_f32_i32_e32 v44, v44
	v_mul_f32_e32 v136, v208, v147
	v_mul_f32_e32 v98, v208, v98
	v_mul_f32_e32 v139, v209, v156
	v_mul_f32_e32 v147, v210, v157
	v_mul_f32_e32 v129, v211, v129
	v_mul_f32_e32 v156, v208, v158
	v_mul_f32_e32 v157, v209, v159
	v_mul_f32_e32 v158, v210, v160
	v_mul_f32_e32 v159, v211, v161
	v_mul_f32_e32 v160, v208, v162
	v_mul_f32_e32 v161, v209, v163
	v_mul_f32_e32 v162, v210, v170
	v_mul_f32_e32 v136, v136, v224
	v_mul_f32_e32 v106, v208, v106
	v_mul_f32_e32 v98, v98, v238
	v_mul_f32_e32 v99, v209, v99
	v_mul_f32_e32 v139, v139, v224
	v_mul_f32_e32 v147, v147, v224
	v_mul_f32_e32 v129, v224, v129
	v_mul_f32_e32 v156, v156, v226
	v_mul_f32_e32 v157, v157, v226
; template <bool I8, class Epi> ...
;     ...
;   for (int i = 0; i < 4; ++i) {
;     const int row = m0 + wm * 64 + i * 16 + (lane >> 4) * 4;
;     float4 rs = float4{1.f, 1.f, 1.f, 1.f};
;     if (I8) rs = *reinterpret_cast<const float4*>(rscale + row);
; #pragma unroll
;     for (int j = 0; j < 8; ++j) {
;       const int col = n0 + wn * 128 + j * 16 + (lane & 15);
;       if (I8) {
;         typedef __attribute__((ext_vector_type(4))) int i32x4;
;         const i32x4 ia = __builtin_bit_cast(i32x4, acc[i][j]);
;         const float cs = cscale[col];
;         epi(row, col, f32x4{(float)ia[0] * rs.x * cs, (float)ia[1] * rs.y * cs, (float)ia[2] * rs.z * cs, (float)ia[3] * rs.w * cs});
;       } else {
;         epi(row, col, acc[i][j]);
;       }
;     }
;   }
;   __device__ __forceinline__ void operator()(int row, int col, f32x4 v) const {
; #pragma unroll
;     for (int r = 0; r < 4; ++r) z[(size_t)(row + r) * 1024 + (col - 2048)] = f2bf(v[r]);
;   }
	v_mul_f32_e32 v158, v158, v226
	v_mul_f32_e32 v159, v159, v226
	v_mul_f32_e32 v160, v160, v228
	v_mul_f32_e32 v161, v161, v228
	v_mul_f32_e32 v162, v162, v228
	v_cvt_pk_bf16_f32 v136, v136, s0
	v_mul_f32_e32 v106, v106, v234
	v_mul_f32_e32 v107, v209, v107
	v_mul_f32_e32 v102, v208, v102
	v_mul_f32_e32 v99, v99, v238
	v_mul_f32_e32 v100, v210, v100
	v_cvt_pk_bf16_f32 v98, v98, s0
	v_cvt_pk_bf16_f32 v139, v139, s0
	v_cvt_pk_bf16_f32 v147, v147, s0
	v_cvt_pk_bf16_f32 v129, v129, s0
	v_cvt_pk_bf16_f32 v156, v156, s0
	v_cvt_pk_bf16_f32 v157, v157, s0
	v_cvt_pk_bf16_f32 v158, v158, s0
	v_cvt_pk_bf16_f32 v159, v159, s0
	v_cvt_pk_bf16_f32 v160, v160, s0
	v_cvt_pk_bf16_f32 v161, v161, s0
	v_cvt_pk_bf16_f32 v162, v162, s0
	global_store_short v[152:153], v136, off offset:-4096
	global_store_short v[148:149], v139, off offset:-4096
	global_store_short v[154:155], v147, off offset:-4096
	global_store_short v[150:151], v129, off offset:-4096
	global_store_short v[152:153], v156, off offset:-4064
	global_store_short v[148:149], v157, off offset:-4064
	global_store_short v[154:155], v158, off offset:-4064
	global_store_short v[150:151], v159, off offset:-4064
	global_store_short v[152:153], v160, off offset:-4032
	global_store_short v[148:149], v161, off offset:-4032
	global_store_short v[154:155], v162, off offset:-4032
	v_mul_f32_e32 v107, v107, v234
	v_mul_f32_e32 v108, v210, v108
	v_cvt_pk_bf16_f32 v106, v106, s0
	v_mul_f32_e32 v102, v102, v236
	v_mul_f32_e32 v103, v209, v103
	v_mul_f32_e32 v100, v100, v238
	v_mul_f32_e32 v101, v211, v101
	global_store_short v[152:153], v98, off offset:-3872
	v_cvt_pk_bf16_f32 v98, v99, s0
	v_mul_f32_e32 v108, v108, v234
	v_mul_f32_e32 v109, v211, v109
	global_store_short v[152:153], v106, off offset:-3936
	v_cvt_pk_bf16_f32 v106, v107, s0
	v_mul_f32_e32 v103, v103, v236
	v_mul_f32_e32 v104, v210, v104
	v_cvt_pk_bf16_f32 v102, v102, s0
	v_mul_f32_e32 v101, v101, v238
	global_store_short v[148:149], v98, off offset:-3872
	v_cvt_pk_bf16_f32 v98, v100, s0
	v_mul_f32_e32 v109, v109, v234
	global_store_short v[148:149], v106, off offset:-3936
	v_cvt_pk_bf16_f32 v106, v108, s0
	v_mul_f32_e32 v104, v104, v236
	v_mul_f32_e32 v105, v211, v105
	global_store_short v[152:153], v102, off offset:-3904
	v_cvt_pk_bf16_f32 v102, v103, s0
	global_store_short v[154:155], v98, off offset:-3872
	v_cvt_pk_bf16_f32 v98, v101, s0
	global_store_short v[154:155], v106, off offset:-3936
	v_cvt_pk_bf16_f32 v106, v109, s0
	v_mul_f32_e32 v105, v105, v236
	global_store_short v[148:149], v102, off offset:-3904
	v_cvt_pk_bf16_f32 v102, v104, s0
	global_store_short v[150:151], v98, off offset:-3872
	v_or_b32_e32 v98, 16, v138
	v_mul_f32_e32 v95, v213, v95
	global_store_short v[150:151], v106, off offset:-3936
	global_store_short v[154:155], v102, off offset:-3904
	v_cvt_pk_bf16_f32 v102, v105, s0
	v_ashrrev_i32_e32 v99, 31, v98
	v_or_b32_e32 v100, 17, v138
	v_mul_f32_e32 v94, v212, v94
	v_mul_f32_e32 v106, v224, v95
	v_mul_f32_e32 v95, v214, v96
	v_mul_f32_e32 v82, v212, v82
	v_mul_f32_e32 v66, v212, v66
	global_store_short v[150:151], v102, off offset:-3904
	v_lshlrev_b64 v[98:99], 11, v[98:99]
	v_ashrrev_i32_e32 v101, 31, v100
	v_or_b32_e32 v102, 18, v138
	v_mul_f32_e32 v94, v224, v94
	v_mul_f32_e32 v107, v224, v95
	v_mul_f32_e32 v95, v215, v97
	v_mul_f32_e32 v82, v230, v82
	v_mul_f32_e32 v83, v213, v83
	v_mul_f32_e32 v66, v238, v66
	v_mul_f32_e32 v67, v213, v67
	v_lshlrev_b64 v[100:101], 11, v[100:101]
	v_ashrrev_i32_e32 v103, 31, v102
	v_or_b32_e32 v104, 19, v138
	v_mul_f32_e32 v108, v224, v95
	v_cvt_pk_bf16_f32 v96, v94, s0
	v_lshl_add_u64 v[94:95], v[122:123], 0, v[98:99]
	v_mul_f32_e32 v83, v230, v83
	v_mul_f32_e32 v84, v214, v84
	v_cvt_pk_bf16_f32 v82, v82, s0
	v_mul_f32_e32 v70, v212, v70
	v_mul_f32_e32 v67, v238, v67
	v_mul_f32_e32 v68, v214, v68
	v_cvt_pk_bf16_f32 v66, v66, s0
	v_lshlrev_b64 v[102:103], 11, v[102:103]
	v_ashrrev_i32_e32 v105, 31, v104
	global_store_short v[94:95], v96, off offset:-4096
	v_cvt_pk_bf16_f32 v98, v106, s0
	v_lshl_add_u64 v[96:97], v[122:123], 0, v[100:101]
	v_mul_f32_e32 v84, v230, v84
	v_mul_f32_e32 v85, v215, v85
	global_store_short v[94:95], v82, off offset:-4000
	v_cvt_pk_bf16_f32 v82, v83, s0
	v_mul_f32_e32 v78, v212, v78
	v_mul_f32_e32 v70, v236, v70
	v_mul_f32_e32 v71, v213, v71
	v_mul_f32_e32 v68, v238, v68
	v_mul_f32_e32 v69, v215, v69
	global_store_short v[94:95], v66, off offset:-3872
	v_cvt_pk_bf16_f32 v66, v67, s0
	v_lshlrev_b64 v[104:105], 11, v[104:105]
	global_store_short v[96:97], v98, off offset:-4096
	v_cvt_pk_bf16_f32 v100, v107, s0
	v_lshl_add_u64 v[98:99], v[122:123], 0, v[102:103]
	v_mul_f32_e32 v85, v230, v85
	global_store_short v[96:97], v82, off offset:-4000
	v_cvt_pk_bf16_f32 v82, v84, s0
	v_mul_f32_e32 v78, v232, v78
	v_mul_f32_e32 v79, v213, v79
	v_mul_f32_e32 v71, v236, v71
	v_mul_f32_e32 v72, v214, v72
	v_cvt_pk_bf16_f32 v70, v70, s0
	v_mul_f32_e32 v69, v238, v69
	global_store_short v[96:97], v66, off offset:-3872
	v_cvt_pk_bf16_f32 v66, v68, s0
	global_store_short v[98:99], v100, off offset:-4096
	v_lshl_add_u64 v[100:101], v[122:123], 0, v[104:105]
	global_store_short v[98:99], v82, off offset:-4000
	v_cvt_pk_bf16_f32 v82, v85, s0
	v_mul_f32_e32 v79, v232, v79
	v_mul_f32_e32 v80, v214, v80
	v_cvt_pk_bf16_f32 v78, v78, s0
	v_mul_f32_e32 v72, v236, v72
	v_mul_f32_e32 v73, v215, v73
	global_store_short v[94:95], v70, off offset:-3904
	v_cvt_pk_bf16_f32 v70, v71, s0
	global_store_short v[98:99], v66, off offset:-3872
	v_cvt_pk_bf16_f32 v66, v69, s0
	global_store_short v[100:101], v82, off offset:-4000
	v_mul_f32_e32 v82, v232, v80
	v_mul_f32_e32 v80, v215, v81
; template <bool I8, class Epi> ...
;     ...
;   for (int i = 0; i < 4; ++i) {
;     const int row = m0 + wm * 64 + i * 16 + (lane >> 4) * 4;
;     float4 rs = float4{1.f, 1.f, 1.f, 1.f};
;     if (I8) rs = *reinterpret_cast<const float4*>(rscale + row);
; #pragma unroll
;     for (int j = 0; j < 8; ++j) {
;       const int col = n0 + wn * 128 + j * 16 + (lane & 15);
;       if (I8) {
;         typedef __attribute__((ext_vector_type(4))) int i32x4;
;         const i32x4 ia = __builtin_bit_cast(i32x4, acc[i][j]);
;         const float cs = cscale[col];
;         epi(row, col, f32x4{(float)ia[0] * rs.x * cs, (float)ia[1] * rs.y * cs, (float)ia[2] * rs.z * cs, (float)ia[3] * rs.w * cs});
;       } else {
;         epi(row, col, acc[i][j]);
;       }
;     }
;   }
;   __device__ __forceinline__ void operator()(int row, int col, f32x4 v) const {
; #pragma unroll
;     for (int r = 0; r < 4; ++r) z[(size_t)(row + r) * 1024 + (col - 2048)] = f2bf(v[r]);
;   }
	global_store_short v[94:95], v78, off offset:-3968
	v_cvt_pk_bf16_f32 v78, v79, s0
	v_mul_f32_e32 v74, v212, v74
	v_mul_f32_e32 v73, v236, v73
	global_store_short v[96:97], v70, off offset:-3904
	v_cvt_pk_bf16_f32 v70, v72, s0
	global_store_short v[100:101], v66, off offset:-3872
	v_or_b32_e32 v66, 32, v138
	v_mul_f32_e32 v83, v232, v80
	global_store_short v[96:97], v78, off offset:-3968
	v_mul_f32_e32 v74, v234, v74
	v_mul_f32_e32 v75, v213, v75
	global_store_short v[98:99], v70, off offset:-3904
	v_cvt_pk_bf16_f32 v70, v73, s0
	v_ashrrev_i32_e32 v67, 31, v66
	v_mul_f32_e32 v75, v234, v75
	v_mul_f32_e32 v76, v214, v76
	v_cvt_pk_bf16_f32 v74, v74, s0
	global_store_short v[100:101], v70, off offset:-3904
	v_lshlrev_b64 v[70:71], 11, v[66:67]
	v_or_b32_e32 v66, 33, v138
	v_mul_f32_e32 v76, v234, v76
	v_mul_f32_e32 v77, v215, v77
	global_store_short v[94:95], v74, off offset:-3936
	v_cvt_pk_bf16_f32 v74, v75, s0
	v_ashrrev_i32_e32 v67, 31, v66
	v_mul_f32_e32 v77, v234, v77
	global_store_short v[96:97], v74, off offset:-3936
	v_cvt_pk_bf16_f32 v74, v76, s0
	v_lshlrev_b64 v[72:73], 11, v[66:67]
	v_or_b32_e32 v66, 34, v138
	global_store_short v[98:99], v74, off offset:-3936
	v_cvt_pk_bf16_f32 v74, v77, s0
	v_ashrrev_i32_e32 v67, 31, v66
	global_store_short v[100:101], v74, off offset:-3936
	v_lshlrev_b64 v[74:75], 11, v[66:67]
	v_or_b32_e32 v66, 35, v138
	v_ashrrev_i32_e32 v67, 31, v66
	v_lshlrev_b64 v[76:77], 11, v[66:67]
	v_cvt_pk_bf16_f32 v82, v82, s0
	global_store_short v[98:99], v82, off offset:-3968
	v_cvt_pk_bf16_f32 v82, v83, s0
	v_cvt_f32_i32_e32 v39, v39
	v_cvt_f32_i32_e32 v37, v37
	global_store_short v[100:101], v82, off offset:-3968
	v_cvt_f32_i32_e32 v45, v45
	v_cvt_f32_i32_e32 v40, v40
	v_cvt_f32_i32_e32 v41, v41
	v_cvt_f32_i32_e32 v31, v31
	v_cvt_f32_i32_e32 v30, v30
	v_cvt_f32_i32_e32 v32, v32
	v_cvt_f32_i32_e32 v2, v2
	v_cvt_f32_i32_e32 v33, v33
	v_cvt_f32_i32_e32 v3, v3
	v_cvt_f32_i32_e32 v4, v4
	v_cvt_f32_i32_e32 v5, v5
	v_cvt_f32_i32_e32 v114, v114
	v_cvt_f32_i32_e32 v110, v110
	v_cvt_f32_i32_e32 v90, v90
	v_cvt_f32_i32_e32 v86, v86
	v_cvt_f32_i32_e32 v58, v58
	v_cvt_f32_i32_e32 v54, v54
	v_cvt_f32_i32_e32 v50, v50
	v_cvt_f32_i32_e32 v46, v46
	v_cvt_f32_i32_e32 v26, v26
	v_cvt_f32_i32_e32 v22, v22
	v_cvt_f32_i32_e32 v18, v18
	v_cvt_f32_i32_e32 v10, v10
	v_cvt_f32_i32_e32 v6, v6
	v_cvt_f32_i32_e32 v115, v115
	v_cvt_f32_i32_e32 v111, v111
	v_cvt_f32_i32_e32 v91, v91
	v_cvt_f32_i32_e32 v87, v87
	v_cvt_f32_i32_e32 v59, v59
	v_cvt_f32_i32_e32 v55, v55
	v_cvt_f32_i32_e32 v51, v51
	v_cvt_f32_i32_e32 v47, v47
	v_cvt_f32_i32_e32 v27, v27
	v_cvt_f32_i32_e32 v23, v23
	v_cvt_f32_i32_e32 v19, v19
	v_cvt_f32_i32_e32 v11, v11
	v_cvt_f32_i32_e32 v7, v7
	v_cvt_f32_i32_e32 v116, v116
	v_cvt_f32_i32_e32 v112, v112
	v_cvt_f32_i32_e32 v92, v92
	v_cvt_f32_i32_e32 v88, v88
	v_cvt_f32_i32_e32 v60, v60
	v_cvt_f32_i32_e32 v56, v56
	v_mul_f32_e32 v63, v217, v63
	v_mul_f32_e32 v62, v216, v62
	v_mul_f32_e32 v82, v224, v63
	v_mul_f32_e32 v63, v218, v64
	v_mul_f32_e32 v34, v216, v34
	v_mul_f32_e32 v62, v224, v62
	v_mul_f32_e32 v83, v224, v63
	v_mul_f32_e32 v63, v219, v65
	v_mul_f32_e32 v42, v216, v42
	v_mul_f32_e32 v34, v238, v34
	v_mul_f32_e32 v35, v217, v35
	v_mul_f32_e32 v84, v224, v63
	v_cvt_pk_bf16_f32 v64, v62, s0
	v_lshl_add_u64 v[62:63], v[122:123], 0, v[70:71]
	v_mul_f32_e32 v42, v234, v42
	v_mul_f32_e32 v43, v217, v43
	v_mul_f32_e32 v38, v216, v38
	v_mul_f32_e32 v35, v238, v35
	v_mul_f32_e32 v36, v218, v36
	v_cvt_pk_bf16_f32 v34, v34, s0
	global_store_short v[62:63], v64, off offset:-4096
	v_cvt_pk_bf16_f32 v70, v82, s0
	v_lshl_add_u64 v[64:65], v[122:123], 0, v[72:73]
	v_mul_f32_e32 v43, v234, v43
	v_mul_f32_e32 v44, v218, v44
	v_cvt_pk_bf16_f32 v42, v42, s0
	v_mul_f32_e32 v38, v236, v38
	v_mul_f32_e32 v39, v217, v39
	v_mul_f32_e32 v36, v238, v36
	v_mul_f32_e32 v37, v219, v37
	global_store_short v[62:63], v34, off offset:-3872
	v_cvt_pk_bf16_f32 v34, v35, s0
	global_store_short v[64:65], v70, off offset:-4096
	v_cvt_pk_bf16_f32 v72, v83, s0
	v_lshl_add_u64 v[70:71], v[122:123], 0, v[74:75]
	v_mul_f32_e32 v44, v234, v44
	v_mul_f32_e32 v45, v219, v45
	global_store_short v[62:63], v42, off offset:-3936
	v_cvt_pk_bf16_f32 v42, v43, s0
	v_mul_f32_e32 v39, v236, v39
	v_mul_f32_e32 v40, v218, v40
	v_cvt_pk_bf16_f32 v38, v38, s0
	v_mul_f32_e32 v37, v238, v37
	global_store_short v[64:65], v34, off offset:-3872
	v_cvt_pk_bf16_f32 v34, v36, s0
	global_store_short v[70:71], v72, off offset:-4096
	v_lshl_add_u64 v[72:73], v[122:123], 0, v[76:77]
	v_mul_f32_e32 v45, v234, v45
	global_store_short v[64:65], v42, off offset:-3936
	v_cvt_pk_bf16_f32 v42, v44, s0
	v_mul_f32_e32 v40, v236, v40
	v_mul_f32_e32 v41, v219, v41
	global_store_short v[62:63], v38, off offset:-3904
	v_cvt_pk_bf16_f32 v38, v39, s0
	global_store_short v[70:71], v34, off offset:-3872
	v_cvt_pk_bf16_f32 v34, v37, s0
	global_store_short v[70:71], v42, off offset:-3936
	v_cvt_pk_bf16_f32 v42, v45, s0
	v_mul_f32_e32 v41, v236, v41
	global_store_short v[64:65], v38, off offset:-3904
	v_cvt_pk_bf16_f32 v38, v40, s0
	global_store_short v[72:73], v34, off offset:-3872
	v_or_b32_e32 v34, 48, v138
	v_mul_f32_e32 v31, v221, v31
	global_store_short v[72:73], v42, off offset:-3936
	global_store_short v[70:71], v38, off offset:-3904
	v_cvt_pk_bf16_f32 v38, v41, s0
	v_ashrrev_i32_e32 v35, 31, v34
	v_or_b32_e32 v36, 49, v138
	v_mul_f32_e32 v30, v220, v30
	v_mul_f32_e32 v42, v224, v31
	v_mul_f32_e32 v31, v222, v32
	v_mul_f32_e32 v2, v220, v2
	global_store_short v[72:73], v38, off offset:-3904
	v_lshlrev_b64 v[34:35], 11, v[34:35]
	v_ashrrev_i32_e32 v37, 31, v36
	v_or_b32_e32 v38, 50, v138
; template <bool I8, class Epi> ...
;     ...
;   for (int i = 0; i < 4; ++i) {
;     const int row = m0 + wm * 64 + i * 16 + (lane >> 4) * 4;
;     float4 rs = float4{1.f, 1.f, 1.f, 1.f};
;     if (I8) rs = *reinterpret_cast<const float4*>(rscale + row);
; #pragma unroll
;     for (int j = 0; j < 8; ++j) {
;       const int col = n0 + wn * 128 + j * 16 + (lane & 15);
;       if (I8) {
;         typedef __attribute__((ext_vector_type(4))) int i32x4;
;         const i32x4 ia = __builtin_bit_cast(i32x4, acc[i][j]);
;         const float cs = cscale[col];
;         epi(row, col, f32x4{(float)ia[0] * rs.x * cs, (float)ia[1] * rs.y * cs, (float)ia[2] * rs.z * cs, (float)ia[3] * rs.w * cs});
;       } else {
;         epi(row, col, acc[i][j]);
;       }
;     }
;   }
;   __device__ __forceinline__ void operator()(int row, int col, f32x4 v) const {
; #pragma unroll
;     for (int r = 0; r < 4; ++r) z[(size_t)(row + r) * 1024 + (col - 2048)] = f2bf(v[r]);
;   }
	v_mul_f32_e32 v30, v224, v30
	v_mul_f32_e32 v43, v224, v31
	v_mul_f32_e32 v31, v223, v33
	v_mul_f32_e32 v2, v236, v2
	v_mul_f32_e32 v3, v221, v3
	v_lshlrev_b64 v[36:37], 11, v[36:37]
	v_ashrrev_i32_e32 v39, 31, v38
	v_or_b32_e32 v40, 51, v138
	v_mul_f32_e32 v44, v224, v31
	v_cvt_pk_bf16_f32 v32, v30, s0
	v_lshl_add_u64 v[30:31], v[122:123], 0, v[34:35]
	v_mul_f32_e32 v3, v236, v3
	v_mul_f32_e32 v4, v222, v4
	v_cvt_pk_bf16_f32 v2, v2, s0
	v_lshlrev_b64 v[38:39], 11, v[38:39]
	v_ashrrev_i32_e32 v41, 31, v40
	global_store_short v[30:31], v32, off offset:-4096
	v_cvt_pk_bf16_f32 v34, v42, s0
	v_lshl_add_u64 v[32:33], v[122:123], 0, v[36:37]
	v_mul_f32_e32 v4, v236, v4
	v_mul_f32_e32 v5, v223, v5
	global_store_short v[30:31], v2, off offset:-3904
	v_cvt_pk_bf16_f32 v2, v3, s0
	v_lshlrev_b64 v[40:41], 11, v[40:41]
	global_store_short v[32:33], v34, off offset:-4096
	v_cvt_pk_bf16_f32 v36, v43, s0
	v_lshl_add_u64 v[34:35], v[122:123], 0, v[38:39]
	v_mul_f32_e32 v5, v236, v5
	global_store_short v[32:33], v2, off offset:-3904
	v_cvt_pk_bf16_f32 v2, v4, s0
	global_store_short v[34:35], v36, off offset:-4096
	v_lshl_add_u64 v[36:37], v[122:123], 0, v[40:41]
	global_store_short v[34:35], v2, off offset:-3904
	v_cvt_f32_i32_e32 v2, v14
	v_cvt_pk_bf16_f32 v3, v5, s0
	global_store_short v[36:37], v3, off offset:-3904
	v_cvt_f32_i32_e32 v3, v15
	v_cvt_f32_i32_e32 v52, v52
	v_cvt_f32_i32_e32 v48, v48
	v_cvt_f32_i32_e32 v28, v28
	v_cvt_f32_i32_e32 v24, v24
	v_cvt_f32_i32_e32 v20, v20
	v_cvt_f32_i32_e32 v12, v12
	v_cvt_f32_i32_e32 v8, v8
	v_cvt_f32_i32_e32 v4, v16
	v_cvt_f32_i32_e32 v117, v117
	v_cvt_f32_i32_e32 v113, v113
	v_cvt_f32_i32_e32 v93, v93
	v_cvt_f32_i32_e32 v89, v89
	v_cvt_f32_i32_e32 v61, v61
	v_cvt_f32_i32_e32 v57, v57
	v_cvt_f32_i32_e32 v53, v53
	v_cvt_f32_i32_e32 v49, v49
	v_cvt_f32_i32_e32 v29, v29
	v_cvt_f32_i32_e32 v25, v25
	v_cvt_f32_i32_e32 v21, v21
	v_cvt_f32_i32_e32 v13, v13
	v_cvt_f32_i32_e32 v9, v9
	v_cvt_f32_i32_e32 v5, v17
	v_mul_f32_e32 v114, v208, v114
	v_mul_f32_e32 v110, v208, v110
	v_mul_f32_e32 v90, v212, v90
	v_mul_f32_e32 v86, v212, v86
	v_mul_f32_e32 v58, v216, v58
	v_mul_f32_e32 v54, v216, v54
	v_mul_f32_e32 v50, v216, v50
	v_mul_f32_e32 v46, v216, v46
	v_mul_f32_e32 v26, v220, v26
	v_mul_f32_e32 v22, v220, v22
	v_mul_f32_e32 v18, v220, v18
	v_mul_f32_e32 v10, v220, v10
	v_mul_f32_e32 v6, v220, v6
	v_mul_f32_e32 v2, v220, v2
	v_mul_f32_e32 v114, v114, v230
	v_mul_f32_e32 v115, v209, v115
	v_mul_f32_e32 v110, v110, v232
	v_mul_f32_e32 v111, v209, v111
	v_mul_f32_e32 v90, v226, v90
	v_mul_f32_e32 v91, v213, v91
	v_mul_f32_e32 v86, v228, v86
	v_mul_f32_e32 v87, v213, v87
	v_mul_f32_e32 v58, v226, v58
	v_mul_f32_e32 v59, v217, v59
	v_mul_f32_e32 v54, v228, v54
	v_mul_f32_e32 v55, v217, v55
	v_mul_f32_e32 v50, v230, v50
	v_mul_f32_e32 v51, v217, v51
	v_mul_f32_e32 v46, v232, v46
	v_mul_f32_e32 v47, v217, v47
	v_mul_f32_e32 v26, v226, v26
	v_mul_f32_e32 v27, v221, v27
	v_mul_f32_e32 v22, v228, v22
	v_mul_f32_e32 v23, v221, v23
	v_mul_f32_e32 v18, v230, v18
	v_mul_f32_e32 v19, v221, v19
	v_mul_f32_e32 v10, v232, v10
	v_mul_f32_e32 v11, v221, v11
	v_mul_f32_e32 v6, v234, v6
	v_mul_f32_e32 v7, v221, v7
	v_mul_f32_e32 v2, v238, v2
	v_mul_f32_e32 v3, v221, v3
	v_mul_f32_e32 v115, v115, v230
	v_mul_f32_e32 v116, v210, v116
	v_cvt_pk_bf16_f32 v114, v114, s0
	v_mul_f32_e32 v111, v111, v232
	v_mul_f32_e32 v112, v210, v112
	v_cvt_pk_bf16_f32 v110, v110, s0
	v_mul_f32_e32 v91, v226, v91
	v_mul_f32_e32 v92, v214, v92
	v_cvt_pk_bf16_f32 v90, v90, s0
	v_mul_f32_e32 v87, v228, v87
	v_mul_f32_e32 v88, v214, v88
	v_cvt_pk_bf16_f32 v86, v86, s0
	v_mul_f32_e32 v59, v226, v59
	v_mul_f32_e32 v60, v218, v60
	v_cvt_pk_bf16_f32 v58, v58, s0
	v_mul_f32_e32 v55, v228, v55
	v_mul_f32_e32 v56, v218, v56
	v_cvt_pk_bf16_f32 v54, v54, s0
	v_mul_f32_e32 v51, v230, v51
	v_mul_f32_e32 v52, v218, v52
	v_cvt_pk_bf16_f32 v50, v50, s0
	v_mul_f32_e32 v47, v232, v47
	v_mul_f32_e32 v48, v218, v48
	v_cvt_pk_bf16_f32 v46, v46, s0
	v_mul_f32_e32 v27, v226, v27
	v_mul_f32_e32 v28, v222, v28
	v_cvt_pk_bf16_f32 v26, v26, s0
	v_mul_f32_e32 v23, v228, v23
	v_mul_f32_e32 v24, v222, v24
	v_cvt_pk_bf16_f32 v22, v22, s0
	v_mul_f32_e32 v19, v230, v19
	v_mul_f32_e32 v20, v222, v20
	v_cvt_pk_bf16_f32 v18, v18, s0
	v_mul_f32_e32 v11, v232, v11
	v_mul_f32_e32 v12, v222, v12
	v_cvt_pk_bf16_f32 v10, v10, s0
	v_mul_f32_e32 v7, v234, v7
	v_mul_f32_e32 v8, v222, v8
	v_cvt_pk_bf16_f32 v6, v6, s0
	v_mul_f32_e32 v3, v238, v3
	v_mul_f32_e32 v4, v222, v4
	v_cvt_pk_bf16_f32 v2, v2, s0
	v_mul_f32_e32 v163, v211, v171
	v_mul_f32_e32 v116, v116, v230
	v_mul_f32_e32 v117, v211, v117
	global_store_short v[152:153], v114, off offset:-4000
	v_cvt_pk_bf16_f32 v114, v115, s0
	v_mul_f32_e32 v112, v112, v232
	v_mul_f32_e32 v113, v211, v113
	global_store_short v[152:153], v110, off offset:-3968
	v_cvt_pk_bf16_f32 v110, v111, s0
	v_mul_f32_e32 v92, v226, v92
	v_mul_f32_e32 v93, v215, v93
	global_store_short v[94:95], v90, off offset:-4064
	v_cvt_pk_bf16_f32 v90, v91, s0
	v_mul_f32_e32 v88, v228, v88
	v_mul_f32_e32 v89, v215, v89
	global_store_short v[94:95], v86, off offset:-4032
	v_cvt_pk_bf16_f32 v86, v87, s0
	v_mul_f32_e32 v60, v226, v60
	v_mul_f32_e32 v61, v219, v61
	global_store_short v[62:63], v58, off offset:-4064
; template <bool I8, class Epi> ...
;     ...
;   for (int i = 0; i < 4; ++i) {
;     const int row = m0 + wm * 64 + i * 16 + (lane >> 4) * 4;
;     float4 rs = float4{1.f, 1.f, 1.f, 1.f};
;     if (I8) rs = *reinterpret_cast<const float4*>(rscale + row);
; #pragma unroll
;     for (int j = 0; j < 8; ++j) {
;       const int col = n0 + wn * 128 + j * 16 + (lane & 15);
;       if (I8) {
;         typedef __attribute__((ext_vector_type(4))) int i32x4;
;         const i32x4 ia = __builtin_bit_cast(i32x4, acc[i][j]);
;         const float cs = cscale[col];
;         epi(row, col, f32x4{(float)ia[0] * rs.x * cs, (float)ia[1] * rs.y * cs, (float)ia[2] * rs.z * cs, (float)ia[3] * rs.w * cs});
;       } else {
;         epi(row, col, acc[i][j]);
;       }
;     }
;   }
;   __device__ __forceinline__ void operator()(int row, int col, f32x4 v) const {
; #pragma unroll
;     for (int r = 0; r < 4; ++r) z[(size_t)(row + r) * 1024 + (col - 2048)] = f2bf(v[r]);
;   }
	v_cvt_pk_bf16_f32 v58, v59, s0
	v_mul_f32_e32 v56, v228, v56
	v_mul_f32_e32 v57, v219, v57
	global_store_short v[62:63], v54, off offset:-4032
	v_cvt_pk_bf16_f32 v54, v55, s0
	v_mul_f32_e32 v52, v230, v52
	v_mul_f32_e32 v53, v219, v53
	global_store_short v[62:63], v50, off offset:-4000
	v_cvt_pk_bf16_f32 v50, v51, s0
	v_mul_f32_e32 v48, v232, v48
	v_mul_f32_e32 v49, v219, v49
	global_store_short v[62:63], v46, off offset:-3968
	v_cvt_pk_bf16_f32 v46, v47, s0
	v_mul_f32_e32 v28, v226, v28
	v_mul_f32_e32 v29, v223, v29
	global_store_short v[30:31], v26, off offset:-4064
	v_cvt_pk_bf16_f32 v26, v27, s0
	v_mul_f32_e32 v24, v228, v24
	v_mul_f32_e32 v25, v223, v25
	global_store_short v[30:31], v22, off offset:-4032
	v_cvt_pk_bf16_f32 v22, v23, s0
	v_mul_f32_e32 v20, v230, v20
	v_mul_f32_e32 v21, v223, v21
	global_store_short v[30:31], v18, off offset:-4000
	v_cvt_pk_bf16_f32 v18, v19, s0
	v_mul_f32_e32 v12, v232, v12
	v_mul_f32_e32 v13, v223, v13
	global_store_short v[30:31], v10, off offset:-3968
	v_cvt_pk_bf16_f32 v10, v11, s0
	v_mul_f32_e32 v8, v234, v8
	v_mul_f32_e32 v9, v223, v9
	global_store_short v[30:31], v6, off offset:-3936
	v_cvt_pk_bf16_f32 v6, v7, s0
	v_mul_f32_e32 v4, v238, v4
	v_mul_f32_e32 v5, v223, v5
	global_store_short v[30:31], v2, off offset:-3872
	v_cvt_pk_bf16_f32 v2, v3, s0
	v_mul_f32_e32 v163, v163, v228
	v_mul_f32_e32 v117, v117, v230
	global_store_short v[148:149], v114, off offset:-4000
	v_cvt_pk_bf16_f32 v114, v116, s0
	v_mul_f32_e32 v113, v113, v232
	global_store_short v[148:149], v110, off offset:-3968
	v_cvt_pk_bf16_f32 v110, v112, s0
	v_mul_f32_e32 v93, v226, v93
	global_store_short v[96:97], v90, off offset:-4064
	v_cvt_pk_bf16_f32 v90, v92, s0
	v_mul_f32_e32 v89, v228, v89
	global_store_short v[96:97], v86, off offset:-4032
	v_cvt_pk_bf16_f32 v86, v88, s0
	v_mul_f32_e32 v61, v226, v61
	global_store_short v[64:65], v58, off offset:-4064
	v_cvt_pk_bf16_f32 v58, v60, s0
	v_mul_f32_e32 v57, v228, v57
	global_store_short v[64:65], v54, off offset:-4032
	v_cvt_pk_bf16_f32 v54, v56, s0
	v_mul_f32_e32 v53, v230, v53
	global_store_short v[64:65], v50, off offset:-4000
	v_cvt_pk_bf16_f32 v50, v52, s0
	v_mul_f32_e32 v49, v232, v49
	global_store_short v[64:65], v46, off offset:-3968
	v_cvt_pk_bf16_f32 v46, v48, s0
	v_mul_f32_e32 v29, v226, v29
	global_store_short v[32:33], v26, off offset:-4064
	v_cvt_pk_bf16_f32 v26, v28, s0
	v_mul_f32_e32 v25, v228, v25
	global_store_short v[32:33], v22, off offset:-4032
	v_cvt_pk_bf16_f32 v22, v24, s0
	v_mul_f32_e32 v21, v230, v21
	global_store_short v[32:33], v18, off offset:-4000
	v_cvt_pk_bf16_f32 v18, v20, s0
	v_mul_f32_e32 v13, v232, v13
	global_store_short v[32:33], v10, off offset:-3968
	v_cvt_pk_bf16_f32 v10, v12, s0
	v_mul_f32_e32 v9, v234, v9
	global_store_short v[32:33], v6, off offset:-3936
	v_cvt_pk_bf16_f32 v6, v8, s0
	v_mul_f32_e32 v5, v238, v5
	global_store_short v[32:33], v2, off offset:-3872
	v_cvt_pk_bf16_f32 v2, v4, s0
	v_cvt_pk_bf16_f32 v129, v163, s0
	global_store_short v[154:155], v114, off offset:-4000
	v_cvt_pk_bf16_f32 v114, v117, s0
	global_store_short v[154:155], v110, off offset:-3968
	v_cvt_pk_bf16_f32 v110, v113, s0
	v_cvt_pk_bf16_f32 v102, v108, s0
	global_store_short v[98:99], v90, off offset:-4064
	v_cvt_pk_bf16_f32 v90, v93, s0
	global_store_short v[98:99], v86, off offset:-4032
	v_cvt_pk_bf16_f32 v86, v89, s0
	v_cvt_pk_bf16_f32 v74, v84, s0
	global_store_short v[70:71], v58, off offset:-4064
	v_cvt_pk_bf16_f32 v58, v61, s0
	global_store_short v[70:71], v54, off offset:-4032
	v_cvt_pk_bf16_f32 v54, v57, s0
	global_store_short v[70:71], v50, off offset:-4000
	v_cvt_pk_bf16_f32 v50, v53, s0
	global_store_short v[70:71], v46, off offset:-3968
	v_cvt_pk_bf16_f32 v46, v49, s0
	v_cvt_pk_bf16_f32 v38, v44, s0
	global_store_short v[34:35], v26, off offset:-4064
	v_cvt_pk_bf16_f32 v26, v29, s0
	global_store_short v[34:35], v22, off offset:-4032
	v_cvt_pk_bf16_f32 v22, v25, s0
	global_store_short v[34:35], v18, off offset:-4000
	v_cvt_pk_bf16_f32 v18, v21, s0
	global_store_short v[34:35], v10, off offset:-3968
	v_cvt_pk_bf16_f32 v10, v13, s0
	global_store_short v[34:35], v6, off offset:-3936
	v_cvt_pk_bf16_f32 v6, v9, s0
	global_store_short v[34:35], v2, off offset:-3872
	v_cvt_pk_bf16_f32 v2, v5, s0
	global_store_short v[150:151], v129, off offset:-4032
	global_store_short v[150:151], v114, off offset:-4000
	global_store_short v[150:151], v110, off offset:-3968
	global_store_short v[100:101], v102, off offset:-4096
	global_store_short v[100:101], v90, off offset:-4064
	global_store_short v[100:101], v86, off offset:-4032
	global_store_short v[72:73], v74, off offset:-4096
	global_store_short v[72:73], v58, off offset:-4064
	global_store_short v[72:73], v54, off offset:-4032
	global_store_short v[72:73], v50, off offset:-4000
	global_store_short v[72:73], v46, off offset:-3968
	global_store_short v[36:37], v38, off offset:-4096
	global_store_short v[36:37], v26, off offset:-4064
	global_store_short v[36:37], v22, off offset:-4032
	global_store_short v[36:37], v18, off offset:-4000
	global_store_short v[36:37], v10, off offset:-3968
	global_store_short v[36:37], v6, off offset:-3936
	global_store_short v[36:37], v2, off offset:-3872

; __device__ __forceinline__ int opaque_tid() { int t = threadIdx.x; asm volatile("" : "+v"(t)); return t; }
; template <bool I8>
; __device__ __forceinline__ void gemm_mainloop_n256(const bf16_t* __restrict__ A, int lda, const bf16_t* __restrict__ Bt, int ldb,
;                                                    int K, int m0, int n0, f32x4 (&acc)[4][8], char* smem) {
;   const int tid = opaque_tid(), lane = tid & 63, w = tid >> 6;
;   const int wm = w >> 1, wn = w & 1;
; #pragma unroll
;   for (int i = 0; i < 4; ++i)
; #pragma unroll
;     for (int j = 0; j < 8; ++j) acc[i][j] = f32x4{0.f, 0.f, 0.f, 0.f};
;   const int nk = K / 64;
;   const int rowoff = lane >> 3, lch = (lane & 7) ^ rowoff;
;   const bf16_t* gA = A + (size_t)(m0 + w * 8 + rowoff) * lda + lch * 8;
;   const bf16_t* gB = Bt + (size_t)(n0 + w * 8 + rowoff) * ldb + lch * 8;
;   const int fr = lane & 15, fq = lane >> 4;
; template <bool I8, class Epi> ...
;     ...
; #pragma unroll
;   for (int i = 0; i < 4; ++i) {
;     const int row = m0 + wm * 64 + i * 16 + (lane >> 4) * 4;
;     float4 rs = float4{1.f, 1.f, 1.f, 1.f};
;     if (I8) rs = *reinterpret_cast<const float4*>(rscale + row);
; #pragma unroll
;     for (int j = 0; j < 8; ++j) {
;       const int col = n0 + wn * 128 + j * 16 + (lane & 15);
;       if (I8) {
;         typedef __attribute__((ext_vector_type(4))) int i32x4;
;         const i32x4 ia = __builtin_bit_cast(i32x4, acc[i][j]);
;         const float cs = cscale[col];
.LBB0_567:
	s_andn2_b64 vcc, exec, s[6:7]
	s_cbranch_vccnz .LBB0_233
	v_mov_b32_e32 v2, v0
	s_lshl_b32 s12, s8, 8
	v_bfe_u32 v4, v2, 3, 3
	v_bfe_u32 v9, v2, 4, 2
	v_ashrrev_i32_e32 v3, 6, v2
	v_and_b32_e32 v5, 7, v2
	v_bitop3_b32 v6, v4, v2, 7 bitop3:0x78
	v_and_b32_e32 v8, 15, v2
	v_lshrrev_b32_e32 v10, 1, v2
	v_bitop3_b32 v2, v9, v2, 7 bitop3:0x78
	v_lshlrev_b32_e32 v138, 4, v2
	v_bitop3_b32 v2, v9, v5, 4 bitop3:0x36
	v_lshlrev_b32_e32 v7, 3, v3
	v_lshlrev_b32_e32 v136, 10, v3
	v_lshlrev_b32_e32 v3, 7, v3
	v_lshlrev_b32_e32 v141, 4, v2
	v_or_b32_e32 v2, s12, v4
	v_and_or_b32 v3, v3, s82, v8
	v_add_u32_e32 v2, v2, v7
	v_lshlrev_b32_e32 v140, 7, v3
	v_ashrrev_i32_e32 v3, 31, v2
	v_lshlrev_b64 v[2:3], 11, v[2:3]
	v_lshlrev_b32_e32 v5, 4, v6
	v_or_b32_e32 v2, v2, v5
	s_add_i32 s11, s11, s10
	v_lshl_add_u64 v[130:131], s[22:23], 0, v[2:3]
	v_add3_u32 v2, s11, v4, v7
	v_ashrrev_i32_e32 v3, 31, v2
	v_and_or_b32 v10, v10, s84, v8
	v_lshlrev_b64 v[2:3], 11, v[2:3]
	v_lshlrev_b32_e32 v139, 7, v10
	v_or_b32_e32 v2, v2, v5
	v_mov_b32_e32 v10, 0
	v_lshl_add_u64 v[132:133], s[20:21], 0, v[2:3]
	s_mov_b64 s[6:7], 0
	v_mov_b32_e32 v11, v10
	v_mov_b32_e32 v12, v10
	v_mov_b32_e32 v13, v10
	v_mov_b32_e32 v2, v10
	v_mov_b32_e32 v3, v10
	v_mov_b32_e32 v4, v10
	v_mov_b32_e32 v5, v10
	v_mov_b32_e32 v6, v10
	v_mov_b32_e32 v7, v10
	v_mov_b32_e32 v8, v10
	v_mov_b32_e32 v9, v10
	v_mov_b32_e32 v14, v10
	v_mov_b32_e32 v15, v10
	v_mov_b32_e32 v16, v10
	v_mov_b32_e32 v17, v10
	v_mov_b32_e32 v18, v10
	v_mov_b32_e32 v19, v10
	v_mov_b32_e32 v20, v10
	v_mov_b32_e32 v21, v10
	v_mov_b32_e32 v22, v10
	v_mov_b32_e32 v23, v10
	v_mov_b32_e32 v24, v10
	v_mov_b32_e32 v25, v10
	v_mov_b32_e32 v26, v10
	v_mov_b32_e32 v27, v10
	v_mov_b32_e32 v28, v10
	v_mov_b32_e32 v29, v10
	v_mov_b32_e32 v30, v10
	v_mov_b32_e32 v31, v10
	v_mov_b32_e32 v32, v10
	v_mov_b32_e32 v33, v10
	v_mov_b32_e32 v34, v10
	v_mov_b32_e32 v35, v10
	v_mov_b32_e32 v36, v10
	v_mov_b32_e32 v37, v10
	v_mov_b32_e32 v38, v10
	v_mov_b32_e32 v39, v10
	v_mov_b32_e32 v40, v10
	v_mov_b32_e32 v41, v10
	v_mov_b32_e32 v42, v10
	v_mov_b32_e32 v43, v10
	v_mov_b32_e32 v44, v10
	v_mov_b32_e32 v45, v10
	v_mov_b32_e32 v46, v10
	v_mov_b32_e32 v47, v10
	v_mov_b32_e32 v48, v10
	v_mov_b32_e32 v49, v10
	v_mov_b32_e32 v50, v10
	v_mov_b32_e32 v51, v10
	v_mov_b32_e32 v52, v10
	v_mov_b32_e32 v53, v10
	v_mov_b32_e32 v54, v10
	v_mov_b32_e32 v55, v10
	v_mov_b32_e32 v56, v10
	v_mov_b32_e32 v57, v10
	v_mov_b32_e32 v58, v10
	v_mov_b32_e32 v59, v10
	v_mov_b32_e32 v60, v10
	v_mov_b32_e32 v61, v10
	v_mov_b32_e32 v62, v10
	v_mov_b32_e32 v63, v10
	v_mov_b32_e32 v64, v10
	v_mov_b32_e32 v65, v10
	v_mov_b32_e32 v66, v10
	v_mov_b32_e32 v67, v10
	v_mov_b32_e32 v68, v10
	v_mov_b32_e32 v69, v10
	v_mov_b32_e32 v70, v10
	v_mov_b32_e32 v71, v10
	v_mov_b32_e32 v72, v10
	v_mov_b32_e32 v73, v10
	v_mov_b32_e32 v74, v10
	v_mov_b32_e32 v75, v10
	v_mov_b32_e32 v76, v10
	v_mov_b32_e32 v77, v10
	v_mov_b32_e32 v78, v10
	v_mov_b32_e32 v79, v10
	v_mov_b32_e32 v80, v10
	v_mov_b32_e32 v81, v10
	v_mov_b32_e32 v82, v10
	v_mov_b32_e32 v83, v10
	v_mov_b32_e32 v84, v10
	v_mov_b32_e32 v85, v10
	v_mov_b32_e32 v86, v10
	v_mov_b32_e32 v87, v10
	v_mov_b32_e32 v88, v10
	v_mov_b32_e32 v89, v10
	v_mov_b32_e32 v90, v10
	v_mov_b32_e32 v91, v10
	v_mov_b32_e32 v92, v10
	v_mov_b32_e32 v93, v10
	v_mov_b32_e32 v94, v10
	v_mov_b32_e32 v95, v10
	v_mov_b32_e32 v96, v10
	v_mov_b32_e32 v97, v10
	v_mov_b32_e32 v98, v10
	v_mov_b32_e32 v99, v10
	v_mov_b32_e32 v100, v10
	v_mov_b32_e32 v101, v10
	v_mov_b32_e32 v102, v10
	v_mov_b32_e32 v103, v10
	v_mov_b32_e32 v104, v10
	v_mov_b32_e32 v105, v10
	v_mov_b32_e32 v106, v10
	v_mov_b32_e32 v107, v10
	v_mov_b32_e32 v108, v10
	v_mov_b32_e32 v109, v10
	v_mov_b32_e32 v110, v10
	v_mov_b32_e32 v111, v10
	v_mov_b32_e32 v112, v10
	v_mov_b32_e32 v113, v10
	v_mov_b32_e32 v114, v10
	v_mov_b32_e32 v115, v10
	v_mov_b32_e32 v116, v10
	v_mov_b32_e32 v117, v10
	v_mov_b32_e32 v118, v10
	v_mov_b32_e32 v119, v10
	v_mov_b32_e32 v120, v10
	v_mov_b32_e32 v121, v10
	v_mov_b32_e32 v122, v10
	v_mov_b32_e32 v123, v10
	v_mov_b32_e32 v124, v10
	v_mov_b32_e32 v125, v10
	v_mov_b32_e32 v126, v10
	v_mov_b32_e32 v127, v10
	v_mov_b32_e32 v128, v10
	v_mov_b32_e32 v129, v10
	v_add_u32_e32 v240, s9, v145
	v_ashrrev_i32_e32 v241, 31, v240
	v_or_b32_e32 v242, s12, v165
	v_lshl_add_u64 v[244:245], v[240:241], 2, s[24:25]
	v_ashrrev_i32_e32 v243, 31, v242
	v_lshl_add_u64 v[246:247], v[242:243], 2, s[26:27]
	global_load_dwordx4 v[208:211], v[244:245], off
	global_load_dwordx4 v[212:215], v[244:245], off offset:64
	global_load_dwordx4 v[216:219], v[244:245], off offset:128
	global_load_dwordx4 v[220:223], v[244:245], off offset:192
	global_load_dword v224, v[246:247], off
	global_load_dword v226, v[246:247], off offset:64
	global_load_dword v228, v[246:247], off offset:128
	global_load_dword v230, v[246:247], off offset:192
	global_load_dword v232, v[246:247], off offset:256
	global_load_dword v234, v[246:247], off offset:320
	global_load_dword v236, v[246:247], off offset:384
	global_load_dword v238, v[246:247], off offset:448
; template <bool I8>
; __device__ __forceinline__ void gemm_mainloop_n256(const bf16_t* __restrict__ A, int lda, const bf16_t* __restrict__ Bt, int ldb,
;                                                    int K, int m0, int n0, f32x4 (&acc)[4][8], char* smem) {
;     ...
;   for (int kt = 0; kt < nk; ++kt) {
; #pragma unroll
;     for (int i_ = 0; i_ < 4; ++i_)
;       __builtin_amdgcn_global_load_lds((const unsigned*)(gA + (size_t)(i_ * 32) * lda + kt * 64),
;                                        (unsigned*)(smem + (i_ * 4 + w) * 1024), 16, 0, 0);
; #pragma unroll
;     for (int i_ = 0; i_ < 8; ++i_)
;       __builtin_amdgcn_global_load_lds((const unsigned*)(gB + (size_t)(i_ * 32) * ldb + kt * 64),
;                                        (unsigned*)(smem + 16384 + (i_ * 4 + w) * 1024), 16, 0, 0);
;     asm volatile("s_waitcnt vmcnt(0)" ::: "memory");
;     __syncthreads();
;     const char* sA = smem;
;     const char* sB = smem + 16384;
; #pragma unroll
;     for (int kk = 0; kk < 2; ++kk) {
;       bf16x8 af[4], bfr[8];
;       const int ch = kk * 4 + fq;
; #pragma unroll
;       for (int i = 0; i < 4; ++i) {
;         const int row = wm * 64 + i * 16 + fr;
;         af[i] = *reinterpret_cast<const bf16x8*>(sA + row * 128 + ((ch ^ (row & 7)) << 4));
;       }
; #pragma unroll
;       for (int j = 0; j < 8; ++j) {
;         const int col = wn * 128 + j * 16 + fr;
;         bfr[j] = *reinterpret_cast<const bf16x8*>(sB + col * 128 + ((ch ^ (col & 7)) << 4));
;       }
; #pragma unroll
;       for (int i = 0; i < 4; ++i)
; #pragma unroll
;         for (int j = 0; j < 8; ++j) {
;           if (I8) {
;             typedef __attribute__((ext_vector_type(4))) int i32x4;
;             acc[i][j] = __builtin_bit_cast(f32x4, __builtin_amdgcn_mfma_i32_16x16x64_i8(__builtin_bit_cast(i32x4, af[i]), __builtin_bit_cast(i32x4, bfr[j]),
;                                                                                          __builtin_bit_cast(i32x4, acc[i][j]), 0, 0, 0));
;           } else {
;             acc[i][j] = __builtin_amdgcn_mfma_f32_16x16x32_bf16(af[i], bfr[j], acc[i][j], 0, 0, 0);
;           }
;         }
;     }
.LBB0_569:
	v_readfirstlane_b32 s10, v136
	v_add_u32_e32 v142, 0x1000, v136
	v_lshl_add_u64 v[146:147], v[132:133], 0, s[6:7]
	v_add_u32_e32 v144, 0x2000, v136
	v_readfirstlane_b32 s11, v142
	s_mov_b32 m0, s10
	v_add_u32_e32 v156, 0x3000, v136
	v_lshl_add_u64 v[150:151], v[146:147], 0, s[54:55]
	v_readfirstlane_b32 s13, v144
	global_load_lds_dwordx4 v[146:147], off
	s_mov_b32 m0, s11
	v_add_u32_e32 v157, 0x4000, v136
	v_lshl_add_u64 v[152:153], v[146:147], 0, s[56:57]
	v_readfirstlane_b32 s14, v156
	global_load_lds_dwordx4 v[150:151], off
	s_mov_b32 m0, s13
	v_add_u32_e32 v158, 0x5000, v136
	v_lshl_add_u64 v[154:155], v[146:147], 0, s[58:59]
	v_readfirstlane_b32 s15, v157
	global_load_lds_dwordx4 v[152:153], off
	s_mov_b32 m0, s14
	v_lshl_add_u64 v[148:149], v[130:131], 0, s[6:7]
	v_add_u32_e32 v160, 0x6000, v136
	v_readfirstlane_b32 s16, v158
	global_load_lds_dwordx4 v[154:155], off
	s_mov_b32 m0, s15
	v_add_u32_e32 v162, 0x7000, v136
	v_lshl_add_u64 v[156:157], v[148:149], 0, s[54:55]
	v_readfirstlane_b32 s17, v160
	global_load_lds_dwordx4 v[148:149], off
	s_mov_b32 m0, s16
	v_add_u32_e32 v170, 0x8000, v136
	v_lshl_add_u64 v[158:159], v[148:149], 0, s[56:57]
	v_readfirstlane_b32 s46, v162
	global_load_lds_dwordx4 v[156:157], off
	s_mov_b32 m0, s17
	v_add_u32_e32 v172, 0x9000, v136
	v_lshl_add_u64 v[160:161], v[148:149], 0, s[58:59]
	v_readfirstlane_b32 s47, v170
	global_load_lds_dwordx4 v[158:159], off
	s_mov_b32 m0, s46
	v_add_u32_e32 v174, 0xa000, v136
	v_lshl_add_u64 v[162:163], v[148:149], 0, s[68:69]
	v_readfirstlane_b32 s76, v172
	global_load_lds_dwordx4 v[160:161], off
	s_mov_b32 m0, s47
	v_add_u32_e32 v176, 0xb000, v136
	v_lshl_add_u64 v[170:171], v[148:149], 0, s[70:71]
	v_readfirstlane_b32 s77, v174
	global_load_lds_dwordx4 v[162:163], off
	s_mov_b32 m0, s76
	v_lshl_add_u64 v[172:173], v[148:149], 0, s[72:73]
	v_readfirstlane_b32 s78, v176
	global_load_lds_dwordx4 v[170:171], off
	s_mov_b32 m0, s77
	v_lshl_add_u64 v[174:175], v[148:149], 0, s[74:75]
	global_load_lds_dwordx4 v[172:173], off
	s_mov_b32 m0, s78
	v_add_u32_e32 v189, v138, v139
	global_load_lds_dwordx4 v[174:175], off
	v_add_u32_e32 v193, v138, v140
	s_waitcnt vmcnt(0)
	s_waitcnt vmcnt(0) lgkmcnt(0)
	s_barrier
	ds_read_b128 v[146:149], v189
	ds_read_b128 v[150:153], v193 offset:16384
	ds_read_b128 v[154:157], v189 offset:2048
	ds_read_b128 v[158:161], v193 offset:18432
	ds_read_b128 v[170:173], v193 offset:20480
	ds_read_b128 v[174:177], v193 offset:22528
	ds_read_b128 v[178:181], v193 offset:24576
	ds_read_b128 v[196:199], v193 offset:26624
	ds_read_b128 v[200:203], v193 offset:28672
	ds_read_b128 v[204:207], v193 offset:30720
	s_waitcnt lgkmcnt(8)
	v_mfma_i32_16x16x64_i8 v[126:129], v[146:149], v[150:153], v[126:129]
	v_add_u32_e32 v142, v141, v139
	v_add_u32_e32 v144, v141, v140
	s_add_u32 s6, s6, 0x80
	s_waitcnt lgkmcnt(6)
	v_mfma_i32_16x16x64_i8 v[122:125], v[146:149], v[158:161], v[122:125]
	s_addc_u32 s7, s7, 0
	s_cmpk_lg_i32 s6, 0x800
	s_waitcnt lgkmcnt(5)
	v_mfma_i32_16x16x64_i8 v[118:121], v[146:149], v[170:173], v[118:121]
	s_waitcnt lgkmcnt(4)
	v_mfma_i32_16x16x64_i8 v[114:117], v[146:149], v[174:177], v[114:117]
	s_waitcnt lgkmcnt(3)
	v_mfma_i32_16x16x64_i8 v[110:113], v[146:149], v[178:181], v[110:113]
	s_waitcnt lgkmcnt(2)
	v_mfma_i32_16x16x64_i8 v[106:109], v[146:149], v[196:199], v[106:109]
	s_waitcnt lgkmcnt(1)
	v_mfma_i32_16x16x64_i8 v[102:105], v[146:149], v[200:203], v[102:105]
	s_waitcnt lgkmcnt(0)
	v_mfma_i32_16x16x64_i8 v[98:101], v[146:149], v[204:207], v[98:101]
	v_mfma_i32_16x16x64_i8 v[94:97], v[154:157], v[150:153], v[94:97]
	v_mfma_i32_16x16x64_i8 v[90:93], v[154:157], v[158:161], v[90:93]
	v_mfma_i32_16x16x64_i8 v[86:89], v[154:157], v[170:173], v[86:89]
	v_mfma_i32_16x16x64_i8 v[82:85], v[154:157], v[174:177], v[82:85]
	v_mfma_i32_16x16x64_i8 v[78:81], v[154:157], v[178:181], v[78:81]
	v_mfma_i32_16x16x64_i8 v[74:77], v[154:157], v[196:199], v[74:77]
	v_mfma_i32_16x16x64_i8 v[70:73], v[154:157], v[200:203], v[70:73]
	v_mfma_i32_16x16x64_i8 v[66:69], v[154:157], v[204:207], v[66:69]
	ds_read_b128 v[146:149], v189 offset:4096
	ds_read_b128 v[154:157], v189 offset:6144
	s_waitcnt lgkmcnt(1)
	v_mfma_i32_16x16x64_i8 v[62:65], v[146:149], v[150:153], v[62:65]
	v_mfma_i32_16x16x64_i8 v[58:61], v[146:149], v[158:161], v[58:61]
	v_mfma_i32_16x16x64_i8 v[54:57], v[146:149], v[170:173], v[54:57]
	v_mfma_i32_16x16x64_i8 v[50:53], v[146:149], v[174:177], v[50:53]
	v_mfma_i32_16x16x64_i8 v[46:49], v[146:149], v[178:181], v[46:49]
	v_mfma_i32_16x16x64_i8 v[42:45], v[146:149], v[196:199], v[42:45]
	v_mfma_i32_16x16x64_i8 v[38:41], v[146:149], v[200:203], v[38:41]
	v_mfma_i32_16x16x64_i8 v[34:37], v[146:149], v[204:207], v[34:37]
	ds_read_b128 v[146:149], v142
	s_waitcnt lgkmcnt(1)
	v_mfma_i32_16x16x64_i8 v[30:33], v[154:157], v[150:153], v[30:33]
	v_mfma_i32_16x16x64_i8 v[26:29], v[154:157], v[158:161], v[26:29]
	v_mfma_i32_16x16x64_i8 v[22:25], v[154:157], v[170:173], v[22:25]
	v_mfma_i32_16x16x64_i8 v[18:21], v[154:157], v[174:177], v[18:21]
	v_mfma_i32_16x16x64_i8 v[14:17], v[154:157], v[178:181], v[14:17]
	v_mfma_i32_16x16x64_i8 v[6:9], v[154:157], v[196:199], v[6:9]
	v_mfma_i32_16x16x64_i8 v[2:5], v[154:157], v[200:203], v[2:5]
	v_mfma_i32_16x16x64_i8 v[10:13], v[154:157], v[204:207], v[10:13]
	ds_read_b128 v[150:153], v144 offset:16384
	ds_read_b128 v[154:157], v142 offset:2048
	ds_read_b128 v[158:161], v144 offset:18432
	ds_read_b128 v[170:173], v144 offset:20480
	ds_read_b128 v[174:177], v144 offset:22528
	ds_read_b128 v[178:181], v144 offset:24576
	ds_read_b128 v[196:199], v144 offset:26624
	ds_read_b128 v[200:203], v144 offset:28672
	ds_read_b128 v[204:207], v144 offset:30720
	s_waitcnt lgkmcnt(8)
; template <bool I8, class Epi> ...
;     ...
;   for (int i = 0; i < 4; ++i) {
;     const int row = m0 + wm * 64 + i * 16 + (lane >> 4) * 4;
;     float4 rs = float4{1.f, 1.f, 1.f, 1.f};
;     if (I8) rs = *reinterpret_cast<const float4*>(rscale + row);
; #pragma unroll
;     for (int j = 0; j < 8; ++j) {
;       const int col = n0 + wn * 128 + j * 16 + (lane & 15);
;       if (I8) {
;         typedef __attribute__((ext_vector_type(4))) int i32x4;
;         const i32x4 ia = __builtin_bit_cast(i32x4, acc[i][j]);
;         const float cs = cscale[col];
;         epi(row, col, f32x4{(float)ia[0] * rs.x * cs, (float)ia[1] * rs.y * cs, (float)ia[2] * rs.z * cs, (float)ia[3] * rs.w * cs});
;       } else {
;         epi(row, col, acc[i][j]);
;       }
;     }
;   }
;   __device__ __forceinline__ void operator()(int row, int col, f32x4 v) const {
;     const int ch = col & 1023, half = col >> 10;
;     const int b = row / seqlen, l = row - b * seqlen;
;     uint2 pk; pk.x = pack2(v[0], v[1]); pk.y = pack2(v[2], v[3]);
;     *reinterpret_cast<uint2*>(ABt + ((size_t)(b * 1024 + ch) * 4096 + half * 2048 + l)) = pk;
;   }
	v_mfma_i32_16x16x64_i8 v[126:129], v[146:149], v[150:153], v[126:129]
	s_waitcnt lgkmcnt(6)
	v_mfma_i32_16x16x64_i8 v[122:125], v[146:149], v[158:161], v[122:125]
	s_waitcnt lgkmcnt(5)
	v_mfma_i32_16x16x64_i8 v[118:121], v[146:149], v[170:173], v[118:121]
	s_waitcnt lgkmcnt(4)
	v_mfma_i32_16x16x64_i8 v[114:117], v[146:149], v[174:177], v[114:117]
	s_waitcnt lgkmcnt(3)
	v_mfma_i32_16x16x64_i8 v[110:113], v[146:149], v[178:181], v[110:113]
	s_waitcnt lgkmcnt(2)
	v_mfma_i32_16x16x64_i8 v[106:109], v[146:149], v[196:199], v[106:109]
	s_waitcnt lgkmcnt(1)
	v_mfma_i32_16x16x64_i8 v[102:105], v[146:149], v[200:203], v[102:105]
	s_waitcnt lgkmcnt(0)
	v_mfma_i32_16x16x64_i8 v[98:101], v[146:149], v[204:207], v[98:101]
	v_mfma_i32_16x16x64_i8 v[94:97], v[154:157], v[150:153], v[94:97]
	v_mfma_i32_16x16x64_i8 v[90:93], v[154:157], v[158:161], v[90:93]
	v_mfma_i32_16x16x64_i8 v[86:89], v[154:157], v[170:173], v[86:89]
	v_mfma_i32_16x16x64_i8 v[82:85], v[154:157], v[174:177], v[82:85]
	v_mfma_i32_16x16x64_i8 v[78:81], v[154:157], v[178:181], v[78:81]
	v_mfma_i32_16x16x64_i8 v[74:77], v[154:157], v[196:199], v[74:77]
	v_mfma_i32_16x16x64_i8 v[70:73], v[154:157], v[200:203], v[70:73]
	v_mfma_i32_16x16x64_i8 v[66:69], v[154:157], v[204:207], v[66:69]
	ds_read_b128 v[146:149], v142 offset:4096
	ds_read_b128 v[154:157], v142 offset:6144
	s_waitcnt lgkmcnt(0)
	s_barrier
	v_mfma_i32_16x16x64_i8 v[62:65], v[146:149], v[150:153], v[62:65]
	v_mfma_i32_16x16x64_i8 v[58:61], v[146:149], v[158:161], v[58:61]
	v_mfma_i32_16x16x64_i8 v[54:57], v[146:149], v[170:173], v[54:57]
	v_mfma_i32_16x16x64_i8 v[50:53], v[146:149], v[174:177], v[50:53]
	v_mfma_i32_16x16x64_i8 v[46:49], v[146:149], v[178:181], v[46:49]
	v_mfma_i32_16x16x64_i8 v[42:45], v[146:149], v[196:199], v[42:45]
	v_mfma_i32_16x16x64_i8 v[38:41], v[146:149], v[200:203], v[38:41]
	v_mfma_i32_16x16x64_i8 v[34:37], v[146:149], v[204:207], v[34:37]
	v_mfma_i32_16x16x64_i8 v[30:33], v[154:157], v[150:153], v[30:33]
	v_mfma_i32_16x16x64_i8 v[26:29], v[154:157], v[158:161], v[26:29]
	v_mfma_i32_16x16x64_i8 v[22:25], v[154:157], v[170:173], v[22:25]
	v_mfma_i32_16x16x64_i8 v[18:21], v[154:157], v[174:177], v[18:21]
	v_mfma_i32_16x16x64_i8 v[14:17], v[154:157], v[178:181], v[14:17]
	v_mfma_i32_16x16x64_i8 v[6:9], v[154:157], v[196:199], v[6:9]
	v_mfma_i32_16x16x64_i8 v[2:5], v[154:157], v[200:203], v[2:5]
	v_mfma_i32_16x16x64_i8 v[10:13], v[154:157], v[204:207], v[10:13]
	s_cbranch_scc1 .LBB0_569
	v_add_u32_e32 v138, s9, v145
	v_ashrrev_i32_e32 v139, 31, v138
	v_lshl_add_u64 v[146:147], v[138:139], 2, s[24:25]
	v_or_b32_e32 v148, s12, v165
	v_ashrrev_i32_e32 v149, 31, v148
	v_lshl_add_u64 v[150:151], v[148:149], 2, s[26:27]
	v_cvt_f32_i32_e32 v158, v118
	v_cvt_f32_i32_e32 v152, v126
	v_cvt_f32_i32_e32 v126, v114
	v_lshrrev_b32_e32 v114, 21, v139
	v_cvt_f32_i32_e32 v153, v127
	v_cvt_f32_i32_e32 v155, v123
	v_cvt_f32_i32_e32 v154, v122
	v_cvt_f32_i32_e32 v156, v124
	v_cvt_f32_i32_e32 v160, v120
	v_cvt_f32_i32_e32 v127, v115
	v_cvt_f32_i32_e32 v163, v117
	v_cvt_f32_i32_e32 v162, v116
	v_add_u32_e32 v123, v114, v138
	v_cvt_f32_i32_e32 v157, v125
	v_ashrrev_i32_e32 v125, 11, v123
	v_and_b32_e32 v149, 0xfffff800, v123
	v_cvt_f32_i32_e32 v129, v129
	v_cvt_f32_i32_e32 v128, v128
	v_bitop3_b32 v141, s12, v166, v165 bitop3:0xc8
	s_lshl_b32 s6, s8, 9
	s_movk_i32 s7, 0x39f
	s_movk_i32 s8, 0x3af
	v_sub_u32_e32 v150, v138, v149
	v_lshlrev_b32_e32 v149, 10, v125
	v_cvt_f32_i32_e32 v159, v119
	v_cvt_f32_i32_e32 v161, v121
	v_bitop3_b32 v121, v148, s7, 16 bitop3:0xc8
	v_bitop3_b32 v119, v148, s8, 32 bitop3:0xc8
	v_or_b32_e32 v170, v149, v141
	s_and_b32 s6, s6, 0xfffff800
	v_or_b32_e32 v172, v149, v121
	v_or_b32_e32 v174, v149, v119
	v_ashrrev_i32_e32 v171, 31, v170
	s_ashr_i32 s7, s6, 31
	v_ashrrev_i32_e32 v173, 31, v172
	v_ashrrev_i32_e32 v175, 31, v174
	v_lshlrev_b64 v[170:171], 13, v[170:171]
	s_lshl_b64 s[6:7], s[6:7], 1
	v_ashrrev_i32_e32 v151, 31, v150
	v_lshlrev_b64 v[172:173], 13, v[172:173]
	v_lshlrev_b64 v[174:175], 13, v[174:175]
	v_lshl_add_u64 v[170:171], s[36:37], 0, v[170:171]
	v_lshlrev_b64 v[150:151], 1, v[150:151]
	v_lshl_add_u64 v[172:173], s[36:37], 0, v[172:173]
	v_lshl_add_u64 v[174:175], s[36:37], 0, v[174:175]
	v_lshl_add_u64 v[170:171], v[170:171], 0, s[6:7]
	v_lshl_add_u64 v[172:173], v[172:173], 0, s[6:7]
	v_lshl_add_u64 v[174:175], v[174:175], 0, s[6:7]
	v_lshl_add_u64 v[170:171], v[170:171], 0, v[150:151]
	v_lshl_add_u64 v[172:173], v[172:173], 0, v[150:151]
	v_lshl_add_u64 v[174:175], v[174:175], 0, v[150:151]
	s_movk_i32 s8, 0x3bf
	v_bitop3_b32 v125, v148, s8, 48 bitop3:0xc8
	v_cvt_f32_i32_e32 v111, v111
	v_cvt_f32_i32_e32 v110, v110
	v_cvt_f32_i32_e32 v113, v113
	v_cvt_f32_i32_e32 v112, v112
	s_movk_i32 s8, 0x3cf
	v_cvt_f32_i32_e32 v107, v107
	v_cvt_f32_i32_e32 v106, v106
	v_cvt_f32_i32_e32 v109, v109
	v_cvt_f32_i32_e32 v108, v108
	v_cvt_f32_i32_e32 v103, v103
	v_cvt_f32_i32_e32 v102, v102
	v_cvt_f32_i32_e32 v105, v105
	v_cvt_f32_i32_e32 v104, v104
	v_cvt_f32_i32_e32 v99, v99
	v_cvt_f32_i32_e32 v98, v98
	v_cvt_f32_i32_e32 v101, v101
	v_cvt_f32_i32_e32 v100, v100
	v_cvt_f32_i32_e32 v95, v95
	v_cvt_f32_i32_e32 v94, v94
	v_cvt_f32_i32_e32 v87, v87
	v_pk_mul_f32 v[152:153], v[208:209], v[152:153]
	v_pk_mul_f32 v[128:129], v[210:211], v[128:129]
	v_pk_mul_f32 v[154:155], v[208:209], v[154:155]
	v_pk_mul_f32 v[156:157], v[210:211], v[156:157]
	v_pk_mul_f32 v[158:159], v[208:209], v[158:159]
	v_pk_mul_f32 v[160:161], v[210:211], v[160:161]
	v_pk_mul_f32 v[152:153], v[152:153], v[224:225] op_sel_hi:[1, 0]
	v_pk_mul_f32 v[128:129], v[128:129], v[224:225] op_sel_hi:[1, 0]
; template <bool I8, class Epi> ...
;     ...
;   for (int i = 0; i < 4; ++i) {
;     const int row = m0 + wm * 64 + i * 16 + (lane >> 4) * 4;
;     float4 rs = float4{1.f, 1.f, 1.f, 1.f};
;     if (I8) rs = *reinterpret_cast<const float4*>(rscale + row);
; #pragma unroll
;     for (int j = 0; j < 8; ++j) {
;       const int col = n0 + wn * 128 + j * 16 + (lane & 15);
;       if (I8) {
;         typedef __attribute__((ext_vector_type(4))) int i32x4;
;         const i32x4 ia = __builtin_bit_cast(i32x4, acc[i][j]);
;         const float cs = cscale[col];
;         epi(row, col, f32x4{(float)ia[0] * rs.x * cs, (float)ia[1] * rs.y * cs, (float)ia[2] * rs.z * cs, (float)ia[3] * rs.w * cs});
;       } else {
;         epi(row, col, acc[i][j]);
;       }
;     }
;   }
;   __device__ __forceinline__ void operator()(int row, int col, f32x4 v) const {
;     const int ch = col & 1023, half = col >> 10;
;     const int b = row / seqlen, l = row - b * seqlen;
;     uint2 pk; pk.x = pack2(v[0], v[1]); pk.y = pack2(v[2], v[3]);
;     *reinterpret_cast<uint2*>(ABt + ((size_t)(b * 1024 + ch) * 4096 + half * 2048 + l)) = pk;
;   }
	v_pk_mul_f32 v[154:155], v[154:155], v[226:227] op_sel_hi:[1, 0]
	v_pk_mul_f32 v[156:157], v[156:157], v[226:227] op_sel_hi:[1, 0]
	v_pk_mul_f32 v[158:159], v[158:159], v[228:229] op_sel_hi:[1, 0]
	v_pk_mul_f32 v[160:161], v[160:161], v[228:229] op_sel_hi:[1, 0]
	v_cvt_pk_bf16_f32 v152, v152, v153
	v_cvt_pk_bf16_f32 v153, v128, v129
	v_cvt_pk_bf16_f32 v128, v154, v155
	v_cvt_pk_bf16_f32 v129, v156, v157
	v_cvt_pk_bf16_f32 v154, v158, v159
	v_cvt_pk_bf16_f32 v155, v160, v161
	global_store_dwordx2 v[170:171], v[152:153], off
	global_store_dwordx2 v[172:173], v[128:129], off
	global_store_dwordx2 v[174:175], v[154:155], off
	v_pk_mul_f32 v[126:127], v[208:209], v[126:127]
	v_pk_mul_f32 v[128:129], v[210:211], v[162:163]
	v_pk_mul_f32 v[126:127], v[126:127], v[230:231] op_sel_hi:[1, 0]
	v_pk_mul_f32 v[128:129], v[128:129], v[230:231] op_sel_hi:[1, 0]
	v_cvt_pk_bf16_f32 v126, v126, v127
	v_cvt_pk_bf16_f32 v127, v128, v129
	v_or_b32_e32 v128, v149, v125
	v_ashrrev_i32_e32 v129, 31, v128
	v_lshlrev_b64 v[128:129], 13, v[128:129]
	v_lshl_add_u64 v[128:129], s[36:37], 0, v[128:129]
	v_lshl_add_u64 v[128:129], v[128:129], 0, s[6:7]
	v_lshl_add_u64 v[128:129], v[128:129], 0, v[150:151]
	v_pk_mul_f32 v[110:111], v[208:209], v[110:111]
	global_store_dwordx2 v[128:129], v[126:127], off
	v_pk_mul_f32 v[126:127], v[110:111], v[232:233] op_sel_hi:[1, 0]
	v_pk_mul_f32 v[110:111], v[210:211], v[112:113]
	v_cvt_pk_bf16_f32 v126, v126, v127
	v_pk_mul_f32 v[112:113], v[110:111], v[232:233] op_sel_hi:[1, 0]
	v_bitop3_b32 v110, v148, s8, 64 bitop3:0xc8
	v_cvt_pk_bf16_f32 v127, v112, v113
	v_or_b32_e32 v112, v149, v110
	v_ashrrev_i32_e32 v113, 31, v112
	v_lshlrev_b64 v[112:113], 13, v[112:113]
	v_lshl_add_u64 v[112:113], s[36:37], 0, v[112:113]
	v_lshl_add_u64 v[112:113], v[112:113], 0, s[6:7]
	v_lshl_add_u64 v[112:113], v[112:113], 0, v[150:151]
	v_pk_mul_f32 v[106:107], v[208:209], v[106:107]
	global_store_dwordx2 v[112:113], v[126:127], off
	v_pk_mul_f32 v[112:113], v[106:107], v[234:235] op_sel_hi:[1, 0]
	v_pk_mul_f32 v[106:107], v[210:211], v[108:109]
	s_movk_i32 s8, 0x3df
	v_pk_mul_f32 v[108:109], v[106:107], v[234:235] op_sel_hi:[1, 0]
	v_bitop3_b32 v106, v148, s8, v167 bitop3:0xc8
	v_cvt_pk_bf16_f32 v112, v112, v113
	v_cvt_pk_bf16_f32 v113, v108, v109
	v_or_b32_e32 v108, v149, v106
	v_ashrrev_i32_e32 v109, 31, v108
	v_lshlrev_b64 v[108:109], 13, v[108:109]
	v_lshl_add_u64 v[108:109], s[36:37], 0, v[108:109]
	v_lshl_add_u64 v[108:109], v[108:109], 0, s[6:7]
	v_lshl_add_u64 v[108:109], v[108:109], 0, v[150:151]
	v_pk_mul_f32 v[102:103], v[208:209], v[102:103]
	global_store_dwordx2 v[108:109], v[112:113], off
	v_pk_mul_f32 v[108:109], v[102:103], v[236:237] op_sel_hi:[1, 0]
	v_pk_mul_f32 v[102:103], v[210:211], v[104:105]
	s_movk_i32 s8, 0x3ef
	v_pk_mul_f32 v[104:105], v[102:103], v[236:237] op_sel_hi:[1, 0]
	v_bitop3_b32 v102, v148, s8, v168 bitop3:0xc8
	v_cvt_pk_bf16_f32 v108, v108, v109
	v_cvt_pk_bf16_f32 v109, v104, v105
	v_or_b32_e32 v104, v149, v102
	v_ashrrev_i32_e32 v105, 31, v104
	v_lshlrev_b64 v[104:105], 13, v[104:105]
	v_lshl_add_u64 v[104:105], s[36:37], 0, v[104:105]
	v_lshl_add_u64 v[104:105], v[104:105], 0, s[6:7]
	v_lshl_add_u64 v[104:105], v[104:105], 0, v[150:151]
	v_pk_mul_f32 v[98:99], v[208:209], v[98:99]
	global_store_dwordx2 v[104:105], v[108:109], off
	v_pk_mul_f32 v[104:105], v[98:99], v[238:239] op_sel_hi:[1, 0]
	v_pk_mul_f32 v[98:99], v[210:211], v[100:101]
	v_cvt_pk_bf16_f32 v104, v104, v105
	v_pk_mul_f32 v[100:101], v[98:99], v[238:239] op_sel_hi:[1, 0]
	v_bitop3_b32 v98, v148, s50, v169 bitop3:0xc8
	v_cvt_pk_bf16_f32 v105, v100, v101
	v_or_b32_e32 v100, v149, v98
	v_ashrrev_i32_e32 v101, 31, v100
	v_lshlrev_b64 v[100:101], 13, v[100:101]
	v_lshl_add_u64 v[100:101], s[36:37], 0, v[100:101]
	v_lshl_add_u64 v[100:101], v[100:101], 0, s[6:7]
	v_cvt_f32_i32_e32 v86, v86
	v_cvt_f32_i32_e32 v89, v89
	v_cvt_f32_i32_e32 v88, v88
	v_lshl_add_u64 v[100:101], v[100:101], 0, v[150:151]
	v_add_u32_e32 v99, 16, v123
	global_store_dwordx2 v[100:101], v[104:105], off
	v_ashrrev_i32_e32 v100, 11, v99
	v_cvt_f32_i32_e32 v97, v97
	v_cvt_f32_i32_e32 v96, v96
	v_pk_mul_f32 v[94:95], v[212:213], v[94:95]
	v_lshlrev_b32_e32 v103, 10, v100
	v_pk_mul_f32 v[94:95], v[224:225], v[94:95] op_sel_hi:[0, 1]
	v_cvt_pk_bf16_f32 v100, v94, v95
	v_or_b32_e32 v94, v103, v141
	v_pk_mul_f32 v[86:87], v[212:213], v[86:87]
	v_pk_mul_f32 v[88:89], v[214:215], v[88:89]
	v_ashrrev_i32_e32 v95, 31, v94
	v_pk_mul_f32 v[86:87], v[228:229], v[86:87] op_sel_hi:[0, 1]
	v_pk_mul_f32 v[88:89], v[228:229], v[88:89] op_sel_hi:[0, 1]
	v_pk_mul_f32 v[96:97], v[214:215], v[96:97]
	v_lshlrev_b64 v[94:95], 13, v[94:95]
	v_cvt_pk_bf16_f32 v86, v86, v87
	v_cvt_pk_bf16_f32 v87, v88, v89
	v_or_b32_e32 v88, v103, v119
	v_cvt_f32_i32_e32 v83, v83
	v_cvt_f32_i32_e32 v82, v82
	v_and_b32_e32 v99, 0xfffff800, v99
	v_pk_mul_f32 v[96:97], v[224:225], v[96:97] op_sel_hi:[0, 1]
	v_lshl_add_u64 v[94:95], s[36:37], 0, v[94:95]
	v_ashrrev_i32_e32 v89, 31, v88
	v_cvt_pk_bf16_f32 v101, v96, v97
	v_lshl_add_u64 v[96:97], v[94:95], 0, s[6:7]
	v_ashrrev_i32_e32 v95, 31, v99
	v_sub_co_u32_e32 v94, vcc, v138, v99
	v_lshlrev_b64 v[88:89], 13, v[88:89]
	s_nop 0
	v_subb_co_u32_e32 v95, vcc, v139, v95, vcc
	v_lshl_add_u64 v[88:89], s[36:37], 0, v[88:89]
	v_lshlrev_b64 v[94:95], 1, v[94:95]
	v_lshl_add_u64 v[88:89], v[88:89], 0, s[6:7]
	v_cvt_f32_i32_e32 v85, v85
	v_cvt_f32_i32_e32 v84, v84
	v_pk_mul_f32 v[82:83], v[212:213], v[82:83]
	v_lshl_add_u64 v[88:89], v[88:89], 0, v[94:95]
	v_pk_mul_f32 v[82:83], v[230:231], v[82:83] op_sel_hi:[0, 1]
	v_cvt_f32_i32_e32 v67, v67
	v_cvt_f32_i32_e32 v66, v66
; template <bool I8, class Epi> ...
;     ...
;   for (int i = 0; i < 4; ++i) {
;     const int row = m0 + wm * 64 + i * 16 + (lane >> 4) * 4;
;     float4 rs = float4{1.f, 1.f, 1.f, 1.f};
;     if (I8) rs = *reinterpret_cast<const float4*>(rscale + row);
; #pragma unroll
;     for (int j = 0; j < 8; ++j) {
;       const int col = n0 + wn * 128 + j * 16 + (lane & 15);
;       if (I8) {
;         typedef __attribute__((ext_vector_type(4))) int i32x4;
;         const i32x4 ia = __builtin_bit_cast(i32x4, acc[i][j]);
;         const float cs = cscale[col];
;         epi(row, col, f32x4{(float)ia[0] * rs.x * cs, (float)ia[1] * rs.y * cs, (float)ia[2] * rs.z * cs, (float)ia[3] * rs.w * cs});
;       } else {
;         epi(row, col, acc[i][j]);
;       }
;     }
;   }
;   __device__ __forceinline__ void operator()(int row, int col, f32x4 v) const {
;     const int ch = col & 1023, half = col >> 10;
;     const int b = row / seqlen, l = row - b * seqlen;
;     uint2 pk; pk.x = pack2(v[0], v[1]); pk.y = pack2(v[2], v[3]);
;     *reinterpret_cast<uint2*>(ABt + ((size_t)(b * 1024 + ch) * 4096 + half * 2048 + l)) = pk;
;   }
	v_cvt_f32_i32_e32 v69, v69
	v_cvt_f32_i32_e32 v68, v68
	global_store_dwordx2 v[88:89], v[86:87], off offset:32
	v_cvt_pk_bf16_f32 v86, v82, v83
	v_or_b32_e32 v82, v103, v125
	v_ashrrev_i32_e32 v83, 31, v82
	v_cvt_f32_i32_e32 v71, v71
	v_cvt_f32_i32_e32 v70, v70
	v_cvt_f32_i32_e32 v73, v73
	v_cvt_f32_i32_e32 v72, v72
	v_pk_mul_f32 v[84:85], v[214:215], v[84:85]
	v_lshlrev_b64 v[82:83], 13, v[82:83]
	v_pk_mul_f32 v[84:85], v[230:231], v[84:85] op_sel_hi:[0, 1]
	v_lshl_add_u64 v[82:83], s[36:37], 0, v[82:83]
	v_pk_mul_f32 v[66:67], v[212:213], v[66:67]
	v_pk_mul_f32 v[68:69], v[214:215], v[68:69]
	v_cvt_pk_bf16_f32 v87, v84, v85
	v_lshl_add_u64 v[88:89], v[82:83], 0, s[6:7]
	v_pk_mul_f32 v[66:67], v[238:239], v[66:67] op_sel_hi:[0, 1]
	v_pk_mul_f32 v[68:69], v[238:239], v[68:69] op_sel_hi:[0, 1]
	v_pk_mul_f32 v[70:71], v[212:213], v[70:71]
	v_pk_mul_f32 v[72:73], v[214:215], v[72:73]
	v_cvt_pk_bf16_f32 v66, v66, v67
	v_cvt_pk_bf16_f32 v67, v68, v69
	v_or_b32_e32 v68, v103, v98
	v_pk_mul_f32 v[70:71], v[236:237], v[70:71] op_sel_hi:[0, 1]
	v_pk_mul_f32 v[72:73], v[236:237], v[72:73] op_sel_hi:[0, 1]
	v_ashrrev_i32_e32 v69, 31, v68
	v_cvt_pk_bf16_f32 v70, v70, v71
	v_cvt_pk_bf16_f32 v71, v72, v73
	v_or_b32_e32 v72, v103, v102
	v_lshlrev_b64 v[68:69], 13, v[68:69]
	v_ashrrev_i32_e32 v73, 31, v72
	v_lshl_add_u64 v[68:69], s[36:37], 0, v[68:69]
	v_lshlrev_b64 v[72:73], 13, v[72:73]
	v_lshl_add_u64 v[68:69], v[68:69], 0, s[6:7]
	v_lshl_add_u64 v[72:73], s[36:37], 0, v[72:73]
	v_lshl_add_u64 v[68:69], v[68:69], 0, v[94:95]
	v_lshl_add_u64 v[72:73], v[72:73], 0, s[6:7]
	global_store_dwordx2 v[68:69], v[66:67], off offset:32
	v_add_u32_e32 v66, 32, v123
	v_lshl_add_u64 v[72:73], v[72:73], 0, v[94:95]
	v_ashrrev_i32_e32 v67, 11, v66
	global_store_dwordx2 v[72:73], v[70:71], off offset:32
	v_and_b32_e32 v71, 0xfffff800, v66
	v_lshlrev_b32_e32 v70, 10, v67
	v_cvt_f32_i32_e32 v67, v63
	v_cvt_f32_i32_e32 v66, v62
	v_cvt_f32_i32_e32 v69, v65
	v_cvt_f32_i32_e32 v68, v64
	v_cvt_f32_i32_e32 v91, v91
	v_cvt_f32_i32_e32 v90, v90
	v_cvt_f32_i32_e32 v93, v93
	v_cvt_f32_i32_e32 v92, v92
	v_cvt_f32_i32_e32 v79, v79
	v_cvt_f32_i32_e32 v78, v78
	v_cvt_f32_i32_e32 v81, v81
	v_cvt_f32_i32_e32 v80, v80
	v_cvt_f32_i32_e32 v75, v75
	v_cvt_f32_i32_e32 v74, v74
	v_cvt_f32_i32_e32 v77, v77
	v_cvt_f32_i32_e32 v76, v76
	v_cvt_f32_i32_e32 v35, v35
	v_cvt_f32_i32_e32 v34, v34
	v_cvt_f32_i32_e32 v37, v37
	v_cvt_f32_i32_e32 v36, v36
	v_pk_mul_f32 v[90:91], v[212:213], v[90:91]
	v_pk_mul_f32 v[92:93], v[214:215], v[92:93]
	v_pk_mul_f32 v[78:79], v[212:213], v[78:79]
	v_pk_mul_f32 v[80:81], v[214:215], v[80:81]
	v_pk_mul_f32 v[74:75], v[212:213], v[74:75]
	v_pk_mul_f32 v[76:77], v[214:215], v[76:77]
	v_pk_mul_f32 v[90:91], v[226:227], v[90:91] op_sel_hi:[0, 1]
	v_pk_mul_f32 v[92:93], v[226:227], v[92:93] op_sel_hi:[0, 1]
	v_pk_mul_f32 v[78:79], v[232:233], v[78:79] op_sel_hi:[0, 1]
	v_pk_mul_f32 v[80:81], v[232:233], v[80:81] op_sel_hi:[0, 1]
	v_pk_mul_f32 v[74:75], v[234:235], v[74:75] op_sel_hi:[0, 1]
	v_pk_mul_f32 v[76:77], v[234:235], v[76:77] op_sel_hi:[0, 1]
	v_cvt_pk_bf16_f32 v90, v90, v91
	v_cvt_pk_bf16_f32 v91, v92, v93
	v_or_b32_e32 v92, v103, v121
	v_cvt_pk_bf16_f32 v78, v78, v79
	v_cvt_pk_bf16_f32 v79, v80, v81
	v_or_b32_e32 v80, v103, v110
	v_cvt_pk_bf16_f32 v74, v74, v75
	v_cvt_pk_bf16_f32 v75, v76, v77
	v_or_b32_e32 v76, v103, v106
	v_ashrrev_i32_e32 v93, 31, v92
	v_ashrrev_i32_e32 v81, 31, v80
	v_ashrrev_i32_e32 v77, 31, v76
	v_lshlrev_b64 v[92:93], 13, v[92:93]
	v_lshlrev_b64 v[80:81], 13, v[80:81]
	v_lshlrev_b64 v[76:77], 13, v[76:77]
	v_ashrrev_i32_e32 v73, 31, v71
	v_sub_co_u32_e32 v72, vcc, v138, v71
	v_pk_mul_f32 v[34:35], v[216:217], v[34:35]
	v_pk_mul_f32 v[36:37], v[218:219], v[36:37]
	v_pk_mul_f32 v[34:35], v[238:239], v[34:35] op_sel_hi:[0, 1]
	v_pk_mul_f32 v[36:37], v[238:239], v[36:37] op_sel_hi:[0, 1]
	v_cvt_pk_bf16_f32 v34, v34, v35
	v_cvt_pk_bf16_f32 v35, v36, v37
	v_or_b32_e32 v36, v70, v98
	v_ashrrev_i32_e32 v37, 31, v36
	v_lshlrev_b64 v[36:37], 13, v[36:37]
	v_lshl_add_u64 v[92:93], s[36:37], 0, v[92:93]
	v_lshl_add_u64 v[80:81], s[36:37], 0, v[80:81]
	v_lshl_add_u64 v[76:77], s[36:37], 0, v[76:77]
	v_subb_co_u32_e32 v73, vcc, v139, v73, vcc
	v_lshl_add_u64 v[36:37], s[36:37], 0, v[36:37]
	v_cvt_f32_i32_e32 v31, v31
	v_cvt_f32_i32_e32 v30, v30
	v_lshl_add_u64 v[92:93], v[92:93], 0, s[6:7]
	v_lshl_add_u64 v[80:81], v[80:81], 0, s[6:7]
	v_lshl_add_u64 v[76:77], v[76:77], 0, s[6:7]
	v_lshlrev_b64 v[72:73], 1, v[72:73]
	v_lshl_add_u64 v[36:37], v[36:37], 0, s[6:7]
	v_lshl_add_u64 v[96:97], v[96:97], 0, v[94:95]
	v_lshl_add_u64 v[92:93], v[92:93], 0, v[94:95]
	v_lshl_add_u64 v[88:89], v[88:89], 0, v[94:95]
	v_lshl_add_u64 v[80:81], v[80:81], 0, v[94:95]
	v_lshl_add_u64 v[76:77], v[76:77], 0, v[94:95]
	v_cvt_f32_i32_e32 v59, v59
	v_cvt_f32_i32_e32 v58, v58
	v_cvt_f32_i32_e32 v61, v61
	v_cvt_f32_i32_e32 v60, v60
	v_cvt_f32_i32_e32 v55, v55
	v_cvt_f32_i32_e32 v54, v54
	v_cvt_f32_i32_e32 v57, v57
	v_cvt_f32_i32_e32 v56, v56
	v_cvt_f32_i32_e32 v51, v51
	v_cvt_f32_i32_e32 v50, v50
	v_cvt_f32_i32_e32 v53, v53
	v_cvt_f32_i32_e32 v52, v52
	v_cvt_f32_i32_e32 v47, v47
	v_cvt_f32_i32_e32 v46, v46
	v_cvt_f32_i32_e32 v49, v49
	v_cvt_f32_i32_e32 v48, v48
	v_cvt_f32_i32_e32 v43, v43
	v_cvt_f32_i32_e32 v42, v42
	v_cvt_f32_i32_e32 v45, v45
	v_cvt_f32_i32_e32 v44, v44
	v_cvt_f32_i32_e32 v39, v39
	v_cvt_f32_i32_e32 v38, v38
	v_cvt_f32_i32_e32 v41, v41
	v_cvt_f32_i32_e32 v40, v40
	v_lshl_add_u64 v[36:37], v[36:37], 0, v[72:73]
	v_cvt_f32_i32_e32 v7, v7
	v_cvt_f32_i32_e32 v6, v6
	v_cvt_f32_i32_e32 v9, v9
	v_cvt_f32_i32_e32 v8, v8
	global_store_dwordx2 v[96:97], v[100:101], off offset:32
; template <bool I8, class Epi> ...
;     ...
;   for (int i = 0; i < 4; ++i) {
;     const int row = m0 + wm * 64 + i * 16 + (lane >> 4) * 4;
;     float4 rs = float4{1.f, 1.f, 1.f, 1.f};
;     if (I8) rs = *reinterpret_cast<const float4*>(rscale + row);
; #pragma unroll
;     for (int j = 0; j < 8; ++j) {
;       const int col = n0 + wn * 128 + j * 16 + (lane & 15);
;       if (I8) {
;         typedef __attribute__((ext_vector_type(4))) int i32x4;
;         const i32x4 ia = __builtin_bit_cast(i32x4, acc[i][j]);
;         const float cs = cscale[col];
;         epi(row, col, f32x4{(float)ia[0] * rs.x * cs, (float)ia[1] * rs.y * cs, (float)ia[2] * rs.z * cs, (float)ia[3] * rs.w * cs});
;       } else {
;         epi(row, col, acc[i][j]);
;       }
;     }
;   }
;   __device__ __forceinline__ void operator()(int row, int col, f32x4 v) const {
;     const int ch = col & 1023, half = col >> 10;
;     const int b = row / seqlen, l = row - b * seqlen;
;     uint2 pk; pk.x = pack2(v[0], v[1]); pk.y = pack2(v[2], v[3]);
;     *reinterpret_cast<uint2*>(ABt + ((size_t)(b * 1024 + ch) * 4096 + half * 2048 + l)) = pk;
;   }
	global_store_dwordx2 v[92:93], v[90:91], off offset:32
	global_store_dwordx2 v[88:89], v[86:87], off offset:32
	global_store_dwordx2 v[80:81], v[78:79], off offset:32
	global_store_dwordx2 v[76:77], v[74:75], off offset:32
	global_store_dwordx2 v[36:37], v[34:35], off offset:64
	v_add_u32_e32 v34, 48, v123
	v_ashrrev_i32_e32 v35, 11, v34
	v_cvt_f32_i32_e32 v33, v33
	v_cvt_f32_i32_e32 v32, v32
	v_pk_mul_f32 v[30:31], v[220:221], v[30:31]
	v_lshlrev_b32_e32 v37, 10, v35
	v_pk_mul_f32 v[30:31], v[224:225], v[30:31] op_sel_hi:[0, 1]
	v_pk_mul_f32 v[66:67], v[216:217], v[66:67]
	v_pk_mul_f32 v[68:69], v[218:219], v[68:69]
	v_pk_mul_f32 v[58:59], v[216:217], v[58:59]
	v_pk_mul_f32 v[60:61], v[218:219], v[60:61]
	v_pk_mul_f32 v[54:55], v[216:217], v[54:55]
	v_pk_mul_f32 v[56:57], v[218:219], v[56:57]
	v_pk_mul_f32 v[50:51], v[216:217], v[50:51]
	v_pk_mul_f32 v[52:53], v[218:219], v[52:53]
	v_pk_mul_f32 v[46:47], v[216:217], v[46:47]
	v_pk_mul_f32 v[48:49], v[218:219], v[48:49]
	v_pk_mul_f32 v[42:43], v[216:217], v[42:43]
	v_pk_mul_f32 v[44:45], v[218:219], v[44:45]
	v_pk_mul_f32 v[38:39], v[216:217], v[38:39]
	v_pk_mul_f32 v[40:41], v[218:219], v[40:41]
	v_and_b32_e32 v36, 0xfffff800, v34
	v_cvt_pk_bf16_f32 v34, v30, v31
	v_or_b32_e32 v30, v37, v141
	v_pk_mul_f32 v[6:7], v[220:221], v[6:7]
	v_pk_mul_f32 v[8:9], v[222:223], v[8:9]
	v_cvt_f32_i32_e32 v3, v3
	v_cvt_f32_i32_e32 v2, v2
	v_cvt_f32_i32_e32 v5, v5
	v_cvt_f32_i32_e32 v4, v4
	v_pk_mul_f32 v[66:67], v[224:225], v[66:67] op_sel_hi:[0, 1]
	v_pk_mul_f32 v[68:69], v[224:225], v[68:69] op_sel_hi:[0, 1]
	v_pk_mul_f32 v[58:59], v[226:227], v[58:59] op_sel_hi:[0, 1]
	v_pk_mul_f32 v[60:61], v[226:227], v[60:61] op_sel_hi:[0, 1]
	v_pk_mul_f32 v[54:55], v[228:229], v[54:55] op_sel_hi:[0, 1]
	v_pk_mul_f32 v[56:57], v[228:229], v[56:57] op_sel_hi:[0, 1]
	v_pk_mul_f32 v[50:51], v[230:231], v[50:51] op_sel_hi:[0, 1]
	v_pk_mul_f32 v[52:53], v[230:231], v[52:53] op_sel_hi:[0, 1]
	v_pk_mul_f32 v[46:47], v[232:233], v[46:47] op_sel_hi:[0, 1]
	v_pk_mul_f32 v[48:49], v[232:233], v[48:49] op_sel_hi:[0, 1]
	v_pk_mul_f32 v[42:43], v[234:235], v[42:43] op_sel_hi:[0, 1]
	v_pk_mul_f32 v[44:45], v[234:235], v[44:45] op_sel_hi:[0, 1]
	v_pk_mul_f32 v[38:39], v[236:237], v[38:39] op_sel_hi:[0, 1]
	v_pk_mul_f32 v[40:41], v[236:237], v[40:41] op_sel_hi:[0, 1]
	v_ashrrev_i32_e32 v31, 31, v30
	v_pk_mul_f32 v[6:7], v[234:235], v[6:7] op_sel_hi:[0, 1]
	v_pk_mul_f32 v[8:9], v[234:235], v[8:9] op_sel_hi:[0, 1]
	v_cvt_pk_bf16_f32 v66, v66, v67
	v_cvt_pk_bf16_f32 v67, v68, v69
	v_or_b32_e32 v68, v70, v141
	v_cvt_pk_bf16_f32 v58, v58, v59
	v_cvt_pk_bf16_f32 v59, v60, v61
	v_or_b32_e32 v60, v70, v121
	v_cvt_pk_bf16_f32 v54, v54, v55
	v_cvt_pk_bf16_f32 v55, v56, v57
	v_or_b32_e32 v56, v70, v119
	v_cvt_pk_bf16_f32 v50, v50, v51
	v_cvt_pk_bf16_f32 v51, v52, v53
	v_or_b32_e32 v52, v70, v125
	v_cvt_pk_bf16_f32 v46, v46, v47
	v_cvt_pk_bf16_f32 v47, v48, v49
	v_or_b32_e32 v48, v70, v110
	v_cvt_pk_bf16_f32 v42, v42, v43
	v_cvt_pk_bf16_f32 v43, v44, v45
	v_or_b32_e32 v44, v70, v106
	v_cvt_pk_bf16_f32 v38, v38, v39
	v_cvt_pk_bf16_f32 v39, v40, v41
	v_or_b32_e32 v40, v70, v102
	v_pk_mul_f32 v[32:33], v[222:223], v[32:33]
	v_lshlrev_b64 v[30:31], 13, v[30:31]
	v_cvt_pk_bf16_f32 v6, v6, v7
	v_cvt_pk_bf16_f32 v7, v8, v9
	v_or_b32_e32 v8, v37, v106
	v_ashrrev_i32_e32 v69, 31, v68
	v_ashrrev_i32_e32 v61, 31, v60
	v_ashrrev_i32_e32 v57, 31, v56
	v_ashrrev_i32_e32 v53, 31, v52
	v_ashrrev_i32_e32 v49, 31, v48
	v_ashrrev_i32_e32 v45, 31, v44
	v_ashrrev_i32_e32 v41, 31, v40
	v_pk_mul_f32 v[32:33], v[224:225], v[32:33] op_sel_hi:[0, 1]
	v_lshl_add_u64 v[30:31], s[36:37], 0, v[30:31]
	v_ashrrev_i32_e32 v9, 31, v8
	v_lshlrev_b64 v[68:69], 13, v[68:69]
	v_lshlrev_b64 v[60:61], 13, v[60:61]
	v_lshlrev_b64 v[56:57], 13, v[56:57]
	v_lshlrev_b64 v[52:53], 13, v[52:53]
	v_lshlrev_b64 v[48:49], 13, v[48:49]
	v_lshlrev_b64 v[44:45], 13, v[44:45]
	v_lshlrev_b64 v[40:41], 13, v[40:41]
	v_cvt_pk_bf16_f32 v35, v32, v33
	v_lshl_add_u64 v[32:33], v[30:31], 0, s[6:7]
	v_ashrrev_i32_e32 v31, 31, v36
	v_sub_co_u32_e32 v30, vcc, v138, v36
	v_lshlrev_b64 v[8:9], 13, v[8:9]
	v_pk_mul_f32 v[2:3], v[220:221], v[2:3]
	v_pk_mul_f32 v[4:5], v[222:223], v[4:5]
	v_lshl_add_u64 v[68:69], s[36:37], 0, v[68:69]
	v_lshl_add_u64 v[60:61], s[36:37], 0, v[60:61]
	v_lshl_add_u64 v[56:57], s[36:37], 0, v[56:57]
	v_lshl_add_u64 v[52:53], s[36:37], 0, v[52:53]
	v_lshl_add_u64 v[48:49], s[36:37], 0, v[48:49]
	v_lshl_add_u64 v[44:45], s[36:37], 0, v[44:45]
	v_lshl_add_u64 v[40:41], s[36:37], 0, v[40:41]
	v_subb_co_u32_e32 v31, vcc, v139, v31, vcc
	v_lshl_add_u64 v[8:9], s[36:37], 0, v[8:9]
	v_pk_mul_f32 v[2:3], v[236:237], v[2:3] op_sel_hi:[0, 1]
	v_pk_mul_f32 v[4:5], v[236:237], v[4:5] op_sel_hi:[0, 1]
	v_lshl_add_u64 v[68:69], v[68:69], 0, s[6:7]
	v_lshl_add_u64 v[60:61], v[60:61], 0, s[6:7]
	v_lshl_add_u64 v[56:57], v[56:57], 0, s[6:7]
	v_lshl_add_u64 v[52:53], v[52:53], 0, s[6:7]
; template <bool I8, class Epi> ...
;     ...
;   for (int i = 0; i < 4; ++i) {
;     const int row = m0 + wm * 64 + i * 16 + (lane >> 4) * 4;
;     float4 rs = float4{1.f, 1.f, 1.f, 1.f};
;     if (I8) rs = *reinterpret_cast<const float4*>(rscale + row);
; #pragma unroll
;     for (int j = 0; j < 8; ++j) {
;       const int col = n0 + wn * 128 + j * 16 + (lane & 15);
;       if (I8) {
;         typedef __attribute__((ext_vector_type(4))) int i32x4;
;         const i32x4 ia = __builtin_bit_cast(i32x4, acc[i][j]);
;         const float cs = cscale[col];
;         epi(row, col, f32x4{(float)ia[0] * rs.x * cs, (float)ia[1] * rs.y * cs, (float)ia[2] * rs.z * cs, (float)ia[3] * rs.w * cs});
;       } else {
;         epi(row, col, acc[i][j]);
;       }
;     }
;   }
;   __device__ __forceinline__ void operator()(int row, int col, f32x4 v) const {
;     const int ch = col & 1023, half = col >> 10;
;     const int b = row / seqlen, l = row - b * seqlen;
;     uint2 pk; pk.x = pack2(v[0], v[1]); pk.y = pack2(v[2], v[3]);
;     *reinterpret_cast<uint2*>(ABt + ((size_t)(b * 1024 + ch) * 4096 + half * 2048 + l)) = pk;
;   }
	v_lshl_add_u64 v[48:49], v[48:49], 0, s[6:7]
	v_lshl_add_u64 v[44:45], v[44:45], 0, s[6:7]
	v_lshl_add_u64 v[40:41], v[40:41], 0, s[6:7]
	v_lshlrev_b64 v[30:31], 1, v[30:31]
	v_lshl_add_u64 v[8:9], v[8:9], 0, s[6:7]
	v_cvt_pk_bf16_f32 v2, v2, v3
	v_cvt_pk_bf16_f32 v3, v4, v5
	v_or_b32_e32 v4, v37, v102
	v_lshl_add_u64 v[68:69], v[68:69], 0, v[72:73]
	v_lshl_add_u64 v[60:61], v[60:61], 0, v[72:73]
	v_lshl_add_u64 v[56:57], v[56:57], 0, v[72:73]
	v_lshl_add_u64 v[52:53], v[52:53], 0, v[72:73]
	v_lshl_add_u64 v[48:49], v[48:49], 0, v[72:73]
	v_lshl_add_u64 v[44:45], v[44:45], 0, v[72:73]
	v_lshl_add_u64 v[40:41], v[40:41], 0, v[72:73]
	v_lshl_add_u64 v[8:9], v[8:9], 0, v[30:31]
	v_ashrrev_i32_e32 v5, 31, v4
	global_store_dwordx2 v[68:69], v[66:67], off offset:64
	global_store_dwordx2 v[60:61], v[58:59], off offset:64
	global_store_dwordx2 v[56:57], v[54:55], off offset:64
	global_store_dwordx2 v[52:53], v[50:51], off offset:64
	global_store_dwordx2 v[48:49], v[46:47], off offset:64
	global_store_dwordx2 v[44:45], v[42:43], off offset:64
	global_store_dwordx2 v[40:41], v[38:39], off offset:64
	v_cvt_f32_i32_e32 v27, v27
	v_cvt_f32_i32_e32 v26, v26
	v_cvt_f32_i32_e32 v29, v29
	v_cvt_f32_i32_e32 v28, v28
	v_cvt_f32_i32_e32 v23, v23
	v_cvt_f32_i32_e32 v22, v22
	v_cvt_f32_i32_e32 v25, v25
	v_cvt_f32_i32_e32 v24, v24
	v_cvt_f32_i32_e32 v19, v19
	v_cvt_f32_i32_e32 v18, v18
	v_cvt_f32_i32_e32 v21, v21
	v_cvt_f32_i32_e32 v20, v20
	v_cvt_f32_i32_e32 v15, v15
	v_cvt_f32_i32_e32 v14, v14
	v_cvt_f32_i32_e32 v17, v17
	v_cvt_f32_i32_e32 v16, v16
	global_store_dwordx2 v[8:9], v[6:7], off offset:96
	v_lshlrev_b64 v[4:5], 13, v[4:5]
	v_cvt_f32_i32_e32 v7, v11
	v_cvt_f32_i32_e32 v6, v10
	v_cvt_f32_i32_e32 v9, v13
	v_cvt_f32_i32_e32 v8, v12
	v_lshl_add_u64 v[4:5], s[36:37], 0, v[4:5]
	v_lshl_add_u64 v[4:5], v[4:5], 0, s[6:7]
	v_lshl_add_u64 v[4:5], v[4:5], 0, v[30:31]
	v_pk_mul_f32 v[26:27], v[220:221], v[26:27]
	v_pk_mul_f32 v[28:29], v[222:223], v[28:29]
	v_pk_mul_f32 v[22:23], v[220:221], v[22:23]
	v_pk_mul_f32 v[24:25], v[222:223], v[24:25]
	v_pk_mul_f32 v[18:19], v[220:221], v[18:19]
	v_pk_mul_f32 v[20:21], v[222:223], v[20:21]
	v_pk_mul_f32 v[14:15], v[220:221], v[14:15]
	v_pk_mul_f32 v[16:17], v[222:223], v[16:17]
	global_store_dwordx2 v[4:5], v[2:3], off offset:96
	v_pk_mul_f32 v[2:3], v[220:221], v[6:7]
	v_pk_mul_f32 v[4:5], v[222:223], v[8:9]
	v_pk_mul_f32 v[26:27], v[226:227], v[26:27] op_sel_hi:[0, 1]
	v_pk_mul_f32 v[28:29], v[226:227], v[28:29] op_sel_hi:[0, 1]
	v_pk_mul_f32 v[22:23], v[228:229], v[22:23] op_sel_hi:[0, 1]
	v_pk_mul_f32 v[24:25], v[228:229], v[24:25] op_sel_hi:[0, 1]
	v_pk_mul_f32 v[18:19], v[230:231], v[18:19] op_sel_hi:[0, 1]
	v_pk_mul_f32 v[20:21], v[230:231], v[20:21] op_sel_hi:[0, 1]
	v_pk_mul_f32 v[14:15], v[232:233], v[14:15] op_sel_hi:[0, 1]
	v_pk_mul_f32 v[16:17], v[232:233], v[16:17] op_sel_hi:[0, 1]
	v_pk_mul_f32 v[2:3], v[238:239], v[2:3] op_sel_hi:[0, 1]
	v_pk_mul_f32 v[4:5], v[238:239], v[4:5] op_sel_hi:[0, 1]
	v_cvt_pk_bf16_f32 v26, v26, v27
	v_cvt_pk_bf16_f32 v27, v28, v29
	v_or_b32_e32 v28, v37, v121
	v_cvt_pk_bf16_f32 v22, v22, v23
	v_cvt_pk_bf16_f32 v23, v24, v25
	v_or_b32_e32 v24, v37, v119
	v_cvt_pk_bf16_f32 v18, v18, v19
	v_cvt_pk_bf16_f32 v19, v20, v21
	v_or_b32_e32 v20, v37, v125
	v_cvt_pk_bf16_f32 v14, v14, v15
	v_cvt_pk_bf16_f32 v15, v16, v17
	v_or_b32_e32 v16, v37, v110
	v_cvt_pk_bf16_f32 v2, v2, v3
	v_cvt_pk_bf16_f32 v3, v4, v5
	v_or_b32_e32 v4, v37, v98
	v_ashrrev_i32_e32 v29, 31, v28
	v_ashrrev_i32_e32 v25, 31, v24
	v_ashrrev_i32_e32 v21, 31, v20
	v_ashrrev_i32_e32 v17, 31, v16
	v_ashrrev_i32_e32 v5, 31, v4
	v_lshlrev_b64 v[28:29], 13, v[28:29]
	v_lshlrev_b64 v[24:25], 13, v[24:25]
	v_lshlrev_b64 v[20:21], 13, v[20:21]
	v_lshlrev_b64 v[16:17], 13, v[16:17]
	v_lshlrev_b64 v[4:5], 13, v[4:5]
	v_lshl_add_u64 v[28:29], s[36:37], 0, v[28:29]
	v_lshl_add_u64 v[24:25], s[36:37], 0, v[24:25]
	v_lshl_add_u64 v[20:21], s[36:37], 0, v[20:21]
	v_lshl_add_u64 v[16:17], s[36:37], 0, v[16:17]
	v_lshl_add_u64 v[4:5], s[36:37], 0, v[4:5]
	v_lshl_add_u64 v[28:29], v[28:29], 0, s[6:7]
	v_lshl_add_u64 v[24:25], v[24:25], 0, s[6:7]
	v_lshl_add_u64 v[20:21], v[20:21], 0, s[6:7]
	v_lshl_add_u64 v[16:17], v[16:17], 0, s[6:7]
	v_lshl_add_u64 v[4:5], v[4:5], 0, s[6:7]
	v_lshl_add_u64 v[32:33], v[32:33], 0, v[30:31]
	v_lshl_add_u64 v[28:29], v[28:29], 0, v[30:31]
	v_lshl_add_u64 v[24:25], v[24:25], 0, v[30:31]
	v_lshl_add_u64 v[20:21], v[20:21], 0, v[30:31]
	v_lshl_add_u64 v[16:17], v[16:17], 0, v[30:31]
	v_lshl_add_u64 v[4:5], v[4:5], 0, v[30:31]
	global_store_dwordx2 v[32:33], v[34:35], off offset:96
	global_store_dwordx2 v[28:29], v[26:27], off offset:96
	global_store_dwordx2 v[24:25], v[22:23], off offset:96
	global_store_dwordx2 v[20:21], v[18:19], off offset:96
	global_store_dwordx2 v[16:17], v[14:15], off offset:96
	global_store_dwordx2 v[4:5], v[2:3], off offset:96
	s_branch .LBB0_233

; __device__ __forceinline__ int opaque_tid() { int t = threadIdx.x; asm volatile("" : "+v"(t)); return t; }
; template <bool I8>
; __device__ __forceinline__ void gemm_mainloop_n256(const bf16_t* __restrict__ A, int lda, const bf16_t* __restrict__ Bt, int ldb,
;                                                    int K, int m0, int n0, f32x4 (&acc)[4][8], char* smem) {
;   const int tid = opaque_tid(), lane = tid & 63, w = tid >> 6;
;   const int wm = w >> 1, wn = w & 1;
; #pragma unroll
;   for (int i = 0; i < 4; ++i)
; #pragma unroll
;     for (int j = 0; j < 8; ++j) acc[i][j] = f32x4{0.f, 0.f, 0.f, 0.f};
;   const int nk = K / 64;
;   const int rowoff = lane >> 3, lch = (lane & 7) ^ rowoff;
;   const bf16_t* gA = A + (size_t)(m0 + w * 8 + rowoff) * lda + lch * 8;
;   const bf16_t* gB = Bt + (size_t)(n0 + w * 8 + rowoff) * ldb + lch * 8;
;   const int fr = lane & 15, fq = lane >> 4;
; __device__ void phase_outproj(KParams& p, int bid, int nb, char* smem) {
;     ...
;   for (int it = start; it < end; it += step) {
;     const int x = aware ? (bid & 7) : (it >> 6), s_ = aware ? it : (it & 63);
;     EpiBf16 epi{reinterpret_cast<bf16_t*>(p.y_x), D};
;     gemm_tile_n256<true>(a8, D / 2, b8, D / 2, D / 2, (8 * x + (s_ & 7)) * 128, (s_ >> 3) * 256, epi, smem, p.yscale, p.woscale);
.LBB0_1069:
	s_lshr_b32 s50, s3, 6
	s_and_b64 s[40:41], s[48:49], exec
	s_cselect_b32 s50, s43, s50
	s_and_b32 s51, s3, 63
	s_and_b64 s[40:41], s[48:49], exec
	v_mov_b32_e32 v2, v0
	s_cselect_b32 s40, s3, s51
	s_lshl_b32 s41, s40, 7
	v_ashrrev_i32_e32 v3, 6, v2
	v_bfe_u32 v4, v2, 3, 3
	v_bfe_u32 v9, v2, 4, 2
	s_lshl_b32 s40, s40, 5
	v_and_b32_e32 v5, 7, v2
	v_bitop3_b32 v6, v4, v2, 7 bitop3:0x78
	v_lshlrev_b32_e32 v7, 3, v3
	v_and_b32_e32 v8, 15, v2
	v_lshlrev_b32_e32 v136, 10, v3
	v_lshrrev_b32_e32 v10, 1, v2
	v_lshlrev_b32_e32 v3, 7, v3
	v_bitop3_b32 v2, v9, v2, 7 bitop3:0x78
	s_lshl_b32 s51, s50, 10
	s_and_b32 s50, s40, 0xffffff00
	v_and_or_b32 v10, v10, s47, v8
	v_and_or_b32 v3, v3, s46, v8
	v_lshlrev_b32_e32 v8, 4, v2
	v_bitop3_b32 v2, v9, v5, 4 bitop3:0x36
	v_lshlrev_b32_e32 v5, 4, v2
	v_or_b32_e32 v2, s50, v4
	v_add_u32_e32 v2, v2, v7
	v_lshlrev_b32_e32 v11, 7, v3
	v_ashrrev_i32_e32 v3, 31, v2
	v_lshlrev_b64 v[2:3], 11, v[2:3]
	v_lshlrev_b32_e32 v6, 4, v6
	v_or_b32_e32 v2, v2, v6
	s_and_b32 s52, s41, 0x380
	s_waitcnt lgkmcnt(0)
	v_lshl_add_u64 v[130:131], s[14:15], 0, v[2:3]
	v_or_b32_e32 v2, s51, v4
	v_or_b32_e32 v2, s52, v2
	v_add_u32_e32 v2, v2, v7
	v_ashrrev_i32_e32 v3, 31, v2
	v_lshlrev_b64 v[2:3], 11, v[2:3]
	v_lshlrev_b32_e32 v10, 7, v10
	v_or_b32_e32 v2, v2, v6
	v_mov_b32_e32 v14, 0
	v_lshl_add_u64 v[132:133], s[12:13], 0, v[2:3]
	s_mov_b64 s[40:41], 0
	v_add_u32_e32 v137, 0x1000, v136
	v_add_u32_e32 v138, 0x2000, v136
	v_add_u32_e32 v139, 0x3000, v136
	v_add_u32_e32 v141, 0x4000, v136
	v_add_u32_e32 v142, 0x5000, v136
	v_add_u32_e32 v143, 0x6000, v136
	v_add_u32_e32 v144, 0x7000, v136
	v_add_u32_e32 v145, 0x8000, v136
	v_add_u32_e32 v146, 0x9000, v136
	v_add_u32_e32 v147, 0xa000, v136
	v_add_u32_e32 v148, 0xb000, v136
	v_add_u32_e32 v149, v8, v10
	v_add_u32_e32 v150, v8, v11
	v_add_u32_e32 v151, v5, v10
	v_add_u32_e32 v152, v5, v11
	v_mov_b32_e32 v15, v14
	v_mov_b32_e32 v16, v14
	v_mov_b32_e32 v17, v14
	v_mov_b32_e32 v2, v14
	v_mov_b32_e32 v3, v14
	v_mov_b32_e32 v4, v14
	v_mov_b32_e32 v5, v14
	v_mov_b32_e32 v6, v14
	v_mov_b32_e32 v7, v14
	v_mov_b32_e32 v8, v14
	v_mov_b32_e32 v9, v14
	v_mov_b32_e32 v10, v14
	v_mov_b32_e32 v11, v14
	v_mov_b32_e32 v12, v14
	v_mov_b32_e32 v13, v14
	v_mov_b32_e32 v18, v14
	v_mov_b32_e32 v19, v14
	v_mov_b32_e32 v20, v14
	v_mov_b32_e32 v21, v14
	v_mov_b32_e32 v22, v14
	v_mov_b32_e32 v23, v14
	v_mov_b32_e32 v24, v14
	v_mov_b32_e32 v25, v14
	v_mov_b32_e32 v26, v14
	v_mov_b32_e32 v27, v14
	v_mov_b32_e32 v28, v14
	v_mov_b32_e32 v29, v14
	v_mov_b32_e32 v30, v14
	v_mov_b32_e32 v31, v14
	v_mov_b32_e32 v32, v14
	v_mov_b32_e32 v33, v14
	v_mov_b32_e32 v34, v14
	v_mov_b32_e32 v35, v14
	v_mov_b32_e32 v36, v14
	v_mov_b32_e32 v37, v14
	v_mov_b32_e32 v38, v14
	v_mov_b32_e32 v39, v14
	v_mov_b32_e32 v40, v14
	v_mov_b32_e32 v41, v14
	v_mov_b32_e32 v42, v14
	v_mov_b32_e32 v43, v14
	v_mov_b32_e32 v44, v14
	v_mov_b32_e32 v45, v14
	v_mov_b32_e32 v46, v14
	v_mov_b32_e32 v47, v14
	v_mov_b32_e32 v48, v14
	v_mov_b32_e32 v49, v14
	v_mov_b32_e32 v50, v14
	v_mov_b32_e32 v51, v14
	v_mov_b32_e32 v52, v14
	v_mov_b32_e32 v53, v14
	v_mov_b32_e32 v54, v14
	v_mov_b32_e32 v55, v14
	v_mov_b32_e32 v56, v14
	v_mov_b32_e32 v57, v14
	v_mov_b32_e32 v58, v14
	v_mov_b32_e32 v59, v14
	v_mov_b32_e32 v60, v14
	v_mov_b32_e32 v61, v14
	v_mov_b32_e32 v62, v14
	v_mov_b32_e32 v63, v14
	v_mov_b32_e32 v64, v14
	v_mov_b32_e32 v65, v14
	v_mov_b32_e32 v66, v14
	v_mov_b32_e32 v67, v14
	v_mov_b32_e32 v68, v14
	v_mov_b32_e32 v69, v14
	v_mov_b32_e32 v70, v14
	v_mov_b32_e32 v71, v14
	v_mov_b32_e32 v72, v14
	v_mov_b32_e32 v73, v14
	v_mov_b32_e32 v74, v14
	v_mov_b32_e32 v75, v14
	v_mov_b32_e32 v76, v14
	v_mov_b32_e32 v77, v14
	v_mov_b32_e32 v78, v14
	v_mov_b32_e32 v79, v14
	v_mov_b32_e32 v80, v14
	v_mov_b32_e32 v81, v14
	v_mov_b32_e32 v82, v14
	v_mov_b32_e32 v83, v14
	v_mov_b32_e32 v84, v14
	v_mov_b32_e32 v85, v14
	v_mov_b32_e32 v86, v14
	v_mov_b32_e32 v87, v14
	v_mov_b32_e32 v88, v14
	v_mov_b32_e32 v89, v14
	v_mov_b32_e32 v90, v14
	v_mov_b32_e32 v91, v14
	v_mov_b32_e32 v92, v14
	v_mov_b32_e32 v93, v14
	v_mov_b32_e32 v94, v14
	v_mov_b32_e32 v95, v14
	v_mov_b32_e32 v96, v14
	v_mov_b32_e32 v97, v14
	v_mov_b32_e32 v98, v14
	v_mov_b32_e32 v99, v14
	v_mov_b32_e32 v100, v14
	v_mov_b32_e32 v101, v14
	v_mov_b32_e32 v102, v14
	v_mov_b32_e32 v103, v14
	v_mov_b32_e32 v104, v14
	v_mov_b32_e32 v105, v14
	v_mov_b32_e32 v106, v14
	v_mov_b32_e32 v107, v14
	v_mov_b32_e32 v108, v14
	v_mov_b32_e32 v109, v14
	v_mov_b32_e32 v110, v14
	v_mov_b32_e32 v111, v14
	v_mov_b32_e32 v112, v14
	v_mov_b32_e32 v113, v14
	v_mov_b32_e32 v114, v14
	v_mov_b32_e32 v115, v14
	v_mov_b32_e32 v116, v14
	v_mov_b32_e32 v117, v14
	v_mov_b32_e32 v118, v14
	v_mov_b32_e32 v119, v14
	v_mov_b32_e32 v120, v14
	v_mov_b32_e32 v121, v14
	v_mov_b32_e32 v122, v14
	v_mov_b32_e32 v123, v14
	v_mov_b32_e32 v124, v14
	v_mov_b32_e32 v125, v14
	v_mov_b32_e32 v126, v14
	v_mov_b32_e32 v127, v14
	v_mov_b32_e32 v128, v14
	v_mov_b32_e32 v129, v14
	s_or_b32 s99, s52, s51
	v_add_u32_e32 v240, s99, v1
	v_ashrrev_i32_e32 v241, 31, v240
	v_or_b32_e32 v242, s50, v135
	v_lshl_add_u64 v[244:245], v[240:241], 2, s[16:17]
	v_ashrrev_i32_e32 v243, 31, v242
	v_lshl_add_u64 v[246:247], v[242:243], 2, s[18:19]
	global_load_dwordx4 v[208:211], v[244:245], off
	global_load_dwordx4 v[212:215], v[244:245], off offset:64
	global_load_dwordx4 v[216:219], v[244:245], off offset:128
	global_load_dwordx4 v[220:223], v[244:245], off offset:192
	global_load_dword v224, v[246:247], off
	global_load_dword v226, v[246:247], off offset:64
	global_load_dword v228, v[246:247], off offset:128
	global_load_dword v230, v[246:247], off offset:192
	global_load_dword v232, v[246:247], off offset:256
	global_load_dword v234, v[246:247], off offset:320
	global_load_dword v236, v[246:247], off offset:384
	global_load_dword v238, v[246:247], off offset:448
; template <bool I8>
; __device__ __forceinline__ void gemm_mainloop_n256(const bf16_t* __restrict__ A, int lda, const bf16_t* __restrict__ Bt, int ldb,
;                                                    int K, int m0, int n0, f32x4 (&acc)[4][8], char* smem) {
;     ...
;   for (int kt = 0; kt < nk; ++kt) {
; #pragma unroll
;     for (int i_ = 0; i_ < 4; ++i_)
;       __builtin_amdgcn_global_load_lds((const unsigned*)(gA + (size_t)(i_ * 32) * lda + kt * 64),
;                                        (unsigned*)(smem + (i_ * 4 + w) * 1024), 16, 0, 0);
; #pragma unroll
;     for (int i_ = 0; i_ < 8; ++i_)
;       __builtin_amdgcn_global_load_lds((const unsigned*)(gB + (size_t)(i_ * 32) * ldb + kt * 64),
;                                        (unsigned*)(smem + 16384 + (i_ * 4 + w) * 1024), 16, 0, 0);
;     asm volatile("s_waitcnt vmcnt(0)" ::: "memory");
;     __syncthreads();
;     const char* sA = smem;
;     const char* sB = smem + 16384;
; #pragma unroll
;     for (int kk = 0; kk < 2; ++kk) {
;       bf16x8 af[4], bfr[8];
;       const int ch = kk * 4 + fq;
; #pragma unroll
;       for (int i = 0; i < 4; ++i) {
;         const int row = wm * 64 + i * 16 + fr;
;         af[i] = *reinterpret_cast<const bf16x8*>(sA + row * 128 + ((ch ^ (row & 7)) << 4));
;       }
; #pragma unroll
;       for (int j = 0; j < 8; ++j) {
;         const int col = wn * 128 + j * 16 + fr;
;         bfr[j] = *reinterpret_cast<const bf16x8*>(sB + col * 128 + ((ch ^ (col & 7)) << 4));
;       }
; #pragma unroll
;       for (int i = 0; i < 4; ++i)
; #pragma unroll
;         for (int j = 0; j < 8; ++j) {
;           if (I8) {
;             typedef __attribute__((ext_vector_type(4))) int i32x4;
;             acc[i][j] = __builtin_bit_cast(f32x4, __builtin_amdgcn_mfma_i32_16x16x64_i8(__builtin_bit_cast(i32x4, af[i]), __builtin_bit_cast(i32x4, bfr[j]),
;                                                                                          __builtin_bit_cast(i32x4, acc[i][j]), 0, 0, 0));
;           } else {
;             acc[i][j] = __builtin_amdgcn_mfma_f32_16x16x32_bf16(af[i], bfr[j], acc[i][j], 0, 0, 0);
;           }
;         }
;     }
;     __syncthreads();
;   }
.LBB0_1070:
	v_readfirstlane_b32 s53, v136
	v_lshl_add_u64 v[154:155], v[132:133], 0, s[40:41]
	v_readfirstlane_b32 s54, v137
	s_mov_b32 m0, s53
	v_readfirstlane_b32 s55, v138
	v_lshl_add_u64 v[158:159], v[154:155], 0, s[22:23]
	global_load_lds_dwordx4 v[154:155], off
	s_mov_b32 m0, s54
	v_readfirstlane_b32 s56, v139
	v_lshl_add_u64 v[160:161], v[154:155], 0, s[24:25]
	global_load_lds_dwordx4 v[158:159], off
	s_mov_b32 m0, s55
	v_readfirstlane_b32 s57, v141
	v_lshl_add_u64 v[162:163], v[154:155], 0, s[26:27]
	global_load_lds_dwordx4 v[160:161], off
	s_mov_b32 m0, s56
	v_lshl_add_u64 v[156:157], v[130:131], 0, s[40:41]
	v_readfirstlane_b32 s58, v142
	global_load_lds_dwordx4 v[162:163], off
	s_mov_b32 m0, s57
	v_readfirstlane_b32 s59, v143
	v_lshl_add_u64 v[164:165], v[156:157], 0, s[22:23]
	global_load_lds_dwordx4 v[156:157], off
	s_mov_b32 m0, s58
	v_readfirstlane_b32 s60, v144
	v_lshl_add_u64 v[166:167], v[156:157], 0, s[24:25]
	global_load_lds_dwordx4 v[164:165], off
	s_mov_b32 m0, s59
	v_readfirstlane_b32 s61, v145
	v_lshl_add_u64 v[168:169], v[156:157], 0, s[26:27]
	global_load_lds_dwordx4 v[166:167], off
	s_mov_b32 m0, s60
	v_readfirstlane_b32 s62, v146
	v_lshl_add_u64 v[170:171], v[156:157], 0, s[28:29]
	global_load_lds_dwordx4 v[168:169], off
	s_mov_b32 m0, s61
	v_readfirstlane_b32 s63, v147
	v_lshl_add_u64 v[172:173], v[156:157], 0, s[30:31]
	global_load_lds_dwordx4 v[170:171], off
	s_mov_b32 m0, s62
	v_readfirstlane_b32 s64, v148
	v_lshl_add_u64 v[174:175], v[156:157], 0, s[36:37]
	global_load_lds_dwordx4 v[172:173], off
	s_mov_b32 m0, s63
	v_lshl_add_u64 v[176:177], v[156:157], 0, s[38:39]
	global_load_lds_dwordx4 v[174:175], off
	s_mov_b32 m0, s64
	s_add_u32 s40, s40, 0x80
	global_load_lds_dwordx4 v[176:177], off
	s_waitcnt vmcnt(0)
	s_waitcnt vmcnt(0) lgkmcnt(0)
	s_barrier
	ds_read_b128 v[154:157], v149
	ds_read_b128 v[158:161], v150 offset:16384
	ds_read_b128 v[162:165], v149 offset:2048
	ds_read_b128 v[166:169], v150 offset:18432
	ds_read_b128 v[170:173], v150 offset:20480
	ds_read_b128 v[174:177], v150 offset:22528
	ds_read_b128 v[192:195], v150 offset:24576
	ds_read_b128 v[196:199], v150 offset:26624
	ds_read_b128 v[200:203], v150 offset:28672
	ds_read_b128 v[204:207], v150 offset:30720
	s_waitcnt lgkmcnt(8)
	v_mfma_i32_16x16x64_i8 v[126:129], v[154:157], v[158:161], v[126:129]
	s_addc_u32 s41, s41, 0
	s_cmpk_lg_i32 s40, 0x800
	s_waitcnt lgkmcnt(6)
	v_mfma_i32_16x16x64_i8 v[122:125], v[154:157], v[166:169], v[122:125]
	s_waitcnt lgkmcnt(5)
	v_mfma_i32_16x16x64_i8 v[118:121], v[154:157], v[170:173], v[118:121]
	s_waitcnt lgkmcnt(4)
	v_mfma_i32_16x16x64_i8 v[114:117], v[154:157], v[174:177], v[114:117]
	s_waitcnt lgkmcnt(3)
	v_mfma_i32_16x16x64_i8 v[110:113], v[154:157], v[192:195], v[110:113]
	s_waitcnt lgkmcnt(2)
	v_mfma_i32_16x16x64_i8 v[106:109], v[154:157], v[196:199], v[106:109]
	s_waitcnt lgkmcnt(1)
	v_mfma_i32_16x16x64_i8 v[102:105], v[154:157], v[200:203], v[102:105]
	s_waitcnt lgkmcnt(0)
	v_mfma_i32_16x16x64_i8 v[98:101], v[154:157], v[204:207], v[98:101]
	v_mfma_i32_16x16x64_i8 v[94:97], v[162:165], v[158:161], v[94:97]
	v_mfma_i32_16x16x64_i8 v[90:93], v[162:165], v[166:169], v[90:93]
	v_mfma_i32_16x16x64_i8 v[86:89], v[162:165], v[170:173], v[86:89]
	v_mfma_i32_16x16x64_i8 v[82:85], v[162:165], v[174:177], v[82:85]
	v_mfma_i32_16x16x64_i8 v[78:81], v[162:165], v[192:195], v[78:81]
	v_mfma_i32_16x16x64_i8 v[74:77], v[162:165], v[196:199], v[74:77]
	v_mfma_i32_16x16x64_i8 v[70:73], v[162:165], v[200:203], v[70:73]
	v_mfma_i32_16x16x64_i8 v[66:69], v[162:165], v[204:207], v[66:69]
	ds_read_b128 v[154:157], v149 offset:4096
	ds_read_b128 v[162:165], v149 offset:6144
	s_waitcnt lgkmcnt(1)
	v_mfma_i32_16x16x64_i8 v[62:65], v[154:157], v[158:161], v[62:65]
	v_mfma_i32_16x16x64_i8 v[58:61], v[154:157], v[166:169], v[58:61]
	v_mfma_i32_16x16x64_i8 v[54:57], v[154:157], v[170:173], v[54:57]
	v_mfma_i32_16x16x64_i8 v[50:53], v[154:157], v[174:177], v[50:53]
	v_mfma_i32_16x16x64_i8 v[46:49], v[154:157], v[192:195], v[46:49]
	v_mfma_i32_16x16x64_i8 v[42:45], v[154:157], v[196:199], v[42:45]
	v_mfma_i32_16x16x64_i8 v[38:41], v[154:157], v[200:203], v[38:41]
	v_mfma_i32_16x16x64_i8 v[34:37], v[154:157], v[204:207], v[34:37]
	ds_read_b128 v[154:157], v151
	s_waitcnt lgkmcnt(1)
	v_mfma_i32_16x16x64_i8 v[30:33], v[162:165], v[158:161], v[30:33]
	v_mfma_i32_16x16x64_i8 v[26:29], v[162:165], v[166:169], v[26:29]
	v_mfma_i32_16x16x64_i8 v[22:25], v[162:165], v[170:173], v[22:25]
	v_mfma_i32_16x16x64_i8 v[18:21], v[162:165], v[174:177], v[18:21]
	v_mfma_i32_16x16x64_i8 v[10:13], v[162:165], v[192:195], v[10:13]
	v_mfma_i32_16x16x64_i8 v[6:9], v[162:165], v[196:199], v[6:9]
	v_mfma_i32_16x16x64_i8 v[2:5], v[162:165], v[200:203], v[2:5]
	v_mfma_i32_16x16x64_i8 v[14:17], v[162:165], v[204:207], v[14:17]
	ds_read_b128 v[158:161], v152 offset:16384
	ds_read_b128 v[162:165], v151 offset:2048
	ds_read_b128 v[166:169], v152 offset:18432
	ds_read_b128 v[170:173], v152 offset:20480
	ds_read_b128 v[174:177], v152 offset:22528
	ds_read_b128 v[192:195], v152 offset:24576
	ds_read_b128 v[196:199], v152 offset:26624
	ds_read_b128 v[200:203], v152 offset:28672
	ds_read_b128 v[204:207], v152 offset:30720
	s_waitcnt lgkmcnt(8)
	v_mfma_i32_16x16x64_i8 v[126:129], v[154:157], v[158:161], v[126:129]
	s_waitcnt lgkmcnt(6)
	v_mfma_i32_16x16x64_i8 v[122:125], v[154:157], v[166:169], v[122:125]
	s_waitcnt lgkmcnt(5)
	v_mfma_i32_16x16x64_i8 v[118:121], v[154:157], v[170:173], v[118:121]
	s_waitcnt lgkmcnt(4)
	v_mfma_i32_16x16x64_i8 v[114:117], v[154:157], v[174:177], v[114:117]
	s_waitcnt lgkmcnt(3)
	v_mfma_i32_16x16x64_i8 v[110:113], v[154:157], v[192:195], v[110:113]
	s_waitcnt lgkmcnt(2)
	v_mfma_i32_16x16x64_i8 v[106:109], v[154:157], v[196:199], v[106:109]
	s_waitcnt lgkmcnt(1)
	v_mfma_i32_16x16x64_i8 v[102:105], v[154:157], v[200:203], v[102:105]
	s_waitcnt lgkmcnt(0)
	v_mfma_i32_16x16x64_i8 v[98:101], v[154:157], v[204:207], v[98:101]
	v_mfma_i32_16x16x64_i8 v[94:97], v[162:165], v[158:161], v[94:97]
	v_mfma_i32_16x16x64_i8 v[90:93], v[162:165], v[166:169], v[90:93]
	v_mfma_i32_16x16x64_i8 v[86:89], v[162:165], v[170:173], v[86:89]
	v_mfma_i32_16x16x64_i8 v[82:85], v[162:165], v[174:177], v[82:85]
	v_mfma_i32_16x16x64_i8 v[78:81], v[162:165], v[192:195], v[78:81]
	v_mfma_i32_16x16x64_i8 v[74:77], v[162:165], v[196:199], v[74:77]
	v_mfma_i32_16x16x64_i8 v[70:73], v[162:165], v[200:203], v[70:73]
	v_mfma_i32_16x16x64_i8 v[66:69], v[162:165], v[204:207], v[66:69]
	ds_read_b128 v[154:157], v151 offset:4096
	ds_read_b128 v[162:165], v151 offset:6144
	s_waitcnt lgkmcnt(0)
	s_barrier
; template <bool I8>
; __device__ __forceinline__ void gemm_mainloop_n256(const bf16_t* __restrict__ A, int lda, const bf16_t* __restrict__ Bt, int ldb,
;                                                    int K, int m0, int n0, f32x4 (&acc)[4][8], char* smem) {
;     ...
;       for (int i = 0; i < 4; ++i)
; #pragma unroll
;         for (int j = 0; j < 8; ++j) {
;           if (I8) {
;             typedef __attribute__((ext_vector_type(4))) int i32x4;
;             acc[i][j] = __builtin_bit_cast(f32x4, __builtin_amdgcn_mfma_i32_16x16x64_i8(__builtin_bit_cast(i32x4, af[i]), __builtin_bit_cast(i32x4, bfr[j]),
;                                                                                          __builtin_bit_cast(i32x4, acc[i][j]), 0, 0, 0));
;           } else {
;             acc[i][j] = __builtin_amdgcn_mfma_f32_16x16x32_bf16(af[i], bfr[j], acc[i][j], 0, 0, 0);
;           }
;         }
;     }
;     __syncthreads();
;   }
; template <bool I8, class Epi> ...
;     ...
; #pragma unroll
;   for (int i = 0; i < 4; ++i) {
;     const int row = m0 + wm * 64 + i * 16 + (lane >> 4) * 4;
;     float4 rs = float4{1.f, 1.f, 1.f, 1.f};
;     if (I8) rs = *reinterpret_cast<const float4*>(rscale + row);
; #pragma unroll
;     for (int j = 0; j < 8; ++j) {
;       const int col = n0 + wn * 128 + j * 16 + (lane & 15);
;       if (I8) {
;         typedef __attribute__((ext_vector_type(4))) int i32x4;
;         const i32x4 ia = __builtin_bit_cast(i32x4, acc[i][j]);
;         const float cs = cscale[col];
;         epi(row, col, f32x4{(float)ia[0] * rs.x * cs, (float)ia[1] * rs.y * cs, (float)ia[2] * rs.z * cs, (float)ia[3] * rs.w * cs});
;       } else {
;         epi(row, col, acc[i][j]);
;       }
;     }
;   }
	v_mfma_i32_16x16x64_i8 v[62:65], v[154:157], v[158:161], v[62:65]
	v_mfma_i32_16x16x64_i8 v[58:61], v[154:157], v[166:169], v[58:61]
	v_mfma_i32_16x16x64_i8 v[54:57], v[154:157], v[170:173], v[54:57]
	v_mfma_i32_16x16x64_i8 v[50:53], v[154:157], v[174:177], v[50:53]
	v_mfma_i32_16x16x64_i8 v[46:49], v[154:157], v[192:195], v[46:49]
	v_mfma_i32_16x16x64_i8 v[42:45], v[154:157], v[196:199], v[42:45]
	v_mfma_i32_16x16x64_i8 v[38:41], v[154:157], v[200:203], v[38:41]
	v_mfma_i32_16x16x64_i8 v[34:37], v[154:157], v[204:207], v[34:37]
	v_mfma_i32_16x16x64_i8 v[30:33], v[162:165], v[158:161], v[30:33]
	v_mfma_i32_16x16x64_i8 v[26:29], v[162:165], v[166:169], v[26:29]
	v_mfma_i32_16x16x64_i8 v[22:25], v[162:165], v[170:173], v[22:25]
	v_mfma_i32_16x16x64_i8 v[18:21], v[162:165], v[174:177], v[18:21]
	v_mfma_i32_16x16x64_i8 v[10:13], v[162:165], v[192:195], v[10:13]
	v_mfma_i32_16x16x64_i8 v[6:9], v[162:165], v[196:199], v[6:9]
	v_mfma_i32_16x16x64_i8 v[2:5], v[162:165], v[200:203], v[2:5]
	v_mfma_i32_16x16x64_i8 v[14:17], v[162:165], v[204:207], v[14:17]
	s_cbranch_scc1 .LBB0_1070
	s_or_b32 s40, s52, s51
	v_add_u32_e32 v136, s40, v1
	v_ashrrev_i32_e32 v137, 31, v136
	v_or_b32_e32 v144, s50, v135
	v_lshl_add_u64 v[138:139], v[136:137], 2, s[16:17]
	v_ashrrev_i32_e32 v145, 31, v144
	v_lshl_add_u64 v[146:147], v[144:145], 2, s[18:19]
	v_cvt_f32_i32_e32 v152, v126
	v_cvt_f32_i32_e32 v153, v127
	v_cvt_f32_i32_e32 v154, v128
	v_cvt_f32_i32_e32 v157, v124
	v_cvt_f32_i32_e32 v158, v125
	v_cvt_f32_i32_e32 v159, v118
	v_cvt_f32_i32_e32 v161, v120
	v_or_b32_e32 v118, 1, v136
	v_or_b32_e32 v120, 2, v136
	v_cvt_f32_i32_e32 v160, v119
	v_cvt_f32_i32_e32 v162, v121
	v_ashrrev_i32_e32 v119, 31, v118
	v_ashrrev_i32_e32 v121, 31, v120
	v_lshlrev_b64 v[146:147], 12, v[118:119]
	v_lshlrev_b64 v[150:151], 12, v[120:121]
	v_cvt_f32_i32_e32 v106, v106
	v_cvt_f32_i32_e32 v98, v98
	v_cvt_f32_i32_e32 v129, v129
	v_cvt_f32_i32_e32 v155, v122
	v_cvt_f32_i32_e32 v156, v123
	v_cvt_f32_i32_e32 v107, v107
	v_cvt_f32_i32_e32 v99, v99
	v_cvt_f32_i32_e32 v108, v108
	v_cvt_f32_i32_e32 v100, v100
	v_cvt_f32_i32_e32 v109, v109
	v_cvt_f32_i32_e32 v101, v101
	v_or_b32_e32 v148, 3, v136
	v_lshl_add_u64 v[122:123], v[144:145], 1, s[20:21]
	v_lshlrev_b64 v[144:145], 12, v[136:137]
	v_cvt_f32_i32_e32 v102, v102
	v_ashrrev_i32_e32 v149, 31, v148
	v_cvt_f32_i32_e32 v103, v103
	v_cvt_f32_i32_e32 v95, v95
	v_lshl_add_u64 v[144:145], v[122:123], 0, v[144:145]
	v_lshlrev_b64 v[148:149], 12, v[148:149]
	v_cvt_f32_i32_e32 v104, v104
	v_cvt_f32_i32_e32 v94, v94
	v_cvt_f32_i32_e32 v96, v96
	v_lshl_add_u64 v[146:147], v[122:123], 0, v[146:147]
	v_lshl_add_u64 v[150:151], v[122:123], 0, v[150:151]
	v_lshl_add_u64 v[148:149], v[122:123], 0, v[148:149]
	v_cvt_f32_i32_e32 v105, v105
	v_cvt_f32_i32_e32 v97, v97
	v_cvt_f32_i32_e32 v82, v82
	v_cvt_f32_i32_e32 v83, v83
	v_cvt_f32_i32_e32 v84, v84
	v_cvt_f32_i32_e32 v85, v85
	v_cvt_f32_i32_e32 v78, v78
	v_cvt_f32_i32_e32 v79, v79
	v_cvt_f32_i32_e32 v66, v66
	v_cvt_f32_i32_e32 v67, v67
	v_cvt_f32_i32_e32 v68, v68
	v_cvt_f32_i32_e32 v69, v69
	v_cvt_f32_i32_e32 v70, v70
	v_cvt_f32_i32_e32 v71, v71
	v_cvt_f32_i32_e32 v72, v72
	v_cvt_f32_i32_e32 v73, v73
	v_cvt_f32_i32_e32 v74, v74
	v_cvt_f32_i32_e32 v75, v75
	v_cvt_f32_i32_e32 v63, v63
	v_cvt_f32_i32_e32 v76, v76
	v_cvt_f32_i32_e32 v62, v62
	v_cvt_f32_i32_e32 v64, v64
	v_cvt_f32_i32_e32 v77, v77
	v_cvt_f32_i32_e32 v65, v65
	v_cvt_f32_i32_e32 v42, v42
	v_cvt_f32_i32_e32 v34, v34
	v_cvt_f32_i32_e32 v43, v43
	v_cvt_f32_i32_e32 v35, v35
	v_cvt_f32_i32_e32 v44, v44
	v_cvt_f32_i32_e32 v36, v36
	v_cvt_f32_i32_e32 v45, v45
	v_cvt_f32_i32_e32 v37, v37
	v_cvt_f32_i32_e32 v38, v38
	v_mul_f32_e32 v137, v208, v152
	v_mul_f32_e32 v106, v208, v106
	v_mul_f32_e32 v98, v208, v98
	v_mul_f32_e32 v152, v209, v153
	v_mul_f32_e32 v153, v210, v154
	v_mul_f32_e32 v129, v211, v129
	v_mul_f32_e32 v154, v208, v155
	v_mul_f32_e32 v155, v209, v156
	v_mul_f32_e32 v156, v210, v157
	v_mul_f32_e32 v157, v211, v158
	v_mul_f32_e32 v158, v208, v159
	v_mul_f32_e32 v159, v209, v160
	v_mul_f32_e32 v137, v137, v224
	v_mul_f32_e32 v106, v106, v234
	v_mul_f32_e32 v107, v209, v107
	v_mul_f32_e32 v98, v98, v238
	v_mul_f32_e32 v99, v209, v99
	v_mul_f32_e32 v152, v152, v224
	v_mul_f32_e32 v153, v153, v224
	v_mul_f32_e32 v129, v224, v129
	v_mul_f32_e32 v154, v154, v226
	v_mul_f32_e32 v155, v155, v226
	v_mul_f32_e32 v156, v156, v226
	v_mul_f32_e32 v157, v157, v226
	v_mul_f32_e32 v158, v158, v228
	v_mul_f32_e32 v159, v159, v228
	v_cvt_pk_bf16_f32 v137, v137, s0
	v_mul_f32_e32 v107, v107, v234
	v_mul_f32_e32 v108, v210, v108
	v_cvt_pk_bf16_f32 v106, v106, s0
	v_mul_f32_e32 v99, v99, v238
	v_mul_f32_e32 v100, v210, v100
	v_cvt_pk_bf16_f32 v98, v98, s0
	v_cvt_pk_bf16_f32 v152, v152, s0
	v_cvt_pk_bf16_f32 v153, v153, s0
	v_cvt_pk_bf16_f32 v129, v129, s0
	v_cvt_pk_bf16_f32 v154, v154, s0
	v_cvt_pk_bf16_f32 v155, v155, s0
	v_cvt_pk_bf16_f32 v156, v156, s0
	v_cvt_pk_bf16_f32 v157, v157, s0
	v_cvt_pk_bf16_f32 v158, v158, s0
	v_cvt_pk_bf16_f32 v159, v159, s0
	global_store_short v[144:145], v137, off
	global_store_short v[146:147], v152, off
	global_store_short v[150:151], v153, off
	global_store_short v[148:149], v129, off
	global_store_short v[144:145], v154, off offset:32
	global_store_short v[146:147], v155, off offset:32
	global_store_short v[150:151], v156, off offset:32
	global_store_short v[148:149], v157, off offset:32
	global_store_short v[144:145], v158, off offset:64
	global_store_short v[146:147], v159, off offset:64
	v_mul_f32_e32 v108, v108, v234
	v_mul_f32_e32 v109, v211, v109
	global_store_short v[144:145], v106, off offset:160
	v_cvt_pk_bf16_f32 v106, v107, s0
; template <bool I8, class Epi> ...
;     ...
; #pragma unroll
;   for (int i = 0; i < 4; ++i) {
;     const int row = m0 + wm * 64 + i * 16 + (lane >> 4) * 4;
;     float4 rs = float4{1.f, 1.f, 1.f, 1.f};
;     if (I8) rs = *reinterpret_cast<const float4*>(rscale + row);
; #pragma unroll
;     for (int j = 0; j < 8; ++j) {
;       const int col = n0 + wn * 128 + j * 16 + (lane & 15);
;       if (I8) {
;         typedef __attribute__((ext_vector_type(4))) int i32x4;
;         const i32x4 ia = __builtin_bit_cast(i32x4, acc[i][j]);
;         const float cs = cscale[col];
;         epi(row, col, f32x4{(float)ia[0] * rs.x * cs, (float)ia[1] * rs.y * cs, (float)ia[2] * rs.z * cs, (float)ia[3] * rs.w * cs});
;       } else {
;         epi(row, col, acc[i][j]);
;       }
;     }
;   }
;   __device__ __forceinline__ void operator()(int row, int col, f32x4 v) const {
; #pragma unroll
;     for (int r = 0; r < 4; ++r) C[(size_t)(row + r) * ldc + col] = f2bf(v[r]);
;   }
	v_mul_f32_e32 v100, v100, v238
	v_mul_f32_e32 v101, v211, v101
	global_store_short v[144:145], v98, off offset:224
	v_cvt_pk_bf16_f32 v98, v99, s0
	v_mul_f32_e32 v109, v109, v234
	global_store_short v[146:147], v106, off offset:160
	v_cvt_pk_bf16_f32 v106, v108, s0
	v_mul_f32_e32 v102, v208, v102
	v_mul_f32_e32 v101, v101, v238
	global_store_short v[146:147], v98, off offset:224
	v_cvt_pk_bf16_f32 v98, v100, s0
	global_store_short v[150:151], v106, off offset:160
	v_cvt_pk_bf16_f32 v106, v109, s0
	v_mul_f32_e32 v102, v102, v236
	v_mul_f32_e32 v103, v209, v103
	global_store_short v[150:151], v98, off offset:224
	v_cvt_pk_bf16_f32 v98, v101, s0
	v_mul_f32_e32 v95, v213, v95
	global_store_short v[148:149], v106, off offset:160
	v_mul_f32_e32 v103, v103, v236
	v_mul_f32_e32 v104, v210, v104
	v_cvt_pk_bf16_f32 v102, v102, s0
	global_store_short v[148:149], v98, off offset:224
	v_or_b32_e32 v98, 16, v136
	v_mul_f32_e32 v94, v212, v94
	v_mul_f32_e32 v106, v224, v95
	v_mul_f32_e32 v95, v214, v96
	v_mul_f32_e32 v104, v104, v236
	v_mul_f32_e32 v105, v211, v105
	global_store_short v[144:145], v102, off offset:192
	v_cvt_pk_bf16_f32 v102, v103, s0
	v_ashrrev_i32_e32 v99, 31, v98
	v_mul_f32_e32 v94, v224, v94
	v_mul_f32_e32 v107, v224, v95
	v_mul_f32_e32 v95, v215, v97
	v_mul_f32_e32 v105, v105, v236
	global_store_short v[146:147], v102, off offset:192
	v_cvt_pk_bf16_f32 v102, v104, s0
	v_or_b32_e32 v100, 17, v136
	v_mul_f32_e32 v108, v224, v95
	v_cvt_pk_bf16_f32 v96, v94, s0
	v_lshlrev_b64 v[94:95], 12, v[98:99]
	global_store_short v[150:151], v102, off offset:192
	v_cvt_pk_bf16_f32 v102, v105, s0
	v_ashrrev_i32_e32 v101, 31, v100
	v_lshl_add_u64 v[94:95], v[122:123], 0, v[94:95]
	global_store_short v[148:149], v102, off offset:192
	v_or_b32_e32 v102, 18, v136
	global_store_short v[94:95], v96, off
	v_lshlrev_b64 v[96:97], 12, v[100:101]
	v_mul_f32_e32 v82, v212, v82
	v_ashrrev_i32_e32 v103, 31, v102
	v_cvt_pk_bf16_f32 v98, v106, s0
	v_lshl_add_u64 v[96:97], v[122:123], 0, v[96:97]
	v_mul_f32_e32 v82, v230, v82
	v_mul_f32_e32 v83, v213, v83
	v_or_b32_e32 v104, 19, v136
	global_store_short v[96:97], v98, off
	v_lshlrev_b64 v[98:99], 12, v[102:103]
	v_mul_f32_e32 v83, v230, v83
	v_mul_f32_e32 v84, v214, v84
	v_cvt_pk_bf16_f32 v82, v82, s0
	v_ashrrev_i32_e32 v105, 31, v104
	v_cvt_pk_bf16_f32 v100, v107, s0
	v_lshl_add_u64 v[98:99], v[122:123], 0, v[98:99]
	v_mul_f32_e32 v84, v230, v84
	v_mul_f32_e32 v85, v215, v85
	global_store_short v[94:95], v82, off offset:96
	v_cvt_pk_bf16_f32 v82, v83, s0
	global_store_short v[98:99], v100, off
	v_lshlrev_b64 v[100:101], 12, v[104:105]
	v_mul_f32_e32 v85, v230, v85
	global_store_short v[96:97], v82, off offset:96
	v_cvt_pk_bf16_f32 v82, v84, s0
	v_lshl_add_u64 v[100:101], v[122:123], 0, v[100:101]
	global_store_short v[98:99], v82, off offset:96
	v_cvt_pk_bf16_f32 v82, v85, s0
	v_mul_f32_e32 v78, v212, v78
	global_store_short v[100:101], v82, off offset:96
	v_mul_f32_e32 v82, v232, v78
	v_cvt_f32_i32_e32 v78, v80
	v_cvt_f32_i32_e32 v80, v81
	v_mul_f32_e32 v79, v213, v79
	v_mul_f32_e32 v83, v232, v79
	v_mul_f32_e32 v78, v214, v78
	v_mul_f32_e32 v84, v232, v78
	v_mul_f32_e32 v78, v215, v80
	v_mul_f32_e32 v85, v232, v78
	v_mul_f32_e32 v66, v212, v66
	v_mul_f32_e32 v66, v238, v66
	v_mul_f32_e32 v67, v213, v67
	v_mul_f32_e32 v67, v238, v67
	v_mul_f32_e32 v68, v214, v68
	v_cvt_pk_bf16_f32 v66, v66, s0
	v_mul_f32_e32 v68, v238, v68
	v_mul_f32_e32 v69, v215, v69
	global_store_short v[94:95], v66, off offset:224
	v_cvt_pk_bf16_f32 v66, v67, s0
	v_mul_f32_e32 v69, v238, v69
	global_store_short v[96:97], v66, off offset:224
	v_cvt_pk_bf16_f32 v66, v68, s0
	global_store_short v[98:99], v66, off offset:224
	v_cvt_pk_bf16_f32 v66, v69, s0
	global_store_short v[100:101], v66, off offset:224
	v_mul_f32_e32 v70, v212, v70
	v_mul_f32_e32 v70, v236, v70
	v_mul_f32_e32 v71, v213, v71
	v_cvt_pk_bf16_f32 v82, v82, s0
	v_mul_f32_e32 v71, v236, v71
	v_mul_f32_e32 v72, v214, v72
	v_cvt_pk_bf16_f32 v70, v70, s0
	global_store_short v[94:95], v82, off offset:128
	v_cvt_pk_bf16_f32 v82, v83, s0
	v_mul_f32_e32 v72, v236, v72
	v_mul_f32_e32 v73, v215, v73
	global_store_short v[94:95], v70, off offset:192
	v_cvt_pk_bf16_f32 v70, v71, s0
	global_store_short v[96:97], v82, off offset:128
	v_cvt_pk_bf16_f32 v82, v84, s0
	v_mul_f32_e32 v74, v212, v74
	v_mul_f32_e32 v73, v236, v73
	global_store_short v[96:97], v70, off offset:192
	v_cvt_pk_bf16_f32 v70, v72, s0
	global_store_short v[98:99], v82, off offset:128
	v_cvt_pk_bf16_f32 v82, v85, s0
	v_mul_f32_e32 v74, v234, v74
	v_mul_f32_e32 v75, v213, v75
	global_store_short v[98:99], v70, off offset:192
	v_cvt_pk_bf16_f32 v70, v73, s0
	global_store_short v[100:101], v82, off offset:128
	v_mul_f32_e32 v75, v234, v75
	v_mul_f32_e32 v76, v214, v76
	v_cvt_pk_bf16_f32 v74, v74, s0
	global_store_short v[100:101], v70, off offset:192
	v_or_b32_e32 v70, 32, v136
	v_mul_f32_e32 v76, v234, v76
	v_mul_f32_e32 v77, v215, v77
	global_store_short v[94:95], v74, off offset:160
	v_cvt_pk_bf16_f32 v74, v75, s0
	v_ashrrev_i32_e32 v71, 31, v70
	v_mul_f32_e32 v77, v234, v77
	global_store_short v[96:97], v74, off offset:160
	v_cvt_pk_bf16_f32 v74, v76, s0
	v_or_b32_e32 v72, 33, v136
	global_store_short v[98:99], v74, off offset:160
	v_cvt_pk_bf16_f32 v74, v77, s0
	v_ashrrev_i32_e32 v73, 31, v72
	global_store_short v[100:101], v74, off offset:160
	v_or_b32_e32 v74, 34, v136
	v_ashrrev_i32_e32 v75, 31, v74
	v_cvt_f32_i32_e32 v39, v39
	v_cvt_f32_i32_e32 v31, v31
	v_or_b32_e32 v76, 35, v136
	v_cvt_f32_i32_e32 v40, v40
	v_cvt_f32_i32_e32 v30, v30
	v_cvt_f32_i32_e32 v32, v32
	v_ashrrev_i32_e32 v77, 31, v76
	v_cvt_f32_i32_e32 v41, v41
; template <bool I8, class Epi> ...
;     ...
; #pragma unroll
;   for (int i = 0; i < 4; ++i) {
;     const int row = m0 + wm * 64 + i * 16 + (lane >> 4) * 4;
;     float4 rs = float4{1.f, 1.f, 1.f, 1.f};
;     if (I8) rs = *reinterpret_cast<const float4*>(rscale + row);
; #pragma unroll
;     for (int j = 0; j < 8; ++j) {
;       const int col = n0 + wn * 128 + j * 16 + (lane & 15);
;       if (I8) {
;         typedef __attribute__((ext_vector_type(4))) int i32x4;
;         const i32x4 ia = __builtin_bit_cast(i32x4, acc[i][j]);
;         const float cs = cscale[col];
;         epi(row, col, f32x4{(float)ia[0] * rs.x * cs, (float)ia[1] * rs.y * cs, (float)ia[2] * rs.z * cs, (float)ia[3] * rs.w * cs});
;       } else {
;         epi(row, col, acc[i][j]);
;       }
;     }
;   }
;   __device__ __forceinline__ void operator()(int row, int col, f32x4 v) const {
; #pragma unroll
;     for (int r = 0; r < 4; ++r) C[(size_t)(row + r) * ldc + col] = f2bf(v[r]);
;   }
	v_cvt_f32_i32_e32 v33, v33
	v_cvt_f32_i32_e32 v2, v2
	v_cvt_f32_i32_e32 v3, v3
	v_cvt_f32_i32_e32 v4, v4
	v_cvt_f32_i32_e32 v5, v5
	v_cvt_f32_i32_e32 v114, v114
	v_cvt_f32_i32_e32 v110, v110
	v_cvt_f32_i32_e32 v90, v90
	v_mul_f32_e32 v63, v217, v63
	v_mul_f32_e32 v62, v216, v62
	v_mul_f32_e32 v82, v224, v63
	v_mul_f32_e32 v63, v218, v64
	v_mul_f32_e32 v62, v224, v62
	v_mul_f32_e32 v83, v224, v63
	v_mul_f32_e32 v63, v219, v65
	v_mul_f32_e32 v84, v224, v63
	v_cvt_pk_bf16_f32 v64, v62, s0
	v_lshlrev_b64 v[62:63], 12, v[70:71]
	v_lshl_add_u64 v[62:63], v[122:123], 0, v[62:63]
	global_store_short v[62:63], v64, off
	v_lshlrev_b64 v[64:65], 12, v[72:73]
	v_mul_f32_e32 v42, v216, v42
	v_mul_f32_e32 v34, v216, v34
	v_cvt_pk_bf16_f32 v70, v82, s0
	v_lshl_add_u64 v[64:65], v[122:123], 0, v[64:65]
	v_mul_f32_e32 v42, v234, v42
	v_mul_f32_e32 v43, v217, v43
	v_mul_f32_e32 v34, v238, v34
	v_mul_f32_e32 v35, v217, v35
	global_store_short v[64:65], v70, off
	v_lshlrev_b64 v[70:71], 12, v[74:75]
	v_mul_f32_e32 v43, v234, v43
	v_mul_f32_e32 v44, v218, v44
	v_cvt_pk_bf16_f32 v42, v42, s0
	v_mul_f32_e32 v35, v238, v35
	v_mul_f32_e32 v36, v218, v36
	v_cvt_pk_bf16_f32 v34, v34, s0
	v_cvt_pk_bf16_f32 v72, v83, s0
	v_lshl_add_u64 v[70:71], v[122:123], 0, v[70:71]
	v_mul_f32_e32 v44, v234, v44
	v_mul_f32_e32 v45, v219, v45
	global_store_short v[62:63], v42, off offset:160
	v_cvt_pk_bf16_f32 v42, v43, s0
	v_mul_f32_e32 v36, v238, v36
	v_mul_f32_e32 v37, v219, v37
	global_store_short v[62:63], v34, off offset:224
	v_cvt_pk_bf16_f32 v34, v35, s0
	global_store_short v[70:71], v72, off
	v_lshlrev_b64 v[72:73], 12, v[76:77]
	v_mul_f32_e32 v45, v234, v45
	global_store_short v[64:65], v42, off offset:160
	v_cvt_pk_bf16_f32 v42, v44, s0
	v_mul_f32_e32 v38, v216, v38
	v_mul_f32_e32 v37, v238, v37
	global_store_short v[64:65], v34, off offset:224
	v_cvt_pk_bf16_f32 v34, v36, s0
	v_lshl_add_u64 v[72:73], v[122:123], 0, v[72:73]
	global_store_short v[70:71], v42, off offset:160
	v_cvt_pk_bf16_f32 v42, v45, s0
	v_mul_f32_e32 v38, v236, v38
	v_mul_f32_e32 v39, v217, v39
	global_store_short v[70:71], v34, off offset:224
	v_cvt_pk_bf16_f32 v34, v37, s0
	v_mul_f32_e32 v31, v221, v31
	global_store_short v[72:73], v42, off offset:160
	v_mul_f32_e32 v39, v236, v39
	v_mul_f32_e32 v40, v218, v40
	v_cvt_pk_bf16_f32 v38, v38, s0
	global_store_short v[72:73], v34, off offset:224
	v_or_b32_e32 v34, 48, v136
	v_mul_f32_e32 v30, v220, v30
	v_mul_f32_e32 v42, v224, v31
	v_mul_f32_e32 v31, v222, v32
	v_mul_f32_e32 v40, v236, v40
	v_mul_f32_e32 v41, v219, v41
	global_store_short v[62:63], v38, off offset:192
	v_cvt_pk_bf16_f32 v38, v39, s0
	v_ashrrev_i32_e32 v35, 31, v34
	v_mul_f32_e32 v30, v224, v30
	v_mul_f32_e32 v43, v224, v31
	v_mul_f32_e32 v31, v223, v33
	v_mul_f32_e32 v41, v236, v41
	global_store_short v[64:65], v38, off offset:192
	v_cvt_pk_bf16_f32 v38, v40, s0
	v_or_b32_e32 v36, 49, v136
	v_mul_f32_e32 v44, v224, v31
	v_cvt_pk_bf16_f32 v32, v30, s0
	v_lshlrev_b64 v[30:31], 12, v[34:35]
	global_store_short v[70:71], v38, off offset:192
	v_cvt_pk_bf16_f32 v38, v41, s0
	v_ashrrev_i32_e32 v37, 31, v36
	v_lshl_add_u64 v[30:31], v[122:123], 0, v[30:31]
	global_store_short v[72:73], v38, off offset:192
	v_or_b32_e32 v38, 50, v136
	global_store_short v[30:31], v32, off
	v_lshlrev_b64 v[32:33], 12, v[36:37]
	v_mul_f32_e32 v2, v220, v2
	v_ashrrev_i32_e32 v39, 31, v38
	v_cvt_pk_bf16_f32 v34, v42, s0
	v_lshl_add_u64 v[32:33], v[122:123], 0, v[32:33]
	v_mul_f32_e32 v2, v236, v2
	v_mul_f32_e32 v3, v221, v3
	v_or_b32_e32 v40, 51, v136
	global_store_short v[32:33], v34, off
	v_lshlrev_b64 v[34:35], 12, v[38:39]
	v_mul_f32_e32 v3, v236, v3
	v_mul_f32_e32 v4, v222, v4
	v_cvt_pk_bf16_f32 v2, v2, s0
	v_ashrrev_i32_e32 v41, 31, v40
	v_cvt_pk_bf16_f32 v36, v43, s0
	v_lshl_add_u64 v[34:35], v[122:123], 0, v[34:35]
	v_mul_f32_e32 v4, v236, v4
	v_mul_f32_e32 v5, v223, v5
	global_store_short v[30:31], v2, off offset:192
	v_cvt_pk_bf16_f32 v2, v3, s0
	global_store_short v[34:35], v36, off
	v_lshlrev_b64 v[36:37], 12, v[40:41]
	v_mul_f32_e32 v5, v236, v5
	global_store_short v[32:33], v2, off offset:192
	v_cvt_pk_bf16_f32 v2, v4, s0
	v_cvt_f32_i32_e32 v86, v86
	v_cvt_f32_i32_e32 v58, v58
	v_cvt_f32_i32_e32 v54, v54
	v_cvt_f32_i32_e32 v50, v50
	v_cvt_f32_i32_e32 v46, v46
	v_cvt_f32_i32_e32 v26, v26
	v_lshl_add_u64 v[36:37], v[122:123], 0, v[36:37]
	v_cvt_f32_i32_e32 v22, v22
	v_cvt_f32_i32_e32 v18, v18
	v_cvt_f32_i32_e32 v10, v10
	v_cvt_f32_i32_e32 v6, v6
	global_store_short v[34:35], v2, off offset:192
	v_cvt_f32_i32_e32 v2, v14
	v_cvt_pk_bf16_f32 v3, v5, s0
	v_cvt_f32_i32_e32 v115, v115
	v_cvt_f32_i32_e32 v111, v111
	v_cvt_f32_i32_e32 v91, v91
	v_cvt_f32_i32_e32 v87, v87
	v_cvt_f32_i32_e32 v59, v59
	v_cvt_f32_i32_e32 v55, v55
	v_cvt_f32_i32_e32 v51, v51
	v_cvt_f32_i32_e32 v47, v47
	v_cvt_f32_i32_e32 v27, v27
	v_cvt_f32_i32_e32 v23, v23
	v_cvt_f32_i32_e32 v19, v19
	v_cvt_f32_i32_e32 v11, v11
	v_cvt_f32_i32_e32 v7, v7
	global_store_short v[36:37], v3, off offset:192
	v_cvt_f32_i32_e32 v3, v15
	v_cvt_f32_i32_e32 v116, v116
	v_cvt_f32_i32_e32 v112, v112
	v_cvt_f32_i32_e32 v92, v92
	v_cvt_f32_i32_e32 v88, v88
	v_cvt_f32_i32_e32 v60, v60
	v_cvt_f32_i32_e32 v56, v56
	v_cvt_f32_i32_e32 v52, v52
	v_cvt_f32_i32_e32 v48, v48
	v_cvt_f32_i32_e32 v28, v28
	v_cvt_f32_i32_e32 v24, v24
	v_cvt_f32_i32_e32 v20, v20
	v_cvt_f32_i32_e32 v12, v12
	v_cvt_f32_i32_e32 v8, v8
	v_cvt_f32_i32_e32 v4, v16
	v_cvt_f32_i32_e32 v117, v117
	v_cvt_f32_i32_e32 v113, v113
	v_cvt_f32_i32_e32 v93, v93
	v_cvt_f32_i32_e32 v89, v89
	v_cvt_f32_i32_e32 v61, v61
	v_cvt_f32_i32_e32 v57, v57
	v_cvt_f32_i32_e32 v53, v53
	v_cvt_f32_i32_e32 v49, v49
; template <bool I8, class Epi> ...
;     ...
; #pragma unroll
;   for (int i = 0; i < 4; ++i) {
;     const int row = m0 + wm * 64 + i * 16 + (lane >> 4) * 4;
;     float4 rs = float4{1.f, 1.f, 1.f, 1.f};
;     if (I8) rs = *reinterpret_cast<const float4*>(rscale + row);
; #pragma unroll
;     for (int j = 0; j < 8; ++j) {
;       const int col = n0 + wn * 128 + j * 16 + (lane & 15);
;       if (I8) {
;         typedef __attribute__((ext_vector_type(4))) int i32x4;
;         const i32x4 ia = __builtin_bit_cast(i32x4, acc[i][j]);
;         const float cs = cscale[col];
;         epi(row, col, f32x4{(float)ia[0] * rs.x * cs, (float)ia[1] * rs.y * cs, (float)ia[2] * rs.z * cs, (float)ia[3] * rs.w * cs});
;       } else {
;         epi(row, col, acc[i][j]);
;       }
;     }
;   }
;   __device__ __forceinline__ void operator()(int row, int col, f32x4 v) const {
; #pragma unroll
;     for (int r = 0; r < 4; ++r) C[(size_t)(row + r) * ldc + col] = f2bf(v[r]);
;   }
	v_cvt_f32_i32_e32 v29, v29
	v_cvt_f32_i32_e32 v25, v25
	v_cvt_f32_i32_e32 v21, v21
	v_cvt_f32_i32_e32 v13, v13
	v_cvt_f32_i32_e32 v9, v9
	v_cvt_f32_i32_e32 v5, v17
	v_mul_f32_e32 v114, v208, v114
	v_mul_f32_e32 v110, v208, v110
	v_mul_f32_e32 v90, v212, v90
	v_mul_f32_e32 v86, v212, v86
	v_mul_f32_e32 v58, v216, v58
	v_mul_f32_e32 v54, v216, v54
	v_mul_f32_e32 v50, v216, v50
	v_mul_f32_e32 v46, v216, v46
	v_mul_f32_e32 v26, v220, v26
	v_mul_f32_e32 v22, v220, v22
	v_mul_f32_e32 v18, v220, v18
	v_mul_f32_e32 v10, v220, v10
	v_mul_f32_e32 v6, v220, v6
	v_mul_f32_e32 v2, v220, v2
	v_mul_f32_e32 v114, v114, v230
	v_mul_f32_e32 v115, v209, v115
	v_mul_f32_e32 v110, v110, v232
	v_mul_f32_e32 v111, v209, v111
	v_mul_f32_e32 v90, v226, v90
	v_mul_f32_e32 v91, v213, v91
	v_mul_f32_e32 v86, v228, v86
	v_mul_f32_e32 v87, v213, v87
	v_mul_f32_e32 v58, v226, v58
	v_mul_f32_e32 v59, v217, v59
	v_mul_f32_e32 v54, v228, v54
	v_mul_f32_e32 v55, v217, v55
	v_mul_f32_e32 v50, v230, v50
	v_mul_f32_e32 v51, v217, v51
	v_mul_f32_e32 v46, v232, v46
	v_mul_f32_e32 v47, v217, v47
	v_mul_f32_e32 v26, v226, v26
	v_mul_f32_e32 v27, v221, v27
	v_mul_f32_e32 v22, v228, v22
	v_mul_f32_e32 v23, v221, v23
	v_mul_f32_e32 v18, v230, v18
	v_mul_f32_e32 v19, v221, v19
	v_mul_f32_e32 v10, v232, v10
	v_mul_f32_e32 v11, v221, v11
	v_mul_f32_e32 v6, v234, v6
	v_mul_f32_e32 v7, v221, v7
	v_mul_f32_e32 v2, v238, v2
	v_mul_f32_e32 v3, v221, v3
	v_mul_f32_e32 v160, v210, v161
	v_mul_f32_e32 v115, v115, v230
	v_mul_f32_e32 v116, v210, v116
	v_cvt_pk_bf16_f32 v114, v114, s0
	v_mul_f32_e32 v111, v111, v232
	v_mul_f32_e32 v112, v210, v112
	v_cvt_pk_bf16_f32 v110, v110, s0
	v_mul_f32_e32 v91, v226, v91
	v_mul_f32_e32 v92, v214, v92
	v_cvt_pk_bf16_f32 v90, v90, s0
	v_mul_f32_e32 v87, v228, v87
	v_mul_f32_e32 v88, v214, v88
	v_cvt_pk_bf16_f32 v86, v86, s0
	v_mul_f32_e32 v59, v226, v59
	v_mul_f32_e32 v60, v218, v60
	v_cvt_pk_bf16_f32 v58, v58, s0
	v_mul_f32_e32 v55, v228, v55
	v_mul_f32_e32 v56, v218, v56
	v_cvt_pk_bf16_f32 v54, v54, s0
	v_mul_f32_e32 v51, v230, v51
	v_mul_f32_e32 v52, v218, v52
	v_cvt_pk_bf16_f32 v50, v50, s0
	v_mul_f32_e32 v47, v232, v47
	v_mul_f32_e32 v48, v218, v48
	v_cvt_pk_bf16_f32 v46, v46, s0
	v_mul_f32_e32 v27, v226, v27
	v_mul_f32_e32 v28, v222, v28
	v_cvt_pk_bf16_f32 v26, v26, s0
	v_mul_f32_e32 v23, v228, v23
	v_mul_f32_e32 v24, v222, v24
	v_cvt_pk_bf16_f32 v22, v22, s0
	v_mul_f32_e32 v19, v230, v19
	v_mul_f32_e32 v20, v222, v20
	v_cvt_pk_bf16_f32 v18, v18, s0
	v_mul_f32_e32 v11, v232, v11
	v_mul_f32_e32 v12, v222, v12
	v_cvt_pk_bf16_f32 v10, v10, s0
	v_mul_f32_e32 v7, v234, v7
	v_mul_f32_e32 v8, v222, v8
	v_cvt_pk_bf16_f32 v6, v6, s0
	v_mul_f32_e32 v3, v238, v3
	v_mul_f32_e32 v4, v222, v4
	v_cvt_pk_bf16_f32 v2, v2, s0
	v_mul_f32_e32 v161, v211, v162
	v_mul_f32_e32 v160, v160, v228
	v_mul_f32_e32 v116, v116, v230
	v_mul_f32_e32 v117, v211, v117
	global_store_short v[144:145], v114, off offset:96
	v_cvt_pk_bf16_f32 v114, v115, s0
	v_mul_f32_e32 v112, v112, v232
	v_mul_f32_e32 v113, v211, v113
	global_store_short v[144:145], v110, off offset:128
	v_cvt_pk_bf16_f32 v110, v111, s0
	v_mul_f32_e32 v92, v226, v92
	v_mul_f32_e32 v93, v215, v93
	global_store_short v[94:95], v90, off offset:32
	v_cvt_pk_bf16_f32 v90, v91, s0
	v_mul_f32_e32 v88, v228, v88
	v_mul_f32_e32 v89, v215, v89
	global_store_short v[94:95], v86, off offset:64
	v_cvt_pk_bf16_f32 v86, v87, s0
	v_mul_f32_e32 v60, v226, v60
	v_mul_f32_e32 v61, v219, v61
	global_store_short v[62:63], v58, off offset:32
	v_cvt_pk_bf16_f32 v58, v59, s0
	v_mul_f32_e32 v56, v228, v56
	v_mul_f32_e32 v57, v219, v57
	global_store_short v[62:63], v54, off offset:64
	v_cvt_pk_bf16_f32 v54, v55, s0
	v_mul_f32_e32 v52, v230, v52
	v_mul_f32_e32 v53, v219, v53
	global_store_short v[62:63], v50, off offset:96
	v_cvt_pk_bf16_f32 v50, v51, s0
	v_mul_f32_e32 v48, v232, v48
	v_mul_f32_e32 v49, v219, v49
	global_store_short v[62:63], v46, off offset:128
	v_cvt_pk_bf16_f32 v46, v47, s0
	v_mul_f32_e32 v28, v226, v28
	v_mul_f32_e32 v29, v223, v29
	global_store_short v[30:31], v26, off offset:32
	v_cvt_pk_bf16_f32 v26, v27, s0
	v_mul_f32_e32 v24, v228, v24
	v_mul_f32_e32 v25, v223, v25
	global_store_short v[30:31], v22, off offset:64
	v_cvt_pk_bf16_f32 v22, v23, s0
	v_mul_f32_e32 v20, v230, v20
	v_mul_f32_e32 v21, v223, v21
	global_store_short v[30:31], v18, off offset:96
; template <bool I8, class Epi> ...
;     ...
; #pragma unroll
;   for (int i = 0; i < 4; ++i) {
;     const int row = m0 + wm * 64 + i * 16 + (lane >> 4) * 4;
;     float4 rs = float4{1.f, 1.f, 1.f, 1.f};
;     if (I8) rs = *reinterpret_cast<const float4*>(rscale + row);
; #pragma unroll
;     for (int j = 0; j < 8; ++j) {
;       const int col = n0 + wn * 128 + j * 16 + (lane & 15);
;       if (I8) {
;         typedef __attribute__((ext_vector_type(4))) int i32x4;
;         const i32x4 ia = __builtin_bit_cast(i32x4, acc[i][j]);
;         const float cs = cscale[col];
;         epi(row, col, f32x4{(float)ia[0] * rs.x * cs, (float)ia[1] * rs.y * cs, (float)ia[2] * rs.z * cs, (float)ia[3] * rs.w * cs});
;       } else {
;         epi(row, col, acc[i][j]);
;       }
;     }
;   }
;   __device__ __forceinline__ void operator()(int row, int col, f32x4 v) const {
; #pragma unroll
;     for (int r = 0; r < 4; ++r) C[(size_t)(row + r) * ldc + col] = f2bf(v[r]);
;   }
; __device__ void phase_outproj(KParams& p, int bid, int nb, char* smem) {
;     ...
;   for (int it = start; it < end; it += step) {
;     const int x = aware ? (bid & 7) : (it >> 6), s_ = aware ? it : (it & 63);
;     EpiBf16 epi{reinterpret_cast<bf16_t*>(p.y_x), D};
;     gemm_tile_n256<true>(a8, D / 2, b8, D / 2, D / 2, (8 * x + (s_ & 7)) * 128, (s_ >> 3) * 256, epi, smem, p.yscale, p.woscale);
;   }
	v_cvt_pk_bf16_f32 v18, v19, s0
	v_mul_f32_e32 v12, v232, v12
	v_mul_f32_e32 v13, v223, v13
	global_store_short v[30:31], v10, off offset:128
	v_cvt_pk_bf16_f32 v10, v11, s0
	v_mul_f32_e32 v8, v234, v8
	v_mul_f32_e32 v9, v223, v9
	global_store_short v[30:31], v6, off offset:160
	v_cvt_pk_bf16_f32 v6, v7, s0
	v_mul_f32_e32 v4, v238, v4
	v_mul_f32_e32 v5, v223, v5
	global_store_short v[30:31], v2, off offset:224
	v_cvt_pk_bf16_f32 v2, v3, s0
	v_mul_f32_e32 v161, v161, v228
	v_cvt_pk_bf16_f32 v129, v160, s0
	v_mul_f32_e32 v117, v117, v230
	global_store_short v[146:147], v114, off offset:96
	v_cvt_pk_bf16_f32 v114, v116, s0
	v_mul_f32_e32 v113, v113, v232
	global_store_short v[146:147], v110, off offset:128
	v_cvt_pk_bf16_f32 v110, v112, s0
	v_mul_f32_e32 v93, v226, v93
	global_store_short v[96:97], v90, off offset:32
	v_cvt_pk_bf16_f32 v90, v92, s0
	v_mul_f32_e32 v89, v228, v89
	global_store_short v[96:97], v86, off offset:64
	v_cvt_pk_bf16_f32 v86, v88, s0
	v_mul_f32_e32 v61, v226, v61
	global_store_short v[64:65], v58, off offset:32
	v_cvt_pk_bf16_f32 v58, v60, s0
	v_mul_f32_e32 v57, v228, v57
	global_store_short v[64:65], v54, off offset:64
	v_cvt_pk_bf16_f32 v54, v56, s0
	v_mul_f32_e32 v53, v230, v53
	global_store_short v[64:65], v50, off offset:96
	v_cvt_pk_bf16_f32 v50, v52, s0
	v_mul_f32_e32 v49, v232, v49
	global_store_short v[64:65], v46, off offset:128
	v_cvt_pk_bf16_f32 v46, v48, s0
	v_mul_f32_e32 v29, v226, v29
	global_store_short v[32:33], v26, off offset:32
	v_cvt_pk_bf16_f32 v26, v28, s0
	v_mul_f32_e32 v25, v228, v25
	global_store_short v[32:33], v22, off offset:64
	v_cvt_pk_bf16_f32 v22, v24, s0
	v_mul_f32_e32 v21, v230, v21
	global_store_short v[32:33], v18, off offset:96
	v_cvt_pk_bf16_f32 v18, v20, s0
	v_mul_f32_e32 v13, v232, v13
	global_store_short v[32:33], v10, off offset:128
	v_cvt_pk_bf16_f32 v10, v12, s0
	v_mul_f32_e32 v9, v234, v9
	global_store_short v[32:33], v6, off offset:160
	v_cvt_pk_bf16_f32 v6, v8, s0
	v_mul_f32_e32 v5, v238, v5
	global_store_short v[32:33], v2, off offset:224
	v_cvt_pk_bf16_f32 v2, v4, s0
	s_add_i32 s3, s3, s35
	global_store_short v[150:151], v129, off offset:64
	v_cvt_pk_bf16_f32 v129, v161, s0
	global_store_short v[150:151], v114, off offset:96
	v_cvt_pk_bf16_f32 v114, v117, s0
	global_store_short v[150:151], v110, off offset:128
	v_cvt_pk_bf16_f32 v110, v113, s0
	v_cvt_pk_bf16_f32 v102, v108, s0
	global_store_short v[98:99], v90, off offset:32
	v_cvt_pk_bf16_f32 v90, v93, s0
	global_store_short v[98:99], v86, off offset:64
	v_cvt_pk_bf16_f32 v86, v89, s0
	v_cvt_pk_bf16_f32 v74, v84, s0
	global_store_short v[70:71], v58, off offset:32
	v_cvt_pk_bf16_f32 v58, v61, s0
	global_store_short v[70:71], v54, off offset:64
	v_cvt_pk_bf16_f32 v54, v57, s0
	global_store_short v[70:71], v50, off offset:96
	v_cvt_pk_bf16_f32 v50, v53, s0
	global_store_short v[70:71], v46, off offset:128
	v_cvt_pk_bf16_f32 v46, v49, s0
	v_cvt_pk_bf16_f32 v38, v44, s0
	global_store_short v[34:35], v26, off offset:32
	v_cvt_pk_bf16_f32 v26, v29, s0
	global_store_short v[34:35], v22, off offset:64
	v_cvt_pk_bf16_f32 v22, v25, s0
	global_store_short v[34:35], v18, off offset:96
	v_cvt_pk_bf16_f32 v18, v21, s0
	global_store_short v[34:35], v10, off offset:128
	v_cvt_pk_bf16_f32 v10, v13, s0
	global_store_short v[34:35], v6, off offset:160
	v_cvt_pk_bf16_f32 v6, v9, s0
	global_store_short v[34:35], v2, off offset:224
	v_cvt_pk_bf16_f32 v2, v5, s0
	s_cmp_lt_i32 s3, s42
	global_store_short v[148:149], v129, off offset:64
	global_store_short v[148:149], v114, off offset:96
	global_store_short v[148:149], v110, off offset:128
	global_store_short v[100:101], v102, off
	global_store_short v[100:101], v90, off offset:32
	global_store_short v[100:101], v86, off offset:64
	global_store_short v[72:73], v74, off
	global_store_short v[72:73], v58, off offset:32
	global_store_short v[72:73], v54, off offset:64
	global_store_short v[72:73], v50, off offset:96
	global_store_short v[72:73], v46, off offset:128
	global_store_short v[36:37], v38, off
	global_store_short v[36:37], v26, off offset:32
	global_store_short v[36:37], v22, off offset:64
	global_store_short v[36:37], v18, off offset:96
	global_store_short v[36:37], v10, off offset:128
	global_store_short v[36:37], v6, off offset:160
	global_store_short v[36:37], v2, off offset:224
	s_cbranch_scc1 .LBB0_1069
